# LN1+router phase: layernorm gamma/beta preloaded once per pass (no per-chunk load+drain), global instead of flat stores, router LDS prefetch
# speedup vs baseline: 1.0180x; 1.0082x over previous
; #define LAS __attribute__((address_space(3)))
; #define AIN(k) ldptr(lds, (k))
; __global__ void __launch_bounds__(NTHREADS, 2) hybrid_fwd(Args a) {
;     ...
;             LAS float* rwT = (LAS float*)lds;
;             LAS int* hist = (LAS int*)(lds + META_OFF);
;             LAS int* ent = (LAS int*)(lds + 131328);
;             {
;                 const unsigned char* img = ws + WS_RWT;
; #pragma unroll
;                 for (int i = 0; i < 16; ++i) __builtin_amdgcn_global_load_lds((const unsigned*)(img + (size_t)(i * 8 + wave) * 1024 + lane * 16), (LAS unsigned*)(lds + (i * 8 + wave) * 1024), 16, 0, 0);
;                 if (wave == 0) __builtin_amdgcn_global_load_lds((const unsigned*)(img + (size_t)128 * 1024 + lane * 16), (LAS unsigned*)(lds + 128 * 1024), 16, 0, 0);
;             }
;             float rb[16]; const float* rtb = AIN(I_RTB);
; #pragma unroll
;             for (int e = 0; e < 16; ++e) rb[e] = rtb[e];
;             const bf16_t* YB = (const bf16_t*)(ws + WS_YBUF); bf16_t* X1B = (bf16_t*)(ws + WS_X1B);
;             int* tokE = (int*)(ws + WS_TOKE); int* tokP = (int*)(ws + WS_TOKS); int* lst = (int*)(ws + WS_LIST); float* lstW = (float*)(ws + WS_LISTW); unsigned char* X1F = ws + WS_XG;
;             unsigned* fill = (unsigned*)(ws + WS_CTL) + CW_FILL + 64 * l;
;             const float* lg = AIN(I_LN1G) + l * DM; const float* lb = AIN(I_LN1B) + l * DM;
;             for (int v = bid; v < 256; v += G) {
.LBB0_884:
	s_mov_b32 s0, 0x20730
	s_add_i32 s0, s4, s0
	v_mov_b32_e32 v0, s0
	ds_read_b64 v[0:1], v0
	s_mov_b32 s5, 0x20720
	s_waitcnt lgkmcnt(0)
	v_readfirstlane_b32 s1, v1
	v_readfirstlane_b32 s0, v0
	s_nop 4
	global_load_dwordx4 v[0:3], v193, s[0:1] offset:48
	global_load_dwordx4 v[4:7], v193, s[0:1] offset:32
	global_load_dwordx4 v[8:11], v193, s[0:1] offset:16
	global_load_dwordx4 v[12:15], v193, s[0:1]
	s_mov_b32 s0, 0x20718
	s_add_i32 s0, s4, s0
	v_mov_b32_e32 v19, s0
	ds_read_b64 v[20:21], v19
	s_add_i32 s5, s4, s5
	v_mov_b32_e32 v19, s5
	s_cmpk_gt_i32 s48, 0xff
	s_waitcnt lgkmcnt(0)
	v_readfirstlane_b32 s0, v21
	v_readfirstlane_b32 s1, v20
	ds_read_b64 v[20:21], v19
	s_waitcnt lgkmcnt(0)
	v_readfirstlane_b32 s5, v21
	v_readfirstlane_b32 s6, v20
	s_cbranch_scc1 .LBB0_933
	s_lshl_b32 s92, s66, 11
	s_add_u32 s24, s2, 0x210000
	s_addc_u32 s25, s3, 0
	s_add_u32 s26, s2, 0x230000
	s_addc_u32 s27, s3, 0
	s_add_u32 s28, s2, 0x500000
	s_addc_u32 s29, s3, 0
	s_add_u32 s30, s2, 0x600000
	s_addc_u32 s31, s3, 0
	s_lshl_b64 s[8:9], s[92:93], 2
	s_add_u32 s34, s1, s8
	s_addc_u32 s35, s0, s9
	s_add_u32 s36, s6, s8
	s_addc_u32 s37, s5, s9
	s_lshl_b32 s92, s66, 6
	s_add_i32 s23, s4, 0x20400
	s_add_i32 s49, s4, 0x20100
	s_lshl_b64 s[0:1], s[92:93], 2
	s_add_u32 s6, s2, s0
	v_lshlrev_b32_e32 v20, 3, v17
	v_mov_b32_e32 v21, v193
	s_addc_u32 s7, s3, s1
	v_lshlrev_b32_e32 v24, 2, v17
	v_mov_b32_e32 v25, v193
	v_lshl_add_u64 v[20:21], s[2:3], 0, v[20:21]
	s_mov_b64 s[0:1], 0x52000000
	s_mov_b64 s[8:9], 0x42000000
	v_lshl_add_u64 v[26:27], v[20:21], 0, s[0:1]
	v_lshl_add_u64 v[28:29], v[20:21], 0, s[8:9]
	v_lshl_add_u64 v[20:21], s[2:3], 0, v[24:25]
	s_mov_b64 s[2:3], 0x56000000
	v_lshl_add_u64 v[30:31], v[20:21], 0, s[2:3]
	v_cmp_eq_u32_e64 s[2:3], 0, v17
	v_ashrrev_i32_e32 v17, 31, v16
	v_add_u32_e32 v25, s4, v192
	v_lshl_add_u64 v[20:21], v[16:17], 2, s[6:7]
	s_mov_b64 s[4:5], 0x8000
	v_ashrrev_i32_e32 v157, 1, v16
	v_and_b32_e32 v17, 1, v18
	v_mov_b32_e32 v18, s49
	v_cmp_gt_i32_e64 s[0:1], 16, v16
	v_lshl_add_u32 v156, v16, 2, s23
	v_lshl_add_u64 v[32:33], v[20:21], 0, s[4:5]
	v_cmp_gt_i32_e64 s[4:5], 64, v16
	v_mad_u64_u32 v[18:19], s[6:7], v157, 24, v[18:19]
	v_and_b32_e32 v16, -2, v16
	v_mul_u32_u24_e32 v19, 12, v17
	v_lshl_add_u32 v16, s48, 6, v16
	v_add_u32_e32 v158, 0x10080, v25
	v_add_u32_e32 v159, 0x12090, v25
	v_add_u32_e32 v160, 0x140a0, v25
	v_add_u32_e32 v161, 0x160b0, v25
	v_add_u32_e32 v162, 0x180c0, v25
	v_add_u32_e32 v163, 0x1a0d0, v25
	v_add_u32_e32 v164, 0x1c0e0, v25
	v_add_u32_e32 v165, 0x1e0f0, v25
	v_add_u32_e32 v166, 0x10480, v25
	v_add_u32_e32 v167, 0x12490, v25
	v_add_u32_e32 v168, 0x144a0, v25
	v_add_u32_e32 v169, 0x164b0, v25
	v_add_u32_e32 v170, 0x184c0, v25
	v_add_u32_e32 v171, 0x1a4d0, v25
	v_add_u32_e32 v172, 0x1c4e0, v25
	v_add_u32_e32 v173, 0x1e4f0, v25
	v_add_u32_e32 v174, 0x10880, v25
	v_add_u32_e32 v175, 0x12890, v25
	v_add_u32_e32 v176, 0x148a0, v25
	v_add_u32_e32 v177, 0x168b0, v25
	v_add_u32_e32 v178, 0x188c0, v25
	v_add_u32_e32 v179, 0x1a8d0, v25
	v_add_u32_e32 v180, 0x1c8e0, v25
	v_add_u32_e32 v181, 0x1e8f0, v25
	v_add_u32_e32 v182, 0x10c80, v25
	v_add_u32_e32 v183, 0x12c90, v25
	v_add_u32_e32 v184, 0x14ca0, v25
	v_add_u32_e32 v185, 0x16cb0, v25
	v_add_u32_e32 v186, 0x18cc0, v25
	v_add_u32_e32 v187, 0x1acd0, v25
	v_add_u32_e32 v188, 0x1cce0, v25
	v_add_u32_e32 v189, 0x1ecf0, v25
	v_add_u32_e32 v190, 0x11080, v25
	v_add_u32_e32 v191, 0x13090, v25
	v_add_u32_e32 v198, 0x150a0, v25
	v_add_u32_e32 v199, 0x170b0, v25
	v_add_u32_e32 v200, 0x190c0, v25
	v_add_u32_e32 v201, 0x1b0d0, v25
	v_add_u32_e32 v202, 0x1d0e0, v25
	v_add_u32_e32 v203, 0x1f0f0, v25
	v_add_u32_e32 v204, 0x11480, v25
	v_add_u32_e32 v205, 0x13490, v25
	v_add_u32_e32 v215, 0x154a0, v25
	v_add_u32_e32 v216, 0x174b0, v25
	v_add_u32_e32 v217, 0x194c0, v25
	v_add_u32_e32 v218, 0x1b4d0, v25
	v_add_u32_e32 v219, 0x1d4e0, v25
	v_add_u32_e32 v220, 0x1f4f0, v25
	v_add_u32_e32 v221, 0x11880, v25
	v_add_u32_e32 v222, 0x13890, v25
	v_add_u32_e32 v223, 0x158a0, v25
	v_add_u32_e32 v224, 0x178b0, v25
	v_add_u32_e32 v225, 0x198c0, v25
	v_add_u32_e32 v226, 0x1b8d0, v25
	v_add_u32_e32 v227, 0x1d8e0, v25
	v_add_u32_e32 v228, 0x1f8f0, v25
	v_add_u32_e32 v229, 0x11c80, v25
	v_add_u32_e32 v230, 0x13c90, v25
	v_add_u32_e32 v231, 0x15ca0, v25
	v_add_u32_e32 v232, 0x17cb0, v25
	v_add_u32_e32 v233, 0x19cc0, v25
	v_add_u32_e32 v234, 0x1bcd0, v25
	v_add_u32_e32 v235, 0x1dce0, v25
	v_add_u32_e32 v236, 0x1fcf0, v25
	v_mbcnt_lo_u32_b32 v242, -1, 0
	v_mbcnt_hi_u32_b32 v242, -1, v242
	v_lshlrev_b32_e32 v242, 4, v242
	v_mov_b32_e32 v243, 0
	v_lshl_add_u64 v[244:245], s[34:35], 0, v[242:243]
	global_load_dwordx4 v[158:161], v[244:245], off
	global_load_dwordx4 v[162:165], v[244:245], off offset:1024
	global_load_dwordx4 v[166:169], v[244:245], off offset:2048
	global_load_dwordx4 v[170:173], v[244:245], off offset:3072
	v_add_co_u32_e32 v244, vcc, 0x1000, v244
	s_nop 1
	v_addc_co_u32_e32 v245, vcc, 0, v245, vcc
	global_load_dwordx4 v[174:177], v[244:245], off
	global_load_dwordx4 v[178:181], v[244:245], off offset:1024
	global_load_dwordx4 v[182:185], v[244:245], off offset:2048
	global_load_dwordx4 v[186:189], v[244:245], off offset:3072
	v_lshl_add_u64 v[244:245], s[36:37], 0, v[242:243]
	global_load_dwordx4 v[198:201], v[244:245], off
	global_load_dwordx4 v[202:205], v[244:245], off offset:1024
	global_load_dwordx4 v[216:219], v[244:245], off offset:2048
	global_load_dwordx4 v[220:223], v[244:245], off offset:3072
	v_add_co_u32_e32 v244, vcc, 0x1000, v244
	s_nop 1
	v_addc_co_u32_e32 v245, vcc, 0, v245, vcc
	global_load_dwordx4 v[224:227], v[244:245], off
	global_load_dwordx4 v[228:231], v[244:245], off offset:1024
	global_load_dwordx4 v[232:235], v[244:245], off offset:2048
	global_load_dwordx4 v[246:249], v[244:245], off offset:3072
	s_mul_i32 s50, s22, 24
	v_or_b32_e32 v34, v16, v17
	s_lshl_b32 s51, s48, 5
	v_add_u32_e32 v237, v18, v19
	s_branch .LBB0_887

; __global__ void __launch_bounds__(NTHREADS, 2) hybrid_fwd(Args a) {
;     ...
;             for (int v = bid; v < 256; v += G) {
;                 u32x2 raw[2][8];
; #pragma unroll
;                 for (int q = 0; q < 2; ++q)
; #pragma unroll
;                     for (int j = 0; j < 8; ++j) raw[q][j] = __builtin_nontemporal_load((const u32x2*)(YB + (size_t)(v * 32 + wave + 8 * q) * DM + j * 256 + lane * 4));
;                 __syncthreads();
;                 if (tid < 16) hist[tid] = 0;
;                 __syncthreads();
;                 asm volatile("s_waitcnt vmcnt(0)" ::: "memory"); __syncthreads();
.LBB0_887:
	s_add_i32 s6, s22, s51
	s_ashr_i32 s7, s6, 31
	s_add_i32 s8, s6, 8
	s_lshl_b64 s[12:13], s[6:7], 12
	s_ashr_i32 s9, s8, 31
	v_lshl_add_u64 v[16:17], v[26:27], 0, s[12:13]
	s_lshl_b64 s[10:11], s[8:9], 12
	flat_load_dwordx2 v[58:59], v[16:17] nt
	flat_load_dwordx2 v[56:57], v[16:17] offset:512 nt
	flat_load_dwordx2 v[54:55], v[16:17] offset:1024 nt
	flat_load_dwordx2 v[52:53], v[16:17] offset:1536 nt
	flat_load_dwordx2 v[50:51], v[16:17] offset:2048 nt
	flat_load_dwordx2 v[48:49], v[16:17] offset:2560 nt
	flat_load_dwordx2 v[46:47], v[16:17] offset:3072 nt
	flat_load_dwordx2 v[44:45], v[16:17] offset:3584 nt
	v_lshl_add_u64 v[16:17], v[26:27], 0, s[10:11]
	flat_load_dwordx2 v[42:43], v[16:17] nt
	flat_load_dwordx2 v[40:41], v[16:17] offset:512 nt
	flat_load_dwordx2 v[38:39], v[16:17] offset:1024 nt
	flat_load_dwordx2 v[36:37], v[16:17] offset:1536 nt
	flat_load_dwordx2 v[22:23], v[16:17] offset:2048 nt
	flat_load_dwordx2 v[20:21], v[16:17] offset:2560 nt
	flat_load_dwordx2 v[18:19], v[16:17] offset:3072 nt
	s_nop 0
	flat_load_dwordx2 v[16:17], v[16:17] offset:3584 nt
	s_waitcnt vmcnt(0) lgkmcnt(0)
	s_barrier
	s_and_saveexec_b64 s[14:15], s[0:1]
	ds_write_b32 v156, v193
	s_or_b64 exec, exec, s[14:15]
	s_waitcnt lgkmcnt(0)
	s_barrier
	s_waitcnt vmcnt(0)
	s_add_i32 s38, s6, 16
	s_barrier
	s_mov_b64 s[14:15], s[34:35]
	v_lshlrev_b32_e32 v192, 2, v24
	s_mov_b64 s[16:17], s[36:37]
	v_lshl_add_u64 v[94:95], s[14:15], 0, v[192:193]
	v_lshlrev_b32_e32 v66, 16, v58
	v_lshl_add_u64 v[96:97], s[16:17], 0, v[192:193]
	s_nop 0
	v_and_b32_e32 v67, 0xffff0000, v58
	v_lshlrev_b32_e32 v64, 16, v59
	v_and_b32_e32 v65, 0xffff0000, v59
	v_add_f32_e32 v35, v66, v67
	v_add_f32_e32 v58, v64, v65
	v_lshlrev_b32_e32 v74, 16, v56
	v_and_b32_e32 v75, 0xffff0000, v56
	v_lshlrev_b32_e32 v72, 16, v57
	v_and_b32_e32 v73, 0xffff0000, v57
	v_add_f32_e32 v35, v35, v58
	v_add_f32_e32 v56, v74, v75
	v_add_f32_e32 v57, v72, v73
	v_lshlrev_b32_e32 v68, 16, v54
	v_and_b32_e32 v69, 0xffff0000, v54
	v_lshlrev_b32_e32 v70, 16, v55
	v_and_b32_e32 v71, 0xffff0000, v55
	v_add_f32_e32 v35, 0, v35
	v_add_f32_e32 v56, v56, v57
	v_add_f32_e32 v54, v68, v69
	v_add_f32_e32 v55, v70, v71
	v_lshlrev_b32_e32 v60, 16, v52
	v_and_b32_e32 v61, 0xffff0000, v52
	v_lshlrev_b32_e32 v62, 16, v53
	v_and_b32_e32 v63, 0xffff0000, v53
	v_add_f32_e32 v35, v35, v56
	v_add_f32_e32 v54, v54, v55
	v_add_f32_e32 v52, v60, v61
	v_add_f32_e32 v53, v62, v63
	v_add_f32_e32 v35, v35, v54
	v_add_f32_e32 v52, v52, v53
	v_lshlrev_b32_e32 v56, 16, v50
	v_and_b32_e32 v57, 0xffff0000, v50
	v_lshlrev_b32_e32 v58, 16, v51
	v_and_b32_e32 v59, 0xffff0000, v51
	v_add_f32_e32 v35, v35, v52
	v_add_f32_e32 v50, v56, v57
	v_add_f32_e32 v51, v58, v59
	v_lshlrev_b32_e32 v52, 16, v48
	v_and_b32_e32 v53, 0xffff0000, v48
	v_lshlrev_b32_e32 v54, 16, v49
	v_and_b32_e32 v55, 0xffff0000, v49
	v_add_f32_e32 v50, v50, v51
	v_add_f32_e32 v48, v52, v53
	v_add_f32_e32 v49, v54, v55
	v_add_f32_e32 v35, v35, v50
	v_add_f32_e32 v48, v48, v49
	v_add_f32_e32 v35, v35, v48
	v_lshlrev_b32_e32 v48, 16, v46
	v_and_b32_e32 v49, 0xffff0000, v46
	v_lshlrev_b32_e32 v50, 16, v47
	v_and_b32_e32 v51, 0xffff0000, v47
	v_add_f32_e32 v46, v48, v49
	v_add_f32_e32 v47, v50, v51
	v_add_f32_e32 v46, v46, v47
	v_add_f32_e32 v35, v35, v46
	v_lshlrev_b32_e32 v46, 16, v44
	v_and_b32_e32 v47, 0xffff0000, v44
	v_lshlrev_b32_e32 v44, 16, v45
	v_and_b32_e32 v45, 0xffff0000, v45
	v_add_f32_e32 v76, v46, v47
	v_add_f32_e32 v77, v44, v45
	v_add_f32_e32 v76, v76, v77
	v_add_f32_e32 v35, v35, v76
	s_lshl_b64 s[14:15], s[6:7], 11
	s_nop 0
	v_add_f32_dpp v35, v35, v35 quad_perm:[1,0,3,2] row_mask:0xf bank_mask:0xf bound_ctrl:1
	s_nop 1
	v_add_f32_dpp v35, v35, v35 quad_perm:[2,3,0,1] row_mask:0xf bank_mask:0xf bound_ctrl:1
	s_nop 1
	v_add_f32_dpp v35, v35, v35 row_ror:4 row_mask:0xf bank_mask:0xf bound_ctrl:1
	s_nop 1
	v_add_f32_dpp v35, v35, v35 row_ror:8 row_mask:0xf bank_mask:0xf bound_ctrl:1
	v_mov_b32_e32 v76, v35
	s_nop 1
	v_permlane16_swap_b32_e32 v35, v76
	v_add_f32_e32 v35, v35, v76
	v_mov_b32_e32 v76, v35
	s_nop 1
	v_permlane32_swap_b32_e32 v35, v76
	v_add_f32_e32 v35, v35, v76
	v_fmac_f32_e32 v65, 0xba000000, v35
	v_fmac_f32_e32 v67, 0xba000000, v35
	v_fmac_f32_e32 v64, 0xba000000, v35
	v_fmac_f32_e32 v66, 0xba000000, v35
	v_mul_f32_e32 v76, v67, v67
	v_mul_f32_e32 v77, v65, v65
	v_fmac_f32_e32 v76, v66, v66
	v_fmac_f32_e32 v77, v64, v64
	v_fmac_f32_e32 v73, 0xba000000, v35
	v_fmac_f32_e32 v75, 0xba000000, v35
	v_add_f32_e32 v76, v76, v77
	v_fmac_f32_e32 v72, 0xba000000, v35
	v_fmac_f32_e32 v74, 0xba000000, v35
	v_mul_f32_e32 v77, v75, v75
	v_mul_f32_e32 v78, v73, v73
	v_fmac_f32_e32 v77, v74, v74
	v_fmac_f32_e32 v78, v72, v72
	v_add_f32_e32 v77, v77, v78
	v_fmac_f32_e32 v71, 0xba000000, v35
	v_fmac_f32_e32 v69, 0xba000000, v35
	v_add_f32_e32 v76, v76, v77
	v_fmac_f32_e32 v70, 0xba000000, v35
	v_fmac_f32_e32 v68, 0xba000000, v35
	v_mul_f32_e32 v77, v69, v69
	v_mul_f32_e32 v78, v71, v71
	v_fmac_f32_e32 v77, v68, v68
	v_fmac_f32_e32 v78, v70, v70
	v_add_f32_e32 v77, v77, v78
	v_fmac_f32_e32 v63, 0xba000000, v35
	v_fmac_f32_e32 v61, 0xba000000, v35
	v_add_f32_e32 v76, v76, v77
	v_fmac_f32_e32 v62, 0xba000000, v35
	v_fmac_f32_e32 v60, 0xba000000, v35
	v_mul_f32_e32 v77, v61, v61
	v_mul_f32_e32 v78, v63, v63
	v_fmac_f32_e32 v77, v60, v60
	v_fmac_f32_e32 v78, v62, v62
	v_add_f32_e32 v77, v77, v78
	v_fmac_f32_e32 v59, 0xba000000, v35
	v_fmac_f32_e32 v57, 0xba000000, v35
	v_add_f32_e32 v76, v76, v77
	v_fmac_f32_e32 v58, 0xba000000, v35
	v_fmac_f32_e32 v56, 0xba000000, v35
	v_mul_f32_e32 v77, v57, v57
	v_mul_f32_e32 v78, v59, v59
	v_fmac_f32_e32 v77, v56, v56
	v_fmac_f32_e32 v78, v58, v58
	v_add_f32_e32 v77, v77, v78
	v_fmac_f32_e32 v55, 0xba000000, v35
	v_fmac_f32_e32 v53, 0xba000000, v35
	v_add_f32_e32 v76, v76, v77
	v_fmac_f32_e32 v54, 0xba000000, v35
	v_fmac_f32_e32 v52, 0xba000000, v35
	v_mul_f32_e32 v77, v53, v53
	v_mul_f32_e32 v78, v55, v55
	v_fmac_f32_e32 v77, v52, v52
	v_fmac_f32_e32 v78, v54, v54
	v_add_f32_e32 v77, v77, v78
	v_fmac_f32_e32 v51, 0xba000000, v35
	v_fmac_f32_e32 v49, 0xba000000, v35
	v_add_f32_e32 v76, v76, v77
	v_fmac_f32_e32 v50, 0xba000000, v35
	v_fmac_f32_e32 v48, 0xba000000, v35
	v_mul_f32_e32 v77, v49, v49
	v_mul_f32_e32 v78, v51, v51
	v_fmac_f32_e32 v77, v48, v48
	v_fmac_f32_e32 v78, v50, v50
	v_add_f32_e32 v77, v77, v78
	v_fmac_f32_e32 v45, 0xba000000, v35
	v_fmac_f32_e32 v47, 0xba000000, v35
	v_add_f32_e32 v76, v76, v77
	v_fmac_f32_e32 v44, 0xba000000, v35
	v_fmac_f32_e32 v46, 0xba000000, v35
	v_mul_f32_e32 v35, v47, v47
	v_mul_f32_e32 v77, v45, v45
	v_fmac_f32_e32 v35, v46, v46
	v_fmac_f32_e32 v77, v44, v44
	v_add_f32_e32 v35, v35, v77
	v_add_f32_e32 v35, v76, v35
	v_lshl_add_u64 v[78:79], v[30:31], 0, s[14:15]
	s_nop 0
	v_add_f32_dpp v35, v35, v35 quad_perm:[1,0,3,2] row_mask:0xf bank_mask:0xf bound_ctrl:1
	s_nop 1
	v_add_f32_dpp v35, v35, v35 quad_perm:[2,3,0,1] row_mask:0xf bank_mask:0xf bound_ctrl:1
	s_nop 1
	v_add_f32_dpp v35, v35, v35 row_ror:4 row_mask:0xf bank_mask:0xf bound_ctrl:1
	s_nop 1
	v_add_f32_dpp v35, v35, v35 row_ror:8 row_mask:0xf bank_mask:0xf bound_ctrl:1
	v_mov_b32_e32 v76, v35
	s_nop 1
	v_permlane16_swap_b32_e32 v35, v76
	v_add_f32_e32 v35, v35, v76
	v_mov_b32_e32 v76, v35
	s_nop 1
	v_permlane32_swap_b32_e32 v35, v76
	v_add_f32_e32 v35, v35, v76
	v_fmamk_f32 v35, v35, 0x3a000000, v207
	v_rsq_f32_e32 v84, v35
	v_lshl_add_u64 v[76:77], v[28:29], 0, s[12:13]
	v_pk_mul_f32 v[66:67], v[84:85], v[66:67] op_sel_hi:[0,1]
	v_pk_mul_f32 v[90:91], v[84:85], v[64:65] op_sel_hi:[0,1]
	s_waitcnt vmcnt(0) lgkmcnt(0)
	v_pk_fma_f32 v[64:65], v[158:159], v[66:67], v[198:199]
	v_mov_b32_e32 v85, 0
	v_med3_f32 v35, v64, s69, v208
	v_med3_f32 v66, v65, s69, v208
	v_cvt_pk_fp8_f32 v85, v35, v66
	v_pk_fma_f32 v[66:67], v[160:161], v[90:91], v[200:201]
	s_nop 0
	v_med3_f32 v35, v66, s69, v208
	v_med3_f32 v80, v67, s69, v208
	v_cvt_pk_fp8_f32 v85, v35, v80 op_sel:[0,0,1]
	v_cvt_pk_bf16_f32 v80, v64, v65
	v_cvt_pk_bf16_f32 v81, v66, v67
	global_store_dwordx2 v[76:77], v[80:81], off nt
	global_store_dword v[78:79], v85, off nt
	s_nop 0
	s_nop 0
	v_pk_mul_f32 v[74:75], v[84:85], v[74:75] op_sel_hi:[0,1]
	v_pk_mul_f32 v[90:91], v[84:85], v[72:73] op_sel_hi:[0,1]
	v_mov_b32_e32 v85, 0
	s_nop 0
	v_pk_fma_f32 v[72:73], v[162:163], v[74:75], v[202:203]
	s_nop 0
	v_med3_f32 v35, v72, s69, v208
	v_med3_f32 v74, v73, s69, v208
	v_cvt_pk_fp8_f32 v85, v35, v74
	v_pk_fma_f32 v[74:75], v[164:165], v[90:91], v[204:205]
	s_nop 0
	v_med3_f32 v35, v74, s69, v208
	v_med3_f32 v80, v75, s69, v208
	v_cvt_pk_fp8_f32 v85, v35, v80 op_sel:[0,0,1]
	v_cvt_pk_bf16_f32 v80, v72, v73
	v_cvt_pk_bf16_f32 v81, v74, v75
	global_store_dwordx2 v[76:77], v[80:81], off offset:512 nt
	global_store_dword v[78:79], v85, off offset:256 nt
	s_nop 0
	v_pk_mul_f32 v[68:69], v[84:85], v[68:69] op_sel_hi:[0,1]
	v_mov_b32_e32 v35, 0
	v_pk_mul_f32 v[70:71], v[84:85], v[70:71] op_sel_hi:[0,1]
	v_pk_mul_f32 v[60:61], v[84:85], v[60:61] op_sel_hi:[0,1]
	v_pk_mul_f32 v[62:63], v[84:85], v[62:63] op_sel_hi:[0,1]
	v_pk_mul_f32 v[56:57], v[84:85], v[56:57] op_sel_hi:[0,1]
	v_pk_mul_f32 v[58:59], v[84:85], v[58:59] op_sel_hi:[0,1]
	v_pk_mul_f32 v[52:53], v[84:85], v[52:53] op_sel_hi:[0,1]
	v_pk_mul_f32 v[54:55], v[84:85], v[54:55] op_sel_hi:[0,1]
	v_pk_mul_f32 v[48:49], v[84:85], v[48:49] op_sel_hi:[0,1]
	v_pk_mul_f32 v[50:51], v[84:85], v[50:51] op_sel_hi:[0,1]
	v_pk_mul_f32 v[46:47], v[84:85], v[46:47] op_sel_hi:[0,1]
	v_pk_mul_f32 v[44:45], v[84:85], v[44:45] op_sel_hi:[0,1]
	s_nop 0
	v_pk_fma_f32 v[82:83], v[166:167], v[68:69], v[216:217]
	s_nop 0
	v_med3_f32 v68, v82, s69, v208
	v_med3_f32 v69, v83, s69, v208
	v_cvt_pk_fp8_f32 v35, v68, v69
	v_pk_fma_f32 v[80:81], v[168:169], v[70:71], v[218:219]
	v_add_co_u32_e32 v90, vcc, s33, v94
	v_med3_f32 v68, v80, s69, v208
	v_med3_f32 v69, v81, s69, v208
	v_cvt_pk_fp8_f32 v35, v68, v69 op_sel:[0,0,1]
	v_cvt_pk_bf16_f32 v68, v82, v83
	v_cvt_pk_bf16_f32 v69, v80, v81
	global_store_dwordx2 v[76:77], v[68:69], off offset:1024 nt
	global_store_dword v[78:79], v35, off offset:512 nt
	s_nop 0
	s_nop 0
	v_addc_co_u32_e32 v91, vcc, 0, v95, vcc
	v_mov_b32_e32 v35, 0
	v_add_co_u32_e32 v96, vcc, s33, v96
	s_nop 0
	v_pk_fma_f32 v[94:95], v[170:171], v[60:61], v[220:221]
	s_nop 0
	v_med3_f32 v60, v94, s69, v208
	v_med3_f32 v61, v95, s69, v208
	v_cvt_pk_fp8_f32 v35, v60, v61
	v_pk_fma_f32 v[92:93], v[172:173], v[62:63], v[222:223]
	v_addc_co_u32_e32 v97, vcc, 0, v97, vcc
	v_med3_f32 v60, v92, s69, v208
	v_med3_f32 v61, v93, s69, v208
	v_cvt_pk_fp8_f32 v35, v60, v61 op_sel:[0,0,1]
	v_cvt_pk_bf16_f32 v60, v94, v95
	v_cvt_pk_bf16_f32 v61, v92, v93
	global_store_dwordx2 v[76:77], v[60:61], off offset:1536 nt
	global_store_dword v[78:79], v35, off offset:768 nt
	s_nop 0
	s_nop 0
	v_mov_b32_e32 v35, 0
	s_nop 0
	v_pk_fma_f32 v[114:115], v[174:175], v[56:57], v[224:225]
	s_nop 0
	v_med3_f32 v56, v114, s69, v208
	v_med3_f32 v57, v115, s69, v208
	v_cvt_pk_fp8_f32 v35, v56, v57
	v_pk_fma_f32 v[112:113], v[176:177], v[58:59], v[226:227]
	s_nop 0
	v_med3_f32 v56, v112, s69, v208
	v_med3_f32 v57, v113, s69, v208
	v_cvt_pk_fp8_f32 v35, v56, v57 op_sel:[0,0,1]
	v_cvt_pk_bf16_f32 v56, v114, v115
	v_cvt_pk_bf16_f32 v57, v112, v113
	global_store_dwordx2 v[76:77], v[56:57], off offset:2048 nt
	global_store_dword v[78:79], v35, off offset:1024 nt
	s_nop 0
	s_nop 0
	v_mov_b32_e32 v35, 0
	s_nop 0
	v_pk_fma_f32 v[118:119], v[178:179], v[52:53], v[228:229]
	s_nop 0
	v_med3_f32 v52, v118, s69, v208
	v_med3_f32 v53, v119, s69, v208
	v_cvt_pk_fp8_f32 v35, v52, v53
	v_pk_fma_f32 v[116:117], v[180:181], v[54:55], v[230:231]
	s_nop 0
	v_med3_f32 v52, v116, s69, v208
	v_med3_f32 v53, v117, s69, v208
	v_cvt_pk_fp8_f32 v35, v52, v53 op_sel:[0,0,1]
	v_cvt_pk_bf16_f32 v52, v118, v119
	v_cvt_pk_bf16_f32 v53, v116, v117
	global_store_dwordx2 v[76:77], v[52:53], off offset:2560 nt
	global_store_dword v[78:79], v35, off offset:1280 nt
	s_nop 0
	s_nop 0
	v_mov_b32_e32 v35, 0
	s_nop 0
	v_pk_fma_f32 v[122:123], v[182:183], v[48:49], v[232:233]
	s_nop 0
	v_med3_f32 v48, v122, s69, v208
	v_med3_f32 v49, v123, s69, v208
	v_cvt_pk_fp8_f32 v35, v48, v49
	v_pk_fma_f32 v[120:121], v[184:185], v[50:51], v[234:235]
	s_nop 0
	v_med3_f32 v48, v120, s69, v208
	v_med3_f32 v49, v121, s69, v208
	v_cvt_pk_fp8_f32 v35, v48, v49 op_sel:[0,0,1]
	v_cvt_pk_bf16_f32 v48, v122, v123
	v_cvt_pk_bf16_f32 v49, v120, v121
	global_store_dwordx2 v[76:77], v[48:49], off offset:3072 nt
	global_store_dword v[78:79], v35, off offset:1536 nt
	s_nop 0
	s_nop 0
	v_mov_b32_e32 v35, 0
	s_nop 0
	v_pk_fma_f32 v[124:125], v[186:187], v[46:47], v[246:247]
	s_nop 0
	v_med3_f32 v46, v124, s69, v208
	v_med3_f32 v47, v125, s69, v208
	v_mov_b32_e32 v48, 0
	v_cvt_pk_fp8_f32 v48, v46, v47
	v_pk_fma_f32 v[126:127], v[188:189], v[44:45], v[248:249]
	s_nop 0
	v_med3_f32 v44, v126, s69, v208
	v_med3_f32 v45, v127, s69, v208
	v_cvt_pk_fp8_f32 v48, v44, v45 op_sel:[0,0,1]
	v_cvt_pk_bf16_f32 v44, v124, v125
	v_cvt_pk_bf16_f32 v45, v126, v127
	global_store_dwordx2 v[76:77], v[44:45], off offset:3584 nt
	global_store_dword v[78:79], v48, off offset:1792 nt
	v_lshlrev_b32_e32 v84, 16, v42
	v_and_b32_e32 v85, 0xffff0000, v42
	v_lshlrev_b32_e32 v78, 16, v43
	v_and_b32_e32 v79, 0xffff0000, v43
	v_add_f32_e32 v42, v84, v85
	v_add_f32_e32 v43, v78, v79
	v_lshlrev_b32_e32 v76, 16, v40
	v_and_b32_e32 v77, 0xffff0000, v40
	v_lshlrev_b32_e32 v70, 16, v41
	v_and_b32_e32 v71, 0xffff0000, v41
	v_add_f32_e32 v42, v42, v43
	v_add_f32_e32 v40, v76, v77
	v_add_f32_e32 v41, v70, v71
	v_lshlrev_b32_e32 v62, 16, v38
	v_and_b32_e32 v63, 0xffff0000, v38
	v_lshlrev_b32_e32 v68, 16, v39
	v_and_b32_e32 v69, 0xffff0000, v39
	v_add_f32_e32 v42, 0, v42
	v_add_f32_e32 v40, v40, v41
	v_add_f32_e32 v38, v62, v63
	v_add_f32_e32 v39, v68, v69
	v_lshlrev_b32_e32 v58, 16, v36
	v_and_b32_e32 v59, 0xffff0000, v36
	v_lshlrev_b32_e32 v60, 16, v37
	v_and_b32_e32 v61, 0xffff0000, v37
	v_add_f32_e32 v40, v42, v40
	v_add_f32_e32 v38, v38, v39
	v_add_f32_e32 v36, v58, v59
	v_add_f32_e32 v37, v60, v61
	v_lshlrev_b32_e32 v50, 16, v22
	v_and_b32_e32 v51, 0xffff0000, v22
	v_lshlrev_b32_e32 v52, 16, v23
	v_and_b32_e32 v53, 0xffff0000, v23
	v_add_f32_e32 v38, v40, v38
	v_add_f32_e32 v36, v36, v37
	v_add_f32_e32 v22, v50, v51
	v_add_f32_e32 v23, v52, v53
	v_lshlrev_b32_e32 v46, 16, v20
	v_and_b32_e32 v47, 0xffff0000, v20
	v_lshlrev_b32_e32 v48, 16, v21
	v_and_b32_e32 v49, 0xffff0000, v21
	v_add_f32_e32 v36, v38, v36
	v_add_f32_e32 v22, v22, v23
	v_add_f32_e32 v20, v46, v47
	v_add_f32_e32 v21, v48, v49
	v_lshlrev_b32_e32 v40, 16, v18
	v_and_b32_e32 v41, 0xffff0000, v18
	v_lshlrev_b32_e32 v42, 16, v19
	v_and_b32_e32 v43, 0xffff0000, v19
	v_add_f32_e32 v22, v36, v22
	v_add_f32_e32 v20, v20, v21
	v_add_f32_e32 v18, v40, v41
	v_add_f32_e32 v19, v42, v43
	v_lshlrev_b32_e32 v38, 16, v16
	v_and_b32_e32 v39, 0xffff0000, v16
	v_lshlrev_b32_e32 v36, 16, v17
	v_and_b32_e32 v37, 0xffff0000, v17
	v_add_f32_e32 v20, v22, v20
	v_add_f32_e32 v18, v18, v19
	v_add_f32_e32 v16, v38, v39
	v_add_f32_e32 v17, v36, v37
	v_add_f32_e32 v18, v20, v18
	v_add_f32_e32 v16, v16, v17
	v_add_f32_e32 v16, v18, v16
	s_mov_b64 s[12:13], s[34:35]
	s_mov_b64 s[14:15], s[36:37]
	v_add_f32_dpp v16, v16, v16 quad_perm:[1,0,3,2] row_mask:0xf bank_mask:0xf bound_ctrl:1
	v_lshl_add_u64 v[100:101], s[12:13], 0, v[192:193]
	v_lshl_add_u64 v[56:57], v[28:29], 0, s[10:11]
	v_add_f32_dpp v16, v16, v16 quad_perm:[2,3,0,1] row_mask:0xf bank_mask:0xf bound_ctrl:1
	v_lshl_add_u64 v[86:87], s[14:15], 0, v[192:193]
	s_lshl_b64 s[8:9], s[8:9], 11
	v_add_f32_dpp v16, v16, v16 row_ror:4 row_mask:0xf bank_mask:0xf bound_ctrl:1
	v_lshl_add_u64 v[54:55], v[30:31], 0, s[8:9]
	s_nop 0
	v_add_f32_dpp v16, v16, v16 row_ror:8 row_mask:0xf bank_mask:0xf bound_ctrl:1
	v_mov_b32_e32 v17, v16
	s_nop 1
	v_permlane16_swap_b32_e32 v16, v17
	v_add_f32_e32 v16, v16, v17
	v_mov_b32_e32 v17, v16
	s_nop 1
	v_permlane32_swap_b32_e32 v16, v17
	v_add_f32_e32 v16, v16, v17
	v_fmac_f32_e32 v79, 0xba000000, v16
	v_fmac_f32_e32 v85, 0xba000000, v16
	v_fmac_f32_e32 v78, 0xba000000, v16
	v_fmac_f32_e32 v84, 0xba000000, v16
	v_mul_f32_e32 v17, v85, v85
	v_mul_f32_e32 v18, v79, v79
	v_fmac_f32_e32 v17, v84, v84
	v_fmac_f32_e32 v18, v78, v78
	v_fmac_f32_e32 v71, 0xba000000, v16
	v_fmac_f32_e32 v77, 0xba000000, v16
	v_add_f32_e32 v17, v17, v18
	v_fmac_f32_e32 v70, 0xba000000, v16
	v_fmac_f32_e32 v76, 0xba000000, v16
	v_mul_f32_e32 v18, v77, v77
	v_mul_f32_e32 v19, v71, v71
	v_fmac_f32_e32 v18, v76, v76
	v_fmac_f32_e32 v19, v70, v70
	v_add_f32_e32 v18, v18, v19
	v_fmac_f32_e32 v69, 0xba000000, v16
	v_fmac_f32_e32 v63, 0xba000000, v16
	v_add_f32_e32 v17, v17, v18
	v_fmac_f32_e32 v68, 0xba000000, v16
	v_fmac_f32_e32 v62, 0xba000000, v16
	v_mul_f32_e32 v18, v63, v63
	v_mul_f32_e32 v19, v69, v69
	v_fmac_f32_e32 v18, v62, v62
	v_fmac_f32_e32 v19, v68, v68
	v_add_f32_e32 v18, v18, v19
	v_fmac_f32_e32 v61, 0xba000000, v16
	v_fmac_f32_e32 v59, 0xba000000, v16
	v_add_f32_e32 v17, v17, v18
	v_fmac_f32_e32 v60, 0xba000000, v16
	v_fmac_f32_e32 v58, 0xba000000, v16
	v_mul_f32_e32 v18, v59, v59
	v_mul_f32_e32 v19, v61, v61
	v_fmac_f32_e32 v18, v58, v58
	v_fmac_f32_e32 v19, v60, v60
	v_add_f32_e32 v18, v18, v19
	v_fmac_f32_e32 v53, 0xba000000, v16
	v_fmac_f32_e32 v51, 0xba000000, v16
	v_add_f32_e32 v17, v17, v18
	v_fmac_f32_e32 v52, 0xba000000, v16
	v_fmac_f32_e32 v50, 0xba000000, v16
	v_mul_f32_e32 v18, v51, v51
	v_mul_f32_e32 v19, v53, v53
	v_fmac_f32_e32 v18, v50, v50
	v_fmac_f32_e32 v19, v52, v52
	v_add_f32_e32 v18, v18, v19
	v_fmac_f32_e32 v49, 0xba000000, v16
	v_fmac_f32_e32 v47, 0xba000000, v16
	v_add_f32_e32 v17, v17, v18
	v_fmac_f32_e32 v48, 0xba000000, v16
	v_fmac_f32_e32 v46, 0xba000000, v16
	v_mul_f32_e32 v18, v47, v47
	v_mul_f32_e32 v19, v49, v49
	v_fmac_f32_e32 v18, v46, v46
	v_fmac_f32_e32 v19, v48, v48
	v_add_f32_e32 v18, v18, v19
	v_fmac_f32_e32 v43, 0xba000000, v16
	v_fmac_f32_e32 v41, 0xba000000, v16
	v_add_f32_e32 v17, v17, v18
	v_fmac_f32_e32 v42, 0xba000000, v16
	v_fmac_f32_e32 v40, 0xba000000, v16
	v_mul_f32_e32 v18, v41, v41
	v_mul_f32_e32 v19, v43, v43
	v_fmac_f32_e32 v18, v40, v40
	v_fmac_f32_e32 v19, v42, v42
	v_add_f32_e32 v18, v18, v19
	v_fmac_f32_e32 v37, 0xba000000, v16
	v_fmac_f32_e32 v39, 0xba000000, v16
	v_add_f32_e32 v17, v17, v18
	v_fmac_f32_e32 v36, 0xba000000, v16
	v_fmac_f32_e32 v38, 0xba000000, v16
	v_mul_f32_e32 v16, v39, v39
	v_mul_f32_e32 v18, v37, v37
	v_fmac_f32_e32 v16, v38, v38
	v_fmac_f32_e32 v18, v36, v36
	v_add_f32_e32 v16, v16, v18
	v_add_f32_e32 v16, v17, v16
	s_nop 1
	v_add_f32_dpp v16, v16, v16 quad_perm:[1,0,3,2] row_mask:0xf bank_mask:0xf bound_ctrl:1
	s_nop 1
	v_add_f32_dpp v16, v16, v16 quad_perm:[2,3,0,1] row_mask:0xf bank_mask:0xf bound_ctrl:1
	s_nop 1
	v_add_f32_dpp v16, v16, v16 row_ror:4 row_mask:0xf bank_mask:0xf bound_ctrl:1
	s_nop 1
	v_add_f32_dpp v16, v16, v16 row_ror:8 row_mask:0xf bank_mask:0xf bound_ctrl:1
	v_mov_b32_e32 v17, v16
	s_nop 1
	v_permlane16_swap_b32_e32 v16, v17
	v_add_f32_e32 v16, v16, v17
	v_mov_b32_e32 v17, v16
	s_nop 1
	v_permlane32_swap_b32_e32 v16, v17
	v_add_f32_e32 v16, v16, v17
	v_fmamk_f32 v16, v16, 0x3a000000, v207
	v_rsq_f32_e32 v44, v16
	s_nop 0
	v_pk_mul_f32 v[84:85], v[44:45], v[84:85] op_sel_hi:[0,1]
	v_pk_mul_f32 v[78:79], v[44:45], v[78:79] op_sel_hi:[0,1]
	v_pk_mul_f32 v[76:77], v[44:45], v[76:77] op_sel_hi:[0,1]
	v_pk_mul_f32 v[70:71], v[44:45], v[70:71] op_sel_hi:[0,1]
	v_pk_mul_f32 v[62:63], v[44:45], v[62:63] op_sel_hi:[0,1]
	v_pk_mul_f32 v[68:69], v[44:45], v[68:69] op_sel_hi:[0,1]
	v_pk_mul_f32 v[58:59], v[44:45], v[58:59] op_sel_hi:[0,1]
	v_pk_mul_f32 v[60:61], v[44:45], v[60:61] op_sel_hi:[0,1]
	v_pk_mul_f32 v[50:51], v[44:45], v[50:51] op_sel_hi:[0,1]
	v_pk_mul_f32 v[52:53], v[44:45], v[52:53] op_sel_hi:[0,1]
	v_mov_b32_e32 v45, 0
	s_waitcnt vmcnt(0) lgkmcnt(0)
	v_pk_fma_f32 v[128:129], v[160:161], v[78:79], v[200:201]
	v_pk_fma_f32 v[130:131], v[158:159], v[84:85], v[198:199]
	v_mov_b32_e32 v20, 0
	v_cvt_pk_bf16_f32 v16, v130, v131
	v_cvt_pk_bf16_f32 v17, v128, v129
	global_store_dwordx2 v[56:57], v[16:17], off nt
	v_med3_f32 v16, v130, s69, v208
	v_med3_f32 v17, v131, s69, v208
	v_cvt_pk_fp8_f32 v20, v16, v17
	v_med3_f32 v18, v128, s69, v208
	v_med3_f32 v19, v129, s69, v208
	v_cvt_pk_fp8_f32 v20, v18, v19 op_sel:[0,0,1]
	global_store_dword v[54:55], v20, off nt
	s_nop 0
	s_nop 0
	s_nop 0
	v_pk_fma_f32 v[104:105], v[164:165], v[70:71], v[204:205]
	v_pk_fma_f32 v[106:107], v[162:163], v[76:77], v[202:203]
	v_mov_b32_e32 v20, 0
	v_cvt_pk_bf16_f32 v16, v106, v107
	v_cvt_pk_bf16_f32 v17, v104, v105
	global_store_dwordx2 v[56:57], v[16:17], off offset:512 nt
	v_med3_f32 v16, v106, s69, v208
	v_med3_f32 v17, v107, s69, v208
	v_cvt_pk_fp8_f32 v20, v16, v17
	v_med3_f32 v18, v104, s69, v208
	v_med3_f32 v19, v105, s69, v208
	v_cvt_pk_fp8_f32 v20, v18, v19 op_sel:[0,0,1]
	global_store_dword v[54:55], v20, off offset:256 nt
	s_nop 0
	s_nop 0
	s_nop 0
	v_pk_fma_f32 v[96:97], v[168:169], v[68:69], v[218:219]
	v_pk_fma_f32 v[98:99], v[166:167], v[62:63], v[216:217]
	v_mov_b32_e32 v20, 0
	v_cvt_pk_bf16_f32 v16, v98, v99
	v_cvt_pk_bf16_f32 v17, v96, v97
	global_store_dwordx2 v[56:57], v[16:17], off offset:1024 nt
	v_med3_f32 v16, v98, s69, v208
	v_med3_f32 v17, v99, s69, v208
	v_cvt_pk_fp8_f32 v20, v16, v17
	v_med3_f32 v18, v96, s69, v208
	v_med3_f32 v19, v97, s69, v208
	v_cvt_pk_fp8_f32 v20, v18, v19 op_sel:[0,0,1]
	global_store_dword v[54:55], v20, off offset:512 nt
	s_nop 0
	s_nop 0
	s_nop 0
	v_pk_fma_f32 v[88:89], v[172:173], v[60:61], v[222:223]
	v_pk_fma_f32 v[90:91], v[170:171], v[58:59], v[220:221]
	v_mov_b32_e32 v20, 0
	v_cvt_pk_bf16_f32 v16, v90, v91
	v_cvt_pk_bf16_f32 v17, v88, v89
	global_store_dwordx2 v[56:57], v[16:17], off offset:1536 nt
	v_med3_f32 v16, v90, s69, v208
	v_med3_f32 v17, v91, s69, v208
	v_cvt_pk_fp8_f32 v20, v16, v17
	v_med3_f32 v18, v88, s69, v208
	v_med3_f32 v19, v89, s69, v208
	v_add_co_u32_e32 v16, vcc, s33, v100
	v_cvt_pk_fp8_f32 v20, v18, v19 op_sel:[0,0,1]
	s_nop 0
	v_addc_co_u32_e32 v17, vcc, 0, v101, vcc
	v_add_co_u32_e32 v18, vcc, s33, v86
	global_store_dword v[54:55], v20, off offset:768 nt
	s_nop 0
	v_addc_co_u32_e32 v19, vcc, 0, v87, vcc
	s_nop 0
	s_nop 0
	v_pk_fma_f32 v[84:85], v[176:177], v[52:53], v[226:227]
	v_pk_fma_f32 v[86:87], v[174:175], v[50:51], v[224:225]
	v_med3_f32 v22, v84, s69, v208
	v_cvt_pk_bf16_f32 v20, v86, v87
	v_cvt_pk_bf16_f32 v21, v84, v85
	global_store_dwordx2 v[56:57], v[20:21], off offset:2048 nt
	v_med3_f32 v20, v86, s69, v208
	v_med3_f32 v21, v87, s69, v208
	v_cvt_pk_fp8_f32 v45, v20, v21
	v_med3_f32 v23, v85, s69, v208
; #define LAS __attribute__((address_space(3)))
; __global__ void __launch_bounds__(NTHREADS, 2) hybrid_fwd(Args a) {
;     ...
;                     if (qp == 0) {
; #pragma unroll
;                         for (int q = 0; q < 2; ++q)
; #pragma unroll
;                             for (int j = 0; j < 8; ++j) raw[q][j] = __builtin_nontemporal_load((const u32x2*)(YB + (size_t)(v * 32 + wave + 8 * (2 + q)) * DM + j * 256 + lane * 4));
;                         __builtin_amdgcn_sched_barrier(0);
;                     }
;                     f32x2 y2[8][4];
; #pragma unroll
;                     for (int j = 0; j < 8; ++j)
; #pragma unroll
;                         for (int c = 0; c < 4; ++c) y2[j][c] = (f32x2){ya[j][c], yb[j][c]};
;                     f32x2 acc2[16];
; #pragma unroll
;                     for (int e = 0; e < 16; ++e) acc2[e] = (f32x2){0.f, 0.f};
; #pragma unroll
;                     for (int j = 0; j < 8; ++j) {
; #pragma unroll
;                         for (int e = 0; e < 16; ++e) { const f32x4 w = *(const LAS f32x4*)(rwT + e * 2052 + j * 256 + lane * 4);
;                             acc2[e] += y2[j][0] * (f32x2){w[0], w[0]}; acc2[e] += y2[j][1] * (f32x2){w[1], w[1]};
;                             acc2[e] += y2[j][2] * (f32x2){w[2], w[2]}; acc2[e] += y2[j][3] * (f32x2){w[3], w[3]}; }
;                         __builtin_amdgcn_sched_barrier(0);
;                     }
	v_cvt_pk_fp8_f32 v45, v22, v23 op_sel:[0,0,1]
	global_store_dword v[54:55], v45, off offset:1024 nt
	s_nop 0
	v_pk_mul_f32 v[46:47], v[44:45], v[46:47] op_sel_hi:[0,1]
	v_pk_mul_f32 v[48:49], v[44:45], v[48:49] op_sel_hi:[0,1]
	v_mov_b32_e32 v45, 0
	s_nop 0
	v_pk_fma_f32 v[76:77], v[180:181], v[48:49], v[230:231]
	v_pk_fma_f32 v[78:79], v[178:179], v[46:47], v[228:229]
	v_med3_f32 v22, v76, s69, v208
	v_cvt_pk_bf16_f32 v20, v78, v79
	v_cvt_pk_bf16_f32 v21, v76, v77
	global_store_dwordx2 v[56:57], v[20:21], off offset:2560 nt
	v_med3_f32 v20, v78, s69, v208
	v_med3_f32 v21, v79, s69, v208
	v_cvt_pk_fp8_f32 v45, v20, v21
	v_med3_f32 v23, v77, s69, v208
	v_cvt_pk_fp8_f32 v45, v22, v23 op_sel:[0,0,1]
	global_store_dword v[54:55], v45, off offset:1280 nt
	s_nop 0
	v_pk_mul_f32 v[40:41], v[44:45], v[40:41] op_sel_hi:[0,1]
	v_pk_mul_f32 v[42:43], v[44:45], v[42:43] op_sel_hi:[0,1]
	v_pk_mul_f32 v[38:39], v[44:45], v[38:39] op_sel_hi:[0,1]
	v_pk_mul_f32 v[36:37], v[44:45], v[36:37] op_sel_hi:[0,1]
	s_nop 0
	v_pk_fma_f32 v[68:69], v[184:185], v[42:43], v[234:235]
	v_pk_fma_f32 v[70:71], v[182:183], v[40:41], v[232:233]
	v_mov_b32_e32 v40, 0
	v_cvt_pk_bf16_f32 v20, v70, v71
	v_cvt_pk_bf16_f32 v21, v68, v69
	global_store_dwordx2 v[56:57], v[20:21], off offset:3072 nt
	v_med3_f32 v20, v70, s69, v208
	v_med3_f32 v21, v71, s69, v208
	v_cvt_pk_fp8_f32 v40, v20, v21
	v_med3_f32 v22, v68, s69, v208
	v_med3_f32 v23, v69, s69, v208
	v_cvt_pk_fp8_f32 v40, v22, v23 op_sel:[0,0,1]
	global_store_dword v[54:55], v40, off offset:1536 nt
	s_nop 0
	s_nop 0
	s_nop 0
	v_pk_fma_f32 v[60:61], v[188:189], v[36:37], v[248:249]
	v_pk_fma_f32 v[62:63], v[186:187], v[38:39], v[246:247]
	v_mov_b32_e32 v20, 0
	v_cvt_pk_bf16_f32 v16, v62, v63
	v_cvt_pk_bf16_f32 v17, v60, v61
	global_store_dwordx2 v[56:57], v[16:17], off offset:3584 nt
	v_med3_f32 v16, v62, s69, v208
	v_med3_f32 v17, v63, s69, v208
	v_cvt_pk_fp8_f32 v20, v16, v17
	v_med3_f32 v18, v60, s69, v208
	v_med3_f32 v19, v61, s69, v208
	v_cvt_pk_fp8_f32 v20, v18, v19 op_sel:[0,0,1]
	global_store_dword v[54:55], v20, off offset:1792 nt
	s_ashr_i32 s39, s38, 31
	s_add_i32 s40, s6, 24
	s_lshl_b64 s[44:45], s[38:39], 12
	s_ashr_i32 s41, s40, 31
	v_lshl_add_u64 v[16:17], v[26:27], 0, s[44:45]
	s_lshl_b64 s[42:43], s[40:41], 12
	flat_load_dwordx2 v[58:59], v[16:17] nt
	flat_load_dwordx2 v[56:57], v[16:17] offset:512 nt
	flat_load_dwordx2 v[54:55], v[16:17] offset:1024 nt
	flat_load_dwordx2 v[52:53], v[16:17] offset:1536 nt
	flat_load_dwordx2 v[50:51], v[16:17] offset:2048 nt
	flat_load_dwordx2 v[48:49], v[16:17] offset:2560 nt
	flat_load_dwordx2 v[46:47], v[16:17] offset:3072 nt
	flat_load_dwordx2 v[44:45], v[16:17] offset:3584 nt
	v_lshl_add_u64 v[16:17], v[26:27], 0, s[42:43]
	flat_load_dwordx2 v[42:43], v[16:17] nt
	flat_load_dwordx2 v[40:41], v[16:17] offset:512 nt
	flat_load_dwordx2 v[38:39], v[16:17] offset:1024 nt
	flat_load_dwordx2 v[36:37], v[16:17] offset:1536 nt
	flat_load_dwordx2 v[22:23], v[16:17] offset:2048 nt
	flat_load_dwordx2 v[20:21], v[16:17] offset:2560 nt
	flat_load_dwordx2 v[18:19], v[16:17] offset:3072 nt
	s_nop 0
	flat_load_dwordx2 v[16:17], v[16:17] offset:3584 nt
	v_add_u32_e32 v238, 0x10000, v25
	ds_read_b128 v[158:161], v25 offset:0
	ds_read_b128 v[162:165], v25 offset:8208
	ds_read_b128 v[166:169], v25 offset:16416
	ds_read_b128 v[170:173], v25 offset:24624
	ds_read_b128 v[174:177], v25 offset:32832
	ds_read_b128 v[178:181], v25 offset:41040
	ds_read_b128 v[182:185], v25 offset:49248
	ds_read_b128 v[186:189], v25 offset:57456
	v_mov_b32_e32 v100, v94
	v_mov_b32_e32 v101, v90
	v_mov_b32_e32 v90, v95
	v_mov_b32_e32 v102, v92
	v_mov_b32_e32 v103, v88
	v_mov_b32_e32 v88, v93
	v_mov_b32_e32 v92, v114
	v_mov_b32_e32 v93, v86
	v_mov_b32_e32 v86, v115
	v_mov_b32_e32 v94, v112
	v_mov_b32_e32 v95, v84
	v_mov_b32_e32 v84, v113
	ds_read_b128 v[198:201], v238 offset:128
	v_mov_b32_e32 v136, v64
	v_mov_b32_e32 v137, v130
	v_mov_b32_e32 v130, v65
	v_mov_b32_e32 v108, v82
	v_mov_b32_e32 v109, v98
	v_mov_b32_e32 v98, v83
	v_mov_b32_e32 v82, v116
	v_mov_b32_e32 v83, v76
	v_mov_b32_e32 v76, v117
	s_waitcnt lgkmcnt(8)
	v_pk_fma_f32 v[116:117], v[136:137], v[158:159], 0 op_sel_hi:[1,0,0]
	v_mov_b32_e32 v138, v66
	v_mov_b32_e32 v139, v128
	v_pk_fma_f32 v[112:113], v[158:159], v[130:131], v[116:117] op_sel:[1,0,0]
	v_mov_b32_e32 v128, v67
	v_pk_fma_f32 v[112:113], v[160:161], v[138:139], v[112:113] op_sel_hi:[0,1,1]
	v_mov_b32_e32 v114, v161
	v_pk_fma_f32 v[112:113], v[114:115], v[128:129], v[112:113] op_sel_hi:[0,1,1]
	ds_read_b128 v[202:205], v238 offset:8336
	v_mov_b32_e32 v110, v80
	v_mov_b32_e32 v111, v96
	v_mov_b32_e32 v96, v81
	v_mov_b32_e32 v80, v118
	v_mov_b32_e32 v81, v78
	v_mov_b32_e32 v78, v119
	s_waitcnt lgkmcnt(8)
	v_pk_fma_f32 v[118:119], v[136:137], v[162:163], 0 op_sel_hi:[1,0,0]
	v_mov_b32_e32 v134, v74
	v_pk_fma_f32 v[114:115], v[162:163], v[130:131], v[118:119] op_sel:[1,0,0]
	v_mov_b32_e32 v135, v104
	v_pk_fma_f32 v[114:115], v[164:165], v[138:139], v[114:115] op_sel_hi:[0,1,1]
	v_mov_b32_e32 v116, v165
	v_pk_fma_f32 v[152:153], v[116:117], v[128:129], v[114:115] op_sel_hi:[0,1,1]
	ds_read_b128 v[216:219], v238 offset:16544
	v_mov_b32_e32 v104, v75
	v_mov_b32_e32 v74, v120
	v_mov_b32_e32 v75, v68
	v_mov_b32_e32 v68, v121
	s_waitcnt lgkmcnt(8)
	v_pk_fma_f32 v[118:119], v[136:137], v[166:167], 0 op_sel_hi:[1,0,0]
	v_mov_b32_e32 v132, v72
	v_pk_fma_f32 v[114:115], v[166:167], v[130:131], v[118:119] op_sel:[1,0,0]
	v_mov_b32_e32 v133, v106
	v_pk_fma_f32 v[114:115], v[168:169], v[138:139], v[114:115] op_sel_hi:[0,1,1]
	v_mov_b32_e32 v116, v169
	v_pk_fma_f32 v[154:155], v[116:117], v[128:129], v[114:115] op_sel_hi:[0,1,1]
	ds_read_b128 v[220:223], v238 offset:24752
	v_mov_b32_e32 v106, v73
	v_mov_b32_e32 v72, v122
	v_mov_b32_e32 v73, v70
	v_mov_b32_e32 v70, v123
	s_waitcnt lgkmcnt(8)
; #define LAS __attribute__((address_space(3)))
; __global__ void __launch_bounds__(NTHREADS, 2) hybrid_fwd(Args a) {
;     ...
;                     for (int j = 0; j < 8; ++j) {
; #pragma unroll
;                         for (int e = 0; e < 16; ++e) { const f32x4 w = *(const LAS f32x4*)(rwT + e * 2052 + j * 256 + lane * 4);
;                             acc2[e] += y2[j][0] * (f32x2){w[0], w[0]}; acc2[e] += y2[j][1] * (f32x2){w[1], w[1]};
;                             acc2[e] += y2[j][2] * (f32x2){w[2], w[2]}; acc2[e] += y2[j][3] * (f32x2){w[3], w[3]}; }
;                         __builtin_amdgcn_sched_barrier(0);
;                     }
	v_pk_fma_f32 v[118:119], v[136:137], v[170:171], 0 op_sel_hi:[1,0,0]
	v_mov_b32_e32 v66, v124
	v_pk_fma_f32 v[114:115], v[170:171], v[130:131], v[118:119] op_sel:[1,0,0]
	v_mov_b32_e32 v67, v62
	v_pk_fma_f32 v[114:115], v[172:173], v[138:139], v[114:115] op_sel_hi:[0,1,1]
	v_mov_b32_e32 v116, v173
	v_pk_fma_f32 v[114:115], v[116:117], v[128:129], v[114:115] op_sel_hi:[0,1,1]
	ds_read_b128 v[224:227], v238 offset:32960
	v_mov_b32_e32 v62, v125
	v_mov_b32_e32 v64, v126
	v_mov_b32_e32 v65, v60
	v_mov_b32_e32 v60, v127
	s_waitcnt lgkmcnt(8)
	v_pk_fma_f32 v[120:121], v[136:137], v[174:175], 0 op_sel_hi:[1,0,0]
	s_nop 0
	v_pk_fma_f32 v[116:117], v[174:175], v[130:131], v[120:121] op_sel:[1,0,0]
	s_nop 0
	v_pk_fma_f32 v[116:117], v[176:177], v[138:139], v[116:117] op_sel_hi:[0,1,1]
	v_mov_b32_e32 v118, v177
	v_pk_fma_f32 v[116:117], v[118:119], v[128:129], v[116:117] op_sel_hi:[0,1,1]
	ds_read_b128 v[228:231], v238 offset:41168
	s_waitcnt lgkmcnt(8)
	v_pk_fma_f32 v[122:123], v[136:137], v[178:179], 0 op_sel_hi:[1,0,0]
	s_nop 0
	v_pk_fma_f32 v[118:119], v[178:179], v[130:131], v[122:123] op_sel:[1,0,0]
	s_nop 0
	v_pk_fma_f32 v[118:119], v[180:181], v[138:139], v[118:119] op_sel_hi:[0,1,1]
	v_mov_b32_e32 v120, v181
	v_pk_fma_f32 v[118:119], v[120:121], v[128:129], v[118:119] op_sel_hi:[0,1,1]
	ds_read_b128 v[232:235], v238 offset:49376
	s_waitcnt lgkmcnt(8)
	v_pk_fma_f32 v[124:125], v[136:137], v[182:183], 0 op_sel_hi:[1,0,0]
	s_nop 0
	v_pk_fma_f32 v[120:121], v[182:183], v[130:131], v[124:125] op_sel:[1,0,0]
	s_nop 0
	v_pk_fma_f32 v[120:121], v[184:185], v[138:139], v[120:121] op_sel_hi:[0,1,1]
	v_mov_b32_e32 v122, v185
	v_pk_fma_f32 v[120:121], v[122:123], v[128:129], v[120:121] op_sel_hi:[0,1,1]
	ds_read_b128 v[242:245], v238 offset:57584
	s_waitcnt lgkmcnt(8)
	v_pk_fma_f32 v[126:127], v[136:137], v[186:187], 0 op_sel_hi:[1,0,0]
	s_nop 0
	v_pk_fma_f32 v[122:123], v[186:187], v[130:131], v[126:127] op_sel:[1,0,0]
	s_nop 0
	v_pk_fma_f32 v[122:123], v[188:189], v[138:139], v[122:123] op_sel_hi:[0,1,1]
	v_mov_b32_e32 v124, v189
	v_pk_fma_f32 v[122:123], v[124:125], v[128:129], v[122:123] op_sel_hi:[0,1,1]
	ds_read_b128 v[246:249], v25 offset:1024
	s_waitcnt lgkmcnt(8)
	v_pk_fma_f32 v[140:141], v[136:137], v[198:199], 0 op_sel_hi:[1,0,0]
	s_nop 0
	v_pk_fma_f32 v[124:125], v[198:199], v[130:131], v[140:141] op_sel:[1,0,0]
	ds_read_b128 v[250:253], v25 offset:9232
	v_pk_fma_f32 v[124:125], v[200:201], v[138:139], v[124:125] op_sel_hi:[0,1,1]
	v_mov_b32_e32 v126, v201
	v_pk_fma_f32 v[124:125], v[126:127], v[128:129], v[124:125] op_sel_hi:[0,1,1]
	s_waitcnt lgkmcnt(8)
	v_pk_fma_f32 v[126:127], v[136:137], v[202:203], 0 op_sel_hi:[1,0,0]
	s_nop 0
	v_pk_fma_f32 v[126:127], v[202:203], v[130:131], v[126:127] op_sel:[1,0,0]
	v_mov_b32_e32 v140, v205
	v_pk_fma_f32 v[126:127], v[204:205], v[138:139], v[126:127] op_sel_hi:[0,1,1]
	v_pk_fma_f32 v[126:127], v[140:141], v[128:129], v[126:127] op_sel_hi:[0,1,1]
	ds_read_b128 v[158:161], v25 offset:17440
	s_waitcnt lgkmcnt(8)
	v_pk_fma_f32 v[144:145], v[136:137], v[216:217], 0 op_sel_hi:[1,0,0]
	s_nop 0
	v_pk_fma_f32 v[140:141], v[216:217], v[130:131], v[144:145] op_sel:[1,0,0]
	s_nop 0
	v_pk_fma_f32 v[140:141], v[218:219], v[138:139], v[140:141] op_sel_hi:[0,1,1]
	v_mov_b32_e32 v142, v219
	v_pk_fma_f32 v[140:141], v[142:143], v[128:129], v[140:141] op_sel_hi:[0,1,1]
	ds_read_b128 v[162:165], v25 offset:25648
	s_waitcnt lgkmcnt(8)
	v_pk_fma_f32 v[146:147], v[136:137], v[220:221], 0 op_sel_hi:[1,0,0]
	s_nop 0
	v_pk_fma_f32 v[142:143], v[220:221], v[130:131], v[146:147] op_sel:[1,0,0]
	s_nop 0
	v_pk_fma_f32 v[142:143], v[222:223], v[138:139], v[142:143] op_sel_hi:[0,1,1]
	v_mov_b32_e32 v144, v223
	v_pk_fma_f32 v[142:143], v[144:145], v[128:129], v[142:143] op_sel_hi:[0,1,1]
	ds_read_b128 v[166:169], v25 offset:33856
	s_waitcnt lgkmcnt(8)
	v_pk_fma_f32 v[148:149], v[136:137], v[224:225], 0 op_sel_hi:[1,0,0]
	s_nop 0
	v_pk_fma_f32 v[144:145], v[224:225], v[130:131], v[148:149] op_sel:[1,0,0]
	s_nop 0
	v_pk_fma_f32 v[144:145], v[226:227], v[138:139], v[144:145] op_sel_hi:[0,1,1]
	v_mov_b32_e32 v146, v227
	v_pk_fma_f32 v[144:145], v[146:147], v[128:129], v[144:145] op_sel_hi:[0,1,1]
	ds_read_b128 v[170:173], v25 offset:42064
	s_waitcnt lgkmcnt(8)
	v_pk_fma_f32 v[150:151], v[136:137], v[228:229], 0 op_sel_hi:[1,0,0]
	s_nop 0
	v_pk_fma_f32 v[146:147], v[228:229], v[130:131], v[150:151] op_sel:[1,0,0]
	s_nop 0
	v_pk_fma_f32 v[146:147], v[230:231], v[138:139], v[146:147] op_sel_hi:[0,1,1]
	v_mov_b32_e32 v148, v231
	v_pk_fma_f32 v[146:147], v[148:149], v[128:129], v[146:147] op_sel_hi:[0,1,1]
	ds_read_b128 v[174:177], v25 offset:50272
	s_waitcnt lgkmcnt(8)
	v_pk_fma_f32 v[194:195], v[136:137], v[232:233], 0 op_sel_hi:[1,0,0]
	s_nop 0
	v_pk_fma_f32 v[148:149], v[232:233], v[130:131], v[194:195] op_sel:[1,0,0]
	ds_read_b128 v[178:181], v25 offset:58480
	v_pk_fma_f32 v[148:149], v[234:235], v[138:139], v[148:149] op_sel_hi:[0,1,1]
	v_mov_b32_e32 v150, v235
	v_pk_fma_f32 v[148:149], v[150:151], v[128:129], v[148:149] op_sel_hi:[0,1,1]
	s_waitcnt lgkmcnt(8)
	v_pk_fma_f32 v[136:137], v[136:137], v[242:243], 0 op_sel_hi:[1,0,0]
	s_nop 0
	v_pk_fma_f32 v[130:131], v[242:243], v[130:131], v[136:137] op_sel:[1,0,0]
	v_mov_b32_e32 v136, v245
	v_pk_fma_f32 v[130:131], v[244:245], v[138:139], v[130:131] op_sel_hi:[0,1,1]
	v_pk_fma_f32 v[150:151], v[136:137], v[128:129], v[130:131] op_sel_hi:[0,1,1]
	ds_read_b128 v[182:185], v238 offset:1152
	s_waitcnt lgkmcnt(8)
; #define LAS __attribute__((address_space(3)))
; __global__ void __launch_bounds__(NTHREADS, 2) hybrid_fwd(Args a) {
;     ...
;                     for (int j = 0; j < 8; ++j) {
; #pragma unroll
;                         for (int e = 0; e < 16; ++e) { const f32x4 w = *(const LAS f32x4*)(rwT + e * 2052 + j * 256 + lane * 4);
;                             acc2[e] += y2[j][0] * (f32x2){w[0], w[0]}; acc2[e] += y2[j][1] * (f32x2){w[1], w[1]};
;                             acc2[e] += y2[j][2] * (f32x2){w[2], w[2]}; acc2[e] += y2[j][3] * (f32x2){w[3], w[3]}; }
;                         __builtin_amdgcn_sched_barrier(0);
;                     }
	v_pk_fma_f32 v[112:113], v[132:133], v[246:247], v[112:113] op_sel_hi:[1,0,1]
	s_nop 0
	v_pk_fma_f32 v[112:113], v[246:247], v[106:107], v[112:113] op_sel:[1,0,0]
	v_mov_b32_e32 v128, v249
	v_pk_fma_f32 v[112:113], v[248:249], v[134:135], v[112:113] op_sel_hi:[0,1,1]
	v_pk_fma_f32 v[112:113], v[128:129], v[104:105], v[112:113] op_sel_hi:[0,1,1]
	ds_read_b128 v[186:189], v238 offset:9360
	s_waitcnt lgkmcnt(8)
	v_pk_fma_f32 v[136:137], v[132:133], v[250:251], v[152:153] op_sel_hi:[1,0,1]
	s_nop 0
	v_pk_fma_f32 v[128:129], v[250:251], v[106:107], v[136:137] op_sel:[1,0,0]
	s_nop 0
	v_pk_fma_f32 v[128:129], v[252:253], v[134:135], v[128:129] op_sel_hi:[0,1,1]
	v_mov_b32_e32 v130, v253
	v_pk_fma_f32 v[152:153], v[130:131], v[104:105], v[128:129] op_sel_hi:[0,1,1]
	ds_read_b128 v[198:201], v238 offset:17568
	s_waitcnt lgkmcnt(8)
	v_pk_fma_f32 v[136:137], v[132:133], v[158:159], v[154:155] op_sel_hi:[1,0,1]
	s_nop 0
	v_pk_fma_f32 v[128:129], v[158:159], v[106:107], v[136:137] op_sel:[1,0,0]
	ds_read_b128 v[202:205], v238 offset:25776
	v_pk_fma_f32 v[128:129], v[160:161], v[134:135], v[128:129] op_sel_hi:[0,1,1]
	v_mov_b32_e32 v130, v161
	v_pk_fma_f32 v[128:129], v[130:131], v[104:105], v[128:129] op_sel_hi:[0,1,1]
	s_waitcnt lgkmcnt(8)
	v_pk_fma_f32 v[114:115], v[132:133], v[162:163], v[114:115] op_sel_hi:[1,0,1]
	s_nop 0
	v_pk_fma_f32 v[114:115], v[162:163], v[106:107], v[114:115] op_sel:[1,0,0]
	v_mov_b32_e32 v130, v165
	v_pk_fma_f32 v[114:115], v[164:165], v[134:135], v[114:115] op_sel_hi:[0,1,1]
	ds_read_b128 v[216:219], v238 offset:33984
	v_pk_fma_f32 v[114:115], v[130:131], v[104:105], v[114:115] op_sel_hi:[0,1,1]
	s_waitcnt lgkmcnt(8)
	v_pk_fma_f32 v[116:117], v[132:133], v[166:167], v[116:117] op_sel_hi:[1,0,1]
	s_nop 0
	v_pk_fma_f32 v[116:117], v[166:167], v[106:107], v[116:117] op_sel:[1,0,0]
	v_mov_b32_e32 v130, v169
	v_pk_fma_f32 v[116:117], v[168:169], v[134:135], v[116:117] op_sel_hi:[0,1,1]
	ds_read_b128 v[220:223], v238 offset:42192
	v_pk_fma_f32 v[116:117], v[130:131], v[104:105], v[116:117] op_sel_hi:[0,1,1]
	s_waitcnt lgkmcnt(8)
	v_pk_fma_f32 v[118:119], v[132:133], v[170:171], v[118:119] op_sel_hi:[1,0,1]
	s_nop 0
	v_pk_fma_f32 v[118:119], v[170:171], v[106:107], v[118:119] op_sel:[1,0,0]
	v_mov_b32_e32 v130, v173
	v_pk_fma_f32 v[118:119], v[172:173], v[134:135], v[118:119] op_sel_hi:[0,1,1]
	ds_read_b128 v[224:227], v238 offset:50400
	v_pk_fma_f32 v[118:119], v[130:131], v[104:105], v[118:119] op_sel_hi:[0,1,1]
	s_waitcnt lgkmcnt(8)
	v_pk_fma_f32 v[120:121], v[132:133], v[174:175], v[120:121] op_sel_hi:[1,0,1]
	s_nop 0
	v_pk_fma_f32 v[120:121], v[174:175], v[106:107], v[120:121] op_sel:[1,0,0]
	v_mov_b32_e32 v130, v177
	v_pk_fma_f32 v[120:121], v[176:177], v[134:135], v[120:121] op_sel_hi:[0,1,1]
	ds_read_b128 v[228:231], v238 offset:58608
	v_pk_fma_f32 v[120:121], v[130:131], v[104:105], v[120:121] op_sel_hi:[0,1,1]
	s_waitcnt lgkmcnt(8)
	v_pk_fma_f32 v[122:123], v[132:133], v[178:179], v[122:123] op_sel_hi:[1,0,1]
	s_nop 0
	v_pk_fma_f32 v[122:123], v[178:179], v[106:107], v[122:123] op_sel:[1,0,0]
	v_mov_b32_e32 v130, v181
	v_pk_fma_f32 v[122:123], v[180:181], v[134:135], v[122:123] op_sel_hi:[0,1,1]
	ds_read_b128 v[232:235], v25 offset:2048
	v_pk_fma_f32 v[122:123], v[130:131], v[104:105], v[122:123] op_sel_hi:[0,1,1]
	s_waitcnt lgkmcnt(8)
	v_pk_fma_f32 v[124:125], v[132:133], v[182:183], v[124:125] op_sel_hi:[1,0,1]
	s_nop 0
	v_pk_fma_f32 v[124:125], v[182:183], v[106:107], v[124:125] op_sel:[1,0,0]
	v_mov_b32_e32 v130, v185
	v_pk_fma_f32 v[124:125], v[184:185], v[134:135], v[124:125] op_sel_hi:[0,1,1]
	ds_read_b128 v[242:245], v25 offset:10256
	v_pk_fma_f32 v[124:125], v[130:131], v[104:105], v[124:125] op_sel_hi:[0,1,1]
	s_waitcnt lgkmcnt(8)
	v_pk_fma_f32 v[126:127], v[132:133], v[186:187], v[126:127] op_sel_hi:[1,0,1]
	s_nop 0
	v_pk_fma_f32 v[126:127], v[186:187], v[106:107], v[126:127] op_sel:[1,0,0]
	v_mov_b32_e32 v130, v189
	v_pk_fma_f32 v[126:127], v[188:189], v[134:135], v[126:127] op_sel_hi:[0,1,1]
	ds_read_b128 v[246:249], v25 offset:18464
	v_pk_fma_f32 v[126:127], v[130:131], v[104:105], v[126:127] op_sel_hi:[0,1,1]
	s_waitcnt lgkmcnt(8)
	v_pk_fma_f32 v[130:131], v[132:133], v[198:199], v[140:141] op_sel_hi:[1,0,1]
	s_nop 0
	v_pk_fma_f32 v[130:131], v[198:199], v[106:107], v[130:131] op_sel:[1,0,0]
	v_mov_b32_e32 v136, v201
	v_pk_fma_f32 v[130:131], v[200:201], v[134:135], v[130:131] op_sel_hi:[0,1,1]
	v_pk_fma_f32 v[130:131], v[136:137], v[104:105], v[130:131] op_sel_hi:[0,1,1]
	ds_read_b128 v[250:253], v25 offset:26672
	s_waitcnt lgkmcnt(8)
	v_pk_fma_f32 v[140:141], v[132:133], v[202:203], v[142:143] op_sel_hi:[1,0,1]
	s_nop 0
	v_pk_fma_f32 v[136:137], v[202:203], v[106:107], v[140:141] op_sel:[1,0,0]
	s_nop 0
	v_pk_fma_f32 v[136:137], v[204:205], v[134:135], v[136:137] op_sel_hi:[0,1,1]
	v_mov_b32_e32 v138, v205
	v_pk_fma_f32 v[136:137], v[138:139], v[104:105], v[136:137] op_sel_hi:[0,1,1]
	ds_read_b128 v[162:165], v25 offset:34880
	s_waitcnt lgkmcnt(8)
	v_pk_fma_f32 v[142:143], v[132:133], v[216:217], v[144:145] op_sel_hi:[1,0,1]
	s_nop 0
	v_pk_fma_f32 v[138:139], v[216:217], v[106:107], v[142:143] op_sel:[1,0,0]
	s_nop 0
	v_pk_fma_f32 v[138:139], v[218:219], v[134:135], v[138:139] op_sel_hi:[0,1,1]
	v_mov_b32_e32 v140, v219
	v_pk_fma_f32 v[138:139], v[140:141], v[104:105], v[138:139] op_sel_hi:[0,1,1]
	ds_read_b128 v[166:169], v25 offset:43088
	s_waitcnt lgkmcnt(8)
	v_pk_fma_f32 v[144:145], v[132:133], v[220:221], v[146:147] op_sel_hi:[1,0,1]
	s_nop 0
	v_pk_fma_f32 v[140:141], v[220:221], v[106:107], v[144:145] op_sel:[1,0,0]
	s_nop 0
	v_pk_fma_f32 v[140:141], v[222:223], v[134:135], v[140:141] op_sel_hi:[0,1,1]
	v_mov_b32_e32 v142, v223
	v_pk_fma_f32 v[140:141], v[142:143], v[104:105], v[140:141] op_sel_hi:[0,1,1]
	ds_read_b128 v[170:173], v25 offset:51296
	s_waitcnt lgkmcnt(8)
; #define LAS __attribute__((address_space(3)))
; __global__ void __launch_bounds__(NTHREADS, 2) hybrid_fwd(Args a) {
;     ...
;                     for (int j = 0; j < 8; ++j) {
; #pragma unroll
;                         for (int e = 0; e < 16; ++e) { const f32x4 w = *(const LAS f32x4*)(rwT + e * 2052 + j * 256 + lane * 4);
;                             acc2[e] += y2[j][0] * (f32x2){w[0], w[0]}; acc2[e] += y2[j][1] * (f32x2){w[1], w[1]};
;                             acc2[e] += y2[j][2] * (f32x2){w[2], w[2]}; acc2[e] += y2[j][3] * (f32x2){w[3], w[3]}; }
;                         __builtin_amdgcn_sched_barrier(0);
;                     }
	v_pk_fma_f32 v[146:147], v[132:133], v[224:225], v[148:149] op_sel_hi:[1,0,1]
	s_nop 0
	v_pk_fma_f32 v[142:143], v[224:225], v[106:107], v[146:147] op_sel:[1,0,0]
	s_nop 0
	v_pk_fma_f32 v[142:143], v[226:227], v[134:135], v[142:143] op_sel_hi:[0,1,1]
	v_mov_b32_e32 v144, v227
	v_pk_fma_f32 v[142:143], v[144:145], v[104:105], v[142:143] op_sel_hi:[0,1,1]
	ds_read_b128 v[174:177], v25 offset:59504
	s_waitcnt lgkmcnt(8)
	v_pk_fma_f32 v[132:133], v[132:133], v[228:229], v[150:151] op_sel_hi:[1,0,1]
	s_nop 0
	v_pk_fma_f32 v[106:107], v[228:229], v[106:107], v[132:133] op_sel:[1,0,0]
	v_mov_b32_e32 v132, v231
	v_pk_fma_f32 v[106:107], v[230:231], v[134:135], v[106:107] op_sel_hi:[0,1,1]
	v_pk_fma_f32 v[144:145], v[132:133], v[104:105], v[106:107] op_sel_hi:[0,1,1]
	ds_read_b128 v[178:181], v238 offset:2176
	ds_read_b128 v[182:185], v238 offset:10384
	s_waitcnt lgkmcnt(8)
	v_pk_fma_f32 v[112:113], v[108:109], v[232:233], v[112:113] op_sel_hi:[1,0,1]
	s_nop 0
	v_pk_fma_f32 v[104:105], v[232:233], v[98:99], v[112:113] op_sel:[1,0,0]
	v_mov_b32_e32 v112, v245
	v_pk_fma_f32 v[104:105], v[234:235], v[110:111], v[104:105] op_sel_hi:[0,1,1]
	v_mov_b32_e32 v106, v235
	v_pk_fma_f32 v[104:105], v[106:107], v[96:97], v[104:105] op_sel_hi:[0,1,1]
	v_pk_fma_f32 v[106:107], v[108:109], v[242:243], v[152:153] op_sel_hi:[1,0,1]
	s_nop 0
	v_pk_fma_f32 v[106:107], v[242:243], v[98:99], v[106:107] op_sel:[1,0,0]
	s_nop 0
	v_pk_fma_f32 v[106:107], v[244:245], v[110:111], v[106:107] op_sel_hi:[0,1,1]
	ds_read_b128 v[186:189], v238 offset:18592
	v_pk_fma_f32 v[146:147], v[112:113], v[96:97], v[106:107] op_sel_hi:[0,1,1]
	s_waitcnt lgkmcnt(8)
	v_pk_fma_f32 v[106:107], v[108:109], v[246:247], v[128:129] op_sel_hi:[1,0,1]
	s_nop 0
	v_pk_fma_f32 v[106:107], v[246:247], v[98:99], v[106:107] op_sel:[1,0,0]
	v_mov_b32_e32 v112, v249
	v_pk_fma_f32 v[106:107], v[248:249], v[110:111], v[106:107] op_sel_hi:[0,1,1]
	ds_read_b128 v[158:161], v238 offset:26800
	v_pk_fma_f32 v[106:107], v[112:113], v[96:97], v[106:107] op_sel_hi:[0,1,1]
	s_waitcnt lgkmcnt(8)
	v_pk_fma_f32 v[112:113], v[108:109], v[250:251], v[114:115] op_sel_hi:[1,0,1]
	s_nop 0
	v_pk_fma_f32 v[112:113], v[250:251], v[98:99], v[112:113] op_sel:[1,0,0]
	v_mov_b32_e32 v114, v253
	v_pk_fma_f32 v[112:113], v[252:253], v[110:111], v[112:113] op_sel_hi:[0,1,1]
	ds_read_b128 v[198:201], v238 offset:35008
	v_pk_fma_f32 v[112:113], v[114:115], v[96:97], v[112:113] op_sel_hi:[0,1,1]
	s_waitcnt lgkmcnt(8)
	v_pk_fma_f32 v[114:115], v[108:109], v[162:163], v[116:117] op_sel_hi:[1,0,1]
	s_nop 0
	v_pk_fma_f32 v[114:115], v[162:163], v[98:99], v[114:115] op_sel:[1,0,0]
	v_mov_b32_e32 v116, v165
	v_pk_fma_f32 v[114:115], v[164:165], v[110:111], v[114:115] op_sel_hi:[0,1,1]
	ds_read_b128 v[202:205], v238 offset:43216
	v_pk_fma_f32 v[114:115], v[116:117], v[96:97], v[114:115] op_sel_hi:[0,1,1]
	s_waitcnt lgkmcnt(8)
	v_pk_fma_f32 v[116:117], v[108:109], v[166:167], v[118:119] op_sel_hi:[1,0,1]
	s_nop 0
	v_pk_fma_f32 v[116:117], v[166:167], v[98:99], v[116:117] op_sel:[1,0,0]
	v_mov_b32_e32 v118, v169
	v_pk_fma_f32 v[116:117], v[168:169], v[110:111], v[116:117] op_sel_hi:[0,1,1]
	ds_read_b128 v[216:219], v238 offset:51424
	v_pk_fma_f32 v[116:117], v[118:119], v[96:97], v[116:117] op_sel_hi:[0,1,1]
	s_waitcnt lgkmcnt(8)
	v_pk_fma_f32 v[118:119], v[108:109], v[170:171], v[120:121] op_sel_hi:[1,0,1]
	s_nop 0
	v_pk_fma_f32 v[118:119], v[170:171], v[98:99], v[118:119] op_sel:[1,0,0]
	v_mov_b32_e32 v120, v173
	v_pk_fma_f32 v[118:119], v[172:173], v[110:111], v[118:119] op_sel_hi:[0,1,1]
	ds_read_b128 v[220:223], v238 offset:59632
	v_pk_fma_f32 v[118:119], v[120:121], v[96:97], v[118:119] op_sel_hi:[0,1,1]
	s_waitcnt lgkmcnt(8)
	v_pk_fma_f32 v[120:121], v[108:109], v[174:175], v[122:123] op_sel_hi:[1,0,1]
	s_nop 0
	v_pk_fma_f32 v[120:121], v[174:175], v[98:99], v[120:121] op_sel:[1,0,0]
	v_mov_b32_e32 v122, v177
	v_pk_fma_f32 v[120:121], v[176:177], v[110:111], v[120:121] op_sel_hi:[0,1,1]
	ds_read_b128 v[224:227], v25 offset:3072
	v_pk_fma_f32 v[120:121], v[122:123], v[96:97], v[120:121] op_sel_hi:[0,1,1]
	s_waitcnt lgkmcnt(8)
	v_pk_fma_f32 v[122:123], v[108:109], v[178:179], v[124:125] op_sel_hi:[1,0,1]
	s_nop 0
	v_pk_fma_f32 v[122:123], v[178:179], v[98:99], v[122:123] op_sel:[1,0,0]
	v_mov_b32_e32 v124, v181
	v_pk_fma_f32 v[122:123], v[180:181], v[110:111], v[122:123] op_sel_hi:[0,1,1]
	ds_read_b128 v[228:231], v25 offset:11280
	v_pk_fma_f32 v[122:123], v[124:125], v[96:97], v[122:123] op_sel_hi:[0,1,1]
	s_waitcnt lgkmcnt(8)
	v_pk_fma_f32 v[124:125], v[108:109], v[182:183], v[126:127] op_sel_hi:[1,0,1]
	s_nop 0
	v_pk_fma_f32 v[124:125], v[182:183], v[98:99], v[124:125] op_sel:[1,0,0]
	v_mov_b32_e32 v126, v185
	v_pk_fma_f32 v[124:125], v[184:185], v[110:111], v[124:125] op_sel_hi:[0,1,1]
	v_pk_fma_f32 v[124:125], v[126:127], v[96:97], v[124:125] op_sel_hi:[0,1,1]
	ds_read_b128 v[232:235], v25 offset:19488
	s_waitcnt lgkmcnt(8)
	v_pk_fma_f32 v[130:131], v[108:109], v[186:187], v[130:131] op_sel_hi:[1,0,1]
	s_nop 0
	v_pk_fma_f32 v[126:127], v[186:187], v[98:99], v[130:131] op_sel:[1,0,0]
	s_nop 0
	v_pk_fma_f32 v[126:127], v[188:189], v[110:111], v[126:127] op_sel_hi:[0,1,1]
	v_mov_b32_e32 v128, v189
	v_pk_fma_f32 v[126:127], v[128:129], v[96:97], v[126:127] op_sel_hi:[0,1,1]
	ds_read_b128 v[242:245], v25 offset:27696
	s_waitcnt lgkmcnt(8)
	v_pk_fma_f32 v[132:133], v[108:109], v[158:159], v[136:137] op_sel_hi:[1,0,1]
	s_nop 0
	v_pk_fma_f32 v[128:129], v[158:159], v[98:99], v[132:133] op_sel:[1,0,0]
	s_nop 0
	v_pk_fma_f32 v[128:129], v[160:161], v[110:111], v[128:129] op_sel_hi:[0,1,1]
	v_mov_b32_e32 v130, v161
	v_pk_fma_f32 v[128:129], v[130:131], v[96:97], v[128:129] op_sel_hi:[0,1,1]
	ds_read_b128 v[246:249], v25 offset:35904
	s_waitcnt lgkmcnt(8)
; #define LAS __attribute__((address_space(3)))
; __global__ void __launch_bounds__(NTHREADS, 2) hybrid_fwd(Args a) {
;     ...
;                     for (int j = 0; j < 8; ++j) {
; #pragma unroll
;                         for (int e = 0; e < 16; ++e) { const f32x4 w = *(const LAS f32x4*)(rwT + e * 2052 + j * 256 + lane * 4);
;                             acc2[e] += y2[j][0] * (f32x2){w[0], w[0]}; acc2[e] += y2[j][1] * (f32x2){w[1], w[1]};
;                             acc2[e] += y2[j][2] * (f32x2){w[2], w[2]}; acc2[e] += y2[j][3] * (f32x2){w[3], w[3]}; }
;                         __builtin_amdgcn_sched_barrier(0);
;                     }
	v_pk_fma_f32 v[134:135], v[108:109], v[198:199], v[138:139] op_sel_hi:[1,0,1]
	s_nop 0
	v_pk_fma_f32 v[130:131], v[198:199], v[98:99], v[134:135] op_sel:[1,0,0]
	s_nop 0
	v_pk_fma_f32 v[130:131], v[200:201], v[110:111], v[130:131] op_sel_hi:[0,1,1]
	v_mov_b32_e32 v132, v201
	v_pk_fma_f32 v[130:131], v[132:133], v[96:97], v[130:131] op_sel_hi:[0,1,1]
	ds_read_b128 v[250:253], v25 offset:44112
	s_waitcnt lgkmcnt(8)
	v_pk_fma_f32 v[136:137], v[108:109], v[202:203], v[140:141] op_sel_hi:[1,0,1]
	s_nop 0
	v_pk_fma_f32 v[132:133], v[202:203], v[98:99], v[136:137] op_sel:[1,0,0]
	s_nop 0
	v_pk_fma_f32 v[132:133], v[204:205], v[110:111], v[132:133] op_sel_hi:[0,1,1]
	v_mov_b32_e32 v134, v205
	v_pk_fma_f32 v[132:133], v[134:135], v[96:97], v[132:133] op_sel_hi:[0,1,1]
	ds_read_b128 v[162:165], v25 offset:52320
	s_waitcnt lgkmcnt(8)
	v_pk_fma_f32 v[138:139], v[108:109], v[216:217], v[142:143] op_sel_hi:[1,0,1]
	s_nop 0
	v_pk_fma_f32 v[134:135], v[216:217], v[98:99], v[138:139] op_sel:[1,0,0]
	s_nop 0
	v_pk_fma_f32 v[134:135], v[218:219], v[110:111], v[134:135] op_sel_hi:[0,1,1]
	v_mov_b32_e32 v136, v219
	v_pk_fma_f32 v[134:135], v[136:137], v[96:97], v[134:135] op_sel_hi:[0,1,1]
	ds_read_b128 v[166:169], v25 offset:60528
	s_waitcnt lgkmcnt(8)
	v_pk_fma_f32 v[108:109], v[108:109], v[220:221], v[144:145] op_sel_hi:[1,0,1]
	s_nop 0
	v_pk_fma_f32 v[98:99], v[220:221], v[98:99], v[108:109] op_sel:[1,0,0]
	v_mov_b32_e32 v108, v223
	v_pk_fma_f32 v[98:99], v[222:223], v[110:111], v[98:99] op_sel_hi:[0,1,1]
	v_pk_fma_f32 v[136:137], v[108:109], v[96:97], v[98:99] op_sel_hi:[0,1,1]
	ds_read_b128 v[170:173], v238 offset:3200
	ds_read_b128 v[174:177], v238 offset:11408
	s_waitcnt lgkmcnt(8)
	v_pk_fma_f32 v[104:105], v[100:101], v[224:225], v[104:105] op_sel_hi:[1,0,1]
	s_nop 0
	v_pk_fma_f32 v[96:97], v[224:225], v[90:91], v[104:105] op_sel:[1,0,0]
	v_mov_b32_e32 v104, v231
	v_pk_fma_f32 v[96:97], v[226:227], v[102:103], v[96:97] op_sel_hi:[0,1,1]
	v_mov_b32_e32 v98, v227
	v_pk_fma_f32 v[96:97], v[98:99], v[88:89], v[96:97] op_sel_hi:[0,1,1]
	v_pk_fma_f32 v[98:99], v[100:101], v[228:229], v[146:147] op_sel_hi:[1,0,1]
	s_nop 0
	v_pk_fma_f32 v[98:99], v[228:229], v[90:91], v[98:99] op_sel:[1,0,0]
	s_nop 0
	v_pk_fma_f32 v[98:99], v[230:231], v[102:103], v[98:99] op_sel_hi:[0,1,1]
	ds_read_b128 v[178:181], v238 offset:19616
	v_pk_fma_f32 v[138:139], v[104:105], v[88:89], v[98:99] op_sel_hi:[0,1,1]
	s_waitcnt lgkmcnt(8)
	v_pk_fma_f32 v[98:99], v[100:101], v[232:233], v[106:107] op_sel_hi:[1,0,1]
	s_nop 0
	v_pk_fma_f32 v[98:99], v[232:233], v[90:91], v[98:99] op_sel:[1,0,0]
	v_mov_b32_e32 v104, v235
	v_pk_fma_f32 v[98:99], v[234:235], v[102:103], v[98:99] op_sel_hi:[0,1,1]
	v_pk_fma_f32 v[98:99], v[104:105], v[88:89], v[98:99] op_sel_hi:[0,1,1]
	ds_read_b128 v[182:185], v238 offset:27824
	s_waitcnt lgkmcnt(8)
	v_pk_fma_f32 v[108:109], v[100:101], v[242:243], v[112:113] op_sel_hi:[1,0,1]
	s_nop 0
	v_pk_fma_f32 v[104:105], v[242:243], v[90:91], v[108:109] op_sel:[1,0,0]
	s_nop 0
	v_pk_fma_f32 v[104:105], v[244:245], v[102:103], v[104:105] op_sel_hi:[0,1,1]
	v_mov_b32_e32 v106, v245
	v_pk_fma_f32 v[104:105], v[106:107], v[88:89], v[104:105] op_sel_hi:[0,1,1]
	ds_read_b128 v[186:189], v238 offset:36032
	s_waitcnt lgkmcnt(8)
	v_pk_fma_f32 v[110:111], v[100:101], v[246:247], v[114:115] op_sel_hi:[1,0,1]
	s_nop 0
	v_pk_fma_f32 v[106:107], v[246:247], v[90:91], v[110:111] op_sel:[1,0,0]
	s_nop 0
	v_pk_fma_f32 v[106:107], v[248:249], v[102:103], v[106:107] op_sel_hi:[0,1,1]
	v_mov_b32_e32 v108, v249
	v_pk_fma_f32 v[106:107], v[108:109], v[88:89], v[106:107] op_sel_hi:[0,1,1]
	ds_read_b128 v[158:161], v238 offset:44240
	s_waitcnt lgkmcnt(8)
	v_pk_fma_f32 v[112:113], v[100:101], v[250:251], v[116:117] op_sel_hi:[1,0,1]
	s_nop 0
	v_pk_fma_f32 v[108:109], v[250:251], v[90:91], v[112:113] op_sel:[1,0,0]
	s_nop 0
	v_pk_fma_f32 v[108:109], v[252:253], v[102:103], v[108:109] op_sel_hi:[0,1,1]
	v_mov_b32_e32 v110, v253
	v_pk_fma_f32 v[108:109], v[110:111], v[88:89], v[108:109] op_sel_hi:[0,1,1]
	ds_read_b128 v[198:201], v238 offset:52448
	s_waitcnt lgkmcnt(8)
	v_pk_fma_f32 v[114:115], v[100:101], v[162:163], v[118:119] op_sel_hi:[1,0,1]
	s_nop 0
	v_pk_fma_f32 v[110:111], v[162:163], v[90:91], v[114:115] op_sel:[1,0,0]
	s_nop 0
	v_pk_fma_f32 v[110:111], v[164:165], v[102:103], v[110:111] op_sel_hi:[0,1,1]
	v_mov_b32_e32 v112, v165
	v_pk_fma_f32 v[110:111], v[112:113], v[88:89], v[110:111] op_sel_hi:[0,1,1]
	ds_read_b128 v[202:205], v238 offset:60656
	s_waitcnt lgkmcnt(8)
	v_pk_fma_f32 v[116:117], v[100:101], v[166:167], v[120:121] op_sel_hi:[1,0,1]
	s_nop 0
	v_pk_fma_f32 v[112:113], v[166:167], v[90:91], v[116:117] op_sel:[1,0,0]
	s_nop 0
	v_pk_fma_f32 v[112:113], v[168:169], v[102:103], v[112:113] op_sel_hi:[0,1,1]
	v_mov_b32_e32 v114, v169
	v_pk_fma_f32 v[112:113], v[114:115], v[88:89], v[112:113] op_sel_hi:[0,1,1]
	ds_read_b128 v[216:219], v25 offset:4096
	s_waitcnt lgkmcnt(8)
	v_pk_fma_f32 v[118:119], v[100:101], v[170:171], v[122:123] op_sel_hi:[1,0,1]
	s_nop 0
	v_pk_fma_f32 v[114:115], v[170:171], v[90:91], v[118:119] op_sel:[1,0,0]
	s_nop 0
	v_pk_fma_f32 v[114:115], v[172:173], v[102:103], v[114:115] op_sel_hi:[0,1,1]
	v_mov_b32_e32 v116, v173
	v_pk_fma_f32 v[114:115], v[116:117], v[88:89], v[114:115] op_sel_hi:[0,1,1]
	ds_read_b128 v[220:223], v25 offset:12304
	s_waitcnt lgkmcnt(8)
	v_pk_fma_f32 v[120:121], v[100:101], v[174:175], v[124:125] op_sel_hi:[1,0,1]
	s_nop 0
	v_pk_fma_f32 v[116:117], v[174:175], v[90:91], v[120:121] op_sel:[1,0,0]
	s_nop 0
	v_pk_fma_f32 v[116:117], v[176:177], v[102:103], v[116:117] op_sel_hi:[0,1,1]
	v_mov_b32_e32 v118, v177
	v_pk_fma_f32 v[116:117], v[118:119], v[88:89], v[116:117] op_sel_hi:[0,1,1]
	ds_read_b128 v[224:227], v25 offset:20512
	s_waitcnt lgkmcnt(8)
; #define LAS __attribute__((address_space(3)))
; __global__ void __launch_bounds__(NTHREADS, 2) hybrid_fwd(Args a) {
;     ...
;                     for (int j = 0; j < 8; ++j) {
; #pragma unroll
;                         for (int e = 0; e < 16; ++e) { const f32x4 w = *(const LAS f32x4*)(rwT + e * 2052 + j * 256 + lane * 4);
;                             acc2[e] += y2[j][0] * (f32x2){w[0], w[0]}; acc2[e] += y2[j][1] * (f32x2){w[1], w[1]};
;                             acc2[e] += y2[j][2] * (f32x2){w[2], w[2]}; acc2[e] += y2[j][3] * (f32x2){w[3], w[3]}; }
;                         __builtin_amdgcn_sched_barrier(0);
;                     }
	v_pk_fma_f32 v[122:123], v[100:101], v[178:179], v[126:127] op_sel_hi:[1,0,1]
	s_nop 0
	v_pk_fma_f32 v[118:119], v[178:179], v[90:91], v[122:123] op_sel:[1,0,0]
	s_nop 0
	v_pk_fma_f32 v[118:119], v[180:181], v[102:103], v[118:119] op_sel_hi:[0,1,1]
	v_mov_b32_e32 v120, v181
	v_pk_fma_f32 v[118:119], v[120:121], v[88:89], v[118:119] op_sel_hi:[0,1,1]
	ds_read_b128 v[228:231], v25 offset:28720
	s_waitcnt lgkmcnt(8)
	v_pk_fma_f32 v[124:125], v[100:101], v[182:183], v[128:129] op_sel_hi:[1,0,1]
	s_nop 0
	v_pk_fma_f32 v[120:121], v[182:183], v[90:91], v[124:125] op_sel:[1,0,0]
	s_nop 0
	v_pk_fma_f32 v[120:121], v[184:185], v[102:103], v[120:121] op_sel_hi:[0,1,1]
	v_mov_b32_e32 v122, v185
	v_pk_fma_f32 v[120:121], v[122:123], v[88:89], v[120:121] op_sel_hi:[0,1,1]
	ds_read_b128 v[232:235], v25 offset:36928
	s_waitcnt lgkmcnt(8)
	v_pk_fma_f32 v[126:127], v[100:101], v[186:187], v[130:131] op_sel_hi:[1,0,1]
	s_nop 0
	v_pk_fma_f32 v[122:123], v[186:187], v[90:91], v[126:127] op_sel:[1,0,0]
	s_nop 0
	v_pk_fma_f32 v[122:123], v[188:189], v[102:103], v[122:123] op_sel_hi:[0,1,1]
	v_mov_b32_e32 v124, v189
	v_pk_fma_f32 v[122:123], v[124:125], v[88:89], v[122:123] op_sel_hi:[0,1,1]
	ds_read_b128 v[242:245], v25 offset:45136
	s_waitcnt lgkmcnt(8)
	v_pk_fma_f32 v[128:129], v[100:101], v[158:159], v[132:133] op_sel_hi:[1,0,1]
	s_nop 0
	v_pk_fma_f32 v[124:125], v[158:159], v[90:91], v[128:129] op_sel:[1,0,0]
	s_nop 0
	v_pk_fma_f32 v[124:125], v[160:161], v[102:103], v[124:125] op_sel_hi:[0,1,1]
	v_mov_b32_e32 v126, v161
	v_pk_fma_f32 v[124:125], v[126:127], v[88:89], v[124:125] op_sel_hi:[0,1,1]
	ds_read_b128 v[246:249], v25 offset:53344
	s_waitcnt lgkmcnt(8)
	v_pk_fma_f32 v[130:131], v[100:101], v[198:199], v[134:135] op_sel_hi:[1,0,1]
	s_nop 0
	v_pk_fma_f32 v[126:127], v[198:199], v[90:91], v[130:131] op_sel:[1,0,0]
	s_nop 0
	v_pk_fma_f32 v[126:127], v[200:201], v[102:103], v[126:127] op_sel_hi:[0,1,1]
	v_mov_b32_e32 v128, v201
	v_pk_fma_f32 v[126:127], v[128:129], v[88:89], v[126:127] op_sel_hi:[0,1,1]
	ds_read_b128 v[250:253], v25 offset:61552
	s_waitcnt lgkmcnt(8)
	v_pk_fma_f32 v[100:101], v[100:101], v[202:203], v[136:137] op_sel_hi:[1,0,1]
	s_nop 0
	v_pk_fma_f32 v[90:91], v[202:203], v[90:91], v[100:101] op_sel:[1,0,0]
	v_mov_b32_e32 v100, v205
	v_pk_fma_f32 v[90:91], v[204:205], v[102:103], v[90:91] op_sel_hi:[0,1,1]
	v_pk_fma_f32 v[128:129], v[100:101], v[88:89], v[90:91] op_sel_hi:[0,1,1]
	ds_read_b128 v[162:165], v238 offset:4224
	ds_read_b128 v[166:169], v238 offset:12432
	s_waitcnt lgkmcnt(8)
	v_pk_fma_f32 v[96:97], v[92:93], v[216:217], v[96:97] op_sel_hi:[1,0,1]
	s_nop 0
	v_pk_fma_f32 v[88:89], v[216:217], v[86:87], v[96:97] op_sel:[1,0,0]
	v_mov_b32_e32 v96, v223
	v_pk_fma_f32 v[88:89], v[218:219], v[94:95], v[88:89] op_sel_hi:[0,1,1]
	v_mov_b32_e32 v90, v219
	v_pk_fma_f32 v[88:89], v[90:91], v[84:85], v[88:89] op_sel_hi:[0,1,1]
	v_pk_fma_f32 v[90:91], v[92:93], v[220:221], v[138:139] op_sel_hi:[1,0,1]
	s_nop 0
	v_pk_fma_f32 v[90:91], v[220:221], v[86:87], v[90:91] op_sel:[1,0,0]
	s_nop 0
	v_pk_fma_f32 v[90:91], v[222:223], v[94:95], v[90:91] op_sel_hi:[0,1,1]
	ds_read_b128 v[170:173], v238 offset:20640
	v_pk_fma_f32 v[130:131], v[96:97], v[84:85], v[90:91] op_sel_hi:[0,1,1]
	s_waitcnt lgkmcnt(8)
	v_pk_fma_f32 v[90:91], v[92:93], v[224:225], v[98:99] op_sel_hi:[1,0,1]
	s_nop 0
	v_pk_fma_f32 v[90:91], v[224:225], v[86:87], v[90:91] op_sel:[1,0,0]
	v_mov_b32_e32 v96, v227
	v_pk_fma_f32 v[90:91], v[226:227], v[94:95], v[90:91] op_sel_hi:[0,1,1]
	v_pk_fma_f32 v[90:91], v[96:97], v[84:85], v[90:91] op_sel_hi:[0,1,1]
	ds_read_b128 v[174:177], v238 offset:28848
	s_waitcnt lgkmcnt(8)
	v_pk_fma_f32 v[100:101], v[92:93], v[228:229], v[104:105] op_sel_hi:[1,0,1]
	s_nop 0
	v_pk_fma_f32 v[96:97], v[228:229], v[86:87], v[100:101] op_sel:[1,0,0]
	s_nop 0
	v_pk_fma_f32 v[96:97], v[230:231], v[94:95], v[96:97] op_sel_hi:[0,1,1]
	v_mov_b32_e32 v98, v231
	v_pk_fma_f32 v[96:97], v[98:99], v[84:85], v[96:97] op_sel_hi:[0,1,1]
	ds_read_b128 v[178:181], v238 offset:37056
	s_waitcnt lgkmcnt(8)
	v_pk_fma_f32 v[102:103], v[92:93], v[232:233], v[106:107] op_sel_hi:[1,0,1]
	s_nop 0
	v_pk_fma_f32 v[98:99], v[232:233], v[86:87], v[102:103] op_sel:[1,0,0]
	s_nop 0
	v_pk_fma_f32 v[98:99], v[234:235], v[94:95], v[98:99] op_sel_hi:[0,1,1]
	v_mov_b32_e32 v100, v235
	v_pk_fma_f32 v[98:99], v[100:101], v[84:85], v[98:99] op_sel_hi:[0,1,1]
	ds_read_b128 v[182:185], v238 offset:45264
	s_waitcnt lgkmcnt(8)
	v_pk_fma_f32 v[104:105], v[92:93], v[242:243], v[108:109] op_sel_hi:[1,0,1]
	s_nop 0
	v_pk_fma_f32 v[100:101], v[242:243], v[86:87], v[104:105] op_sel:[1,0,0]
	s_nop 0
	v_pk_fma_f32 v[100:101], v[244:245], v[94:95], v[100:101] op_sel_hi:[0,1,1]
	v_mov_b32_e32 v102, v245
	v_pk_fma_f32 v[100:101], v[102:103], v[84:85], v[100:101] op_sel_hi:[0,1,1]
	ds_read_b128 v[186:189], v238 offset:53472
	s_waitcnt lgkmcnt(8)
	v_pk_fma_f32 v[106:107], v[92:93], v[246:247], v[110:111] op_sel_hi:[1,0,1]
	s_nop 0
	v_pk_fma_f32 v[102:103], v[246:247], v[86:87], v[106:107] op_sel:[1,0,0]
	s_nop 0
	v_pk_fma_f32 v[102:103], v[248:249], v[94:95], v[102:103] op_sel_hi:[0,1,1]
	v_mov_b32_e32 v104, v249
	v_pk_fma_f32 v[102:103], v[104:105], v[84:85], v[102:103] op_sel_hi:[0,1,1]
	ds_read_b128 v[158:161], v238 offset:61680
	s_waitcnt lgkmcnt(8)
	v_pk_fma_f32 v[108:109], v[92:93], v[250:251], v[112:113] op_sel_hi:[1,0,1]
	s_nop 0
	v_pk_fma_f32 v[104:105], v[250:251], v[86:87], v[108:109] op_sel:[1,0,0]
	s_nop 0
	v_pk_fma_f32 v[104:105], v[252:253], v[94:95], v[104:105] op_sel_hi:[0,1,1]
	v_mov_b32_e32 v106, v253
	v_pk_fma_f32 v[104:105], v[106:107], v[84:85], v[104:105] op_sel_hi:[0,1,1]
	ds_read_b128 v[198:201], v25 offset:5120
	s_waitcnt lgkmcnt(8)
; #define LAS __attribute__((address_space(3)))
; __global__ void __launch_bounds__(NTHREADS, 2) hybrid_fwd(Args a) {
;     ...
;                     for (int j = 0; j < 8; ++j) {
; #pragma unroll
;                         for (int e = 0; e < 16; ++e) { const f32x4 w = *(const LAS f32x4*)(rwT + e * 2052 + j * 256 + lane * 4);
;                             acc2[e] += y2[j][0] * (f32x2){w[0], w[0]}; acc2[e] += y2[j][1] * (f32x2){w[1], w[1]};
;                             acc2[e] += y2[j][2] * (f32x2){w[2], w[2]}; acc2[e] += y2[j][3] * (f32x2){w[3], w[3]}; }
;                         __builtin_amdgcn_sched_barrier(0);
;                     }
	v_pk_fma_f32 v[110:111], v[92:93], v[162:163], v[114:115] op_sel_hi:[1,0,1]
	s_nop 0
	v_pk_fma_f32 v[106:107], v[162:163], v[86:87], v[110:111] op_sel:[1,0,0]
	s_nop 0
	v_pk_fma_f32 v[106:107], v[164:165], v[94:95], v[106:107] op_sel_hi:[0,1,1]
	v_mov_b32_e32 v108, v165
	v_pk_fma_f32 v[106:107], v[108:109], v[84:85], v[106:107] op_sel_hi:[0,1,1]
	ds_read_b128 v[202:205], v25 offset:13328
	s_waitcnt lgkmcnt(8)
	v_pk_fma_f32 v[112:113], v[92:93], v[166:167], v[116:117] op_sel_hi:[1,0,1]
	s_nop 0
	v_pk_fma_f32 v[108:109], v[166:167], v[86:87], v[112:113] op_sel:[1,0,0]
	s_nop 0
	v_pk_fma_f32 v[108:109], v[168:169], v[94:95], v[108:109] op_sel_hi:[0,1,1]
	v_mov_b32_e32 v110, v169
	v_pk_fma_f32 v[108:109], v[110:111], v[84:85], v[108:109] op_sel_hi:[0,1,1]
	ds_read_b128 v[216:219], v25 offset:21536
	s_waitcnt lgkmcnt(8)
	v_pk_fma_f32 v[114:115], v[92:93], v[170:171], v[118:119] op_sel_hi:[1,0,1]
	s_nop 0
	v_pk_fma_f32 v[110:111], v[170:171], v[86:87], v[114:115] op_sel:[1,0,0]
	s_nop 0
	v_pk_fma_f32 v[110:111], v[172:173], v[94:95], v[110:111] op_sel_hi:[0,1,1]
	v_mov_b32_e32 v112, v173
	v_pk_fma_f32 v[110:111], v[112:113], v[84:85], v[110:111] op_sel_hi:[0,1,1]
	ds_read_b128 v[220:223], v25 offset:29744
	s_waitcnt lgkmcnt(8)
	v_pk_fma_f32 v[116:117], v[92:93], v[174:175], v[120:121] op_sel_hi:[1,0,1]
	s_nop 0
	v_pk_fma_f32 v[112:113], v[174:175], v[86:87], v[116:117] op_sel:[1,0,0]
	s_nop 0
	v_pk_fma_f32 v[112:113], v[176:177], v[94:95], v[112:113] op_sel_hi:[0,1,1]
	v_mov_b32_e32 v114, v177
	v_pk_fma_f32 v[112:113], v[114:115], v[84:85], v[112:113] op_sel_hi:[0,1,1]
	ds_read_b128 v[224:227], v25 offset:37952
	s_waitcnt lgkmcnt(8)
	v_pk_fma_f32 v[118:119], v[92:93], v[178:179], v[122:123] op_sel_hi:[1,0,1]
	s_nop 0
	v_pk_fma_f32 v[114:115], v[178:179], v[86:87], v[118:119] op_sel:[1,0,0]
	s_nop 0
	v_pk_fma_f32 v[114:115], v[180:181], v[94:95], v[114:115] op_sel_hi:[0,1,1]
	v_mov_b32_e32 v116, v181
	v_pk_fma_f32 v[114:115], v[116:117], v[84:85], v[114:115] op_sel_hi:[0,1,1]
	ds_read_b128 v[228:231], v25 offset:46160
	s_waitcnt lgkmcnt(8)
	v_pk_fma_f32 v[120:121], v[92:93], v[182:183], v[124:125] op_sel_hi:[1,0,1]
	s_nop 0
	v_pk_fma_f32 v[116:117], v[182:183], v[86:87], v[120:121] op_sel:[1,0,0]
	s_nop 0
	v_pk_fma_f32 v[116:117], v[184:185], v[94:95], v[116:117] op_sel_hi:[0,1,1]
	v_mov_b32_e32 v118, v185
	v_pk_fma_f32 v[116:117], v[118:119], v[84:85], v[116:117] op_sel_hi:[0,1,1]
	ds_read_b128 v[232:235], v25 offset:54368
	s_waitcnt lgkmcnt(8)
	v_pk_fma_f32 v[122:123], v[92:93], v[186:187], v[126:127] op_sel_hi:[1,0,1]
	s_nop 0
	v_pk_fma_f32 v[118:119], v[186:187], v[86:87], v[122:123] op_sel:[1,0,0]
	s_nop 0
	v_pk_fma_f32 v[118:119], v[188:189], v[94:95], v[118:119] op_sel_hi:[0,1,1]
	v_mov_b32_e32 v120, v189
	v_pk_fma_f32 v[118:119], v[120:121], v[84:85], v[118:119] op_sel_hi:[0,1,1]
	ds_read_b128 v[242:245], v25 offset:62576
	s_waitcnt lgkmcnt(8)
	v_pk_fma_f32 v[92:93], v[92:93], v[158:159], v[128:129] op_sel_hi:[1,0,1]
	s_nop 0
	v_pk_fma_f32 v[86:87], v[158:159], v[86:87], v[92:93] op_sel:[1,0,0]
	v_mov_b32_e32 v92, v161
	v_pk_fma_f32 v[86:87], v[160:161], v[94:95], v[86:87] op_sel_hi:[0,1,1]
	v_pk_fma_f32 v[120:121], v[92:93], v[84:85], v[86:87] op_sel_hi:[0,1,1]
	ds_read_b128 v[246:249], v238 offset:5248
	s_waitcnt lgkmcnt(8)
	v_pk_fma_f32 v[88:89], v[80:81], v[198:199], v[88:89] op_sel_hi:[1,0,1]
	s_nop 0
	v_pk_fma_f32 v[84:85], v[198:199], v[78:79], v[88:89] op_sel:[1,0,0]
	s_nop 0
	v_pk_fma_f32 v[84:85], v[200:201], v[82:83], v[84:85] op_sel_hi:[0,1,1]
	v_mov_b32_e32 v86, v201
	v_pk_fma_f32 v[84:85], v[86:87], v[76:77], v[84:85] op_sel_hi:[0,1,1]
	ds_read_b128 v[250:253], v238 offset:13456
	s_waitcnt lgkmcnt(8)
	v_pk_fma_f32 v[92:93], v[80:81], v[202:203], v[130:131] op_sel_hi:[1,0,1]
	s_nop 0
	v_pk_fma_f32 v[86:87], v[202:203], v[78:79], v[92:93] op_sel:[1,0,0]
	s_nop 0
	v_pk_fma_f32 v[86:87], v[204:205], v[82:83], v[86:87] op_sel_hi:[0,1,1]
	v_mov_b32_e32 v88, v205
	v_pk_fma_f32 v[122:123], v[88:89], v[76:77], v[86:87] op_sel_hi:[0,1,1]
	ds_read_b128 v[162:165], v238 offset:21664
	s_waitcnt lgkmcnt(8)
	v_pk_fma_f32 v[90:91], v[80:81], v[216:217], v[90:91] op_sel_hi:[1,0,1]
	s_nop 0
	v_pk_fma_f32 v[86:87], v[216:217], v[78:79], v[90:91] op_sel:[1,0,0]
	s_nop 0
	v_pk_fma_f32 v[86:87], v[218:219], v[82:83], v[86:87] op_sel_hi:[0,1,1]
	v_mov_b32_e32 v88, v219
	v_pk_fma_f32 v[86:87], v[88:89], v[76:77], v[86:87] op_sel_hi:[0,1,1]
	ds_read_b128 v[166:169], v238 offset:29872
	s_waitcnt lgkmcnt(8)
	v_pk_fma_f32 v[92:93], v[80:81], v[220:221], v[96:97] op_sel_hi:[1,0,1]
	s_nop 0
	v_pk_fma_f32 v[88:89], v[220:221], v[78:79], v[92:93] op_sel:[1,0,0]
	s_nop 0
	v_pk_fma_f32 v[88:89], v[222:223], v[82:83], v[88:89] op_sel_hi:[0,1,1]
	v_mov_b32_e32 v90, v223
	v_pk_fma_f32 v[88:89], v[90:91], v[76:77], v[88:89] op_sel_hi:[0,1,1]
	ds_read_b128 v[170:173], v238 offset:38080
	s_waitcnt lgkmcnt(8)
	v_pk_fma_f32 v[94:95], v[80:81], v[224:225], v[98:99] op_sel_hi:[1,0,1]
	s_nop 0
	v_pk_fma_f32 v[90:91], v[224:225], v[78:79], v[94:95] op_sel:[1,0,0]
	s_nop 0
	v_pk_fma_f32 v[90:91], v[226:227], v[82:83], v[90:91] op_sel_hi:[0,1,1]
	v_mov_b32_e32 v92, v227
	v_pk_fma_f32 v[90:91], v[92:93], v[76:77], v[90:91] op_sel_hi:[0,1,1]
	ds_read_b128 v[174:177], v238 offset:46288
	s_waitcnt lgkmcnt(8)
	v_pk_fma_f32 v[96:97], v[80:81], v[228:229], v[100:101] op_sel_hi:[1,0,1]
	s_nop 0
	v_pk_fma_f32 v[92:93], v[228:229], v[78:79], v[96:97] op_sel:[1,0,0]
	s_nop 0
	v_pk_fma_f32 v[92:93], v[230:231], v[82:83], v[92:93] op_sel_hi:[0,1,1]
	v_mov_b32_e32 v94, v231
	v_pk_fma_f32 v[92:93], v[94:95], v[76:77], v[92:93] op_sel_hi:[0,1,1]
	ds_read_b128 v[178:181], v238 offset:54496
	s_waitcnt lgkmcnt(8)
; #define LAS __attribute__((address_space(3)))
; __global__ void __launch_bounds__(NTHREADS, 2) hybrid_fwd(Args a) {
;     ...
;                     for (int j = 0; j < 8; ++j) {
; #pragma unroll
;                         for (int e = 0; e < 16; ++e) { const f32x4 w = *(const LAS f32x4*)(rwT + e * 2052 + j * 256 + lane * 4);
;                             acc2[e] += y2[j][0] * (f32x2){w[0], w[0]}; acc2[e] += y2[j][1] * (f32x2){w[1], w[1]};
;                             acc2[e] += y2[j][2] * (f32x2){w[2], w[2]}; acc2[e] += y2[j][3] * (f32x2){w[3], w[3]}; }
;                         __builtin_amdgcn_sched_barrier(0);
;                     }
	v_pk_fma_f32 v[98:99], v[80:81], v[232:233], v[102:103] op_sel_hi:[1,0,1]
	s_nop 0
	v_pk_fma_f32 v[94:95], v[232:233], v[78:79], v[98:99] op_sel:[1,0,0]
	s_nop 0
	v_pk_fma_f32 v[94:95], v[234:235], v[82:83], v[94:95] op_sel_hi:[0,1,1]
	v_mov_b32_e32 v96, v235
	v_pk_fma_f32 v[94:95], v[96:97], v[76:77], v[94:95] op_sel_hi:[0,1,1]
	ds_read_b128 v[182:185], v238 offset:62704
	s_waitcnt lgkmcnt(8)
	v_pk_fma_f32 v[100:101], v[80:81], v[242:243], v[104:105] op_sel_hi:[1,0,1]
	s_nop 0
	v_pk_fma_f32 v[96:97], v[242:243], v[78:79], v[100:101] op_sel:[1,0,0]
	s_nop 0
	v_pk_fma_f32 v[96:97], v[244:245], v[82:83], v[96:97] op_sel_hi:[0,1,1]
	v_mov_b32_e32 v98, v245
	v_pk_fma_f32 v[96:97], v[98:99], v[76:77], v[96:97] op_sel_hi:[0,1,1]
	ds_read_b128 v[186:189], v25 offset:6144
	s_waitcnt lgkmcnt(8)
	v_pk_fma_f32 v[102:103], v[80:81], v[246:247], v[106:107] op_sel_hi:[1,0,1]
	s_nop 0
	v_pk_fma_f32 v[98:99], v[246:247], v[78:79], v[102:103] op_sel:[1,0,0]
	s_nop 0
	v_pk_fma_f32 v[98:99], v[248:249], v[82:83], v[98:99] op_sel_hi:[0,1,1]
	v_mov_b32_e32 v100, v249
	v_pk_fma_f32 v[98:99], v[100:101], v[76:77], v[98:99] op_sel_hi:[0,1,1]
	ds_read_b128 v[158:161], v25 offset:14352
	s_waitcnt lgkmcnt(8)
	v_pk_fma_f32 v[104:105], v[80:81], v[250:251], v[108:109] op_sel_hi:[1,0,1]
	s_nop 0
	v_pk_fma_f32 v[100:101], v[250:251], v[78:79], v[104:105] op_sel:[1,0,0]
	s_nop 0
	v_pk_fma_f32 v[100:101], v[252:253], v[82:83], v[100:101] op_sel_hi:[0,1,1]
	v_mov_b32_e32 v102, v253
	v_pk_fma_f32 v[100:101], v[102:103], v[76:77], v[100:101] op_sel_hi:[0,1,1]
	ds_read_b128 v[198:201], v25 offset:22560
	s_waitcnt lgkmcnt(8)
	v_pk_fma_f32 v[106:107], v[80:81], v[162:163], v[110:111] op_sel_hi:[1,0,1]
	s_nop 0
	v_pk_fma_f32 v[102:103], v[162:163], v[78:79], v[106:107] op_sel:[1,0,0]
	s_nop 0
	v_pk_fma_f32 v[102:103], v[164:165], v[82:83], v[102:103] op_sel_hi:[0,1,1]
	v_mov_b32_e32 v104, v165
	v_pk_fma_f32 v[102:103], v[104:105], v[76:77], v[102:103] op_sel_hi:[0,1,1]
	ds_read_b128 v[202:205], v25 offset:30768
	s_waitcnt lgkmcnt(8)
	v_pk_fma_f32 v[108:109], v[80:81], v[166:167], v[112:113] op_sel_hi:[1,0,1]
	s_nop 0
	v_pk_fma_f32 v[104:105], v[166:167], v[78:79], v[108:109] op_sel:[1,0,0]
	s_nop 0
	v_pk_fma_f32 v[104:105], v[168:169], v[82:83], v[104:105] op_sel_hi:[0,1,1]
	v_mov_b32_e32 v106, v169
	v_pk_fma_f32 v[104:105], v[106:107], v[76:77], v[104:105] op_sel_hi:[0,1,1]
	ds_read_b128 v[216:219], v25 offset:38976
	s_waitcnt lgkmcnt(8)
	v_pk_fma_f32 v[110:111], v[80:81], v[170:171], v[114:115] op_sel_hi:[1,0,1]
	s_nop 0
	v_pk_fma_f32 v[106:107], v[170:171], v[78:79], v[110:111] op_sel:[1,0,0]
	s_nop 0
	v_pk_fma_f32 v[106:107], v[172:173], v[82:83], v[106:107] op_sel_hi:[0,1,1]
	v_mov_b32_e32 v108, v173
	v_pk_fma_f32 v[106:107], v[108:109], v[76:77], v[106:107] op_sel_hi:[0,1,1]
	ds_read_b128 v[220:223], v25 offset:47184
	s_waitcnt lgkmcnt(8)
	v_pk_fma_f32 v[112:113], v[80:81], v[174:175], v[116:117] op_sel_hi:[1,0,1]
	s_nop 0
	v_pk_fma_f32 v[108:109], v[174:175], v[78:79], v[112:113] op_sel:[1,0,0]
	s_nop 0
	v_pk_fma_f32 v[108:109], v[176:177], v[82:83], v[108:109] op_sel_hi:[0,1,1]
	v_mov_b32_e32 v110, v177
	v_pk_fma_f32 v[108:109], v[110:111], v[76:77], v[108:109] op_sel_hi:[0,1,1]
	ds_read_b128 v[224:227], v25 offset:55392
	s_waitcnt lgkmcnt(8)
	v_pk_fma_f32 v[114:115], v[80:81], v[178:179], v[118:119] op_sel_hi:[1,0,1]
	s_nop 0
	v_pk_fma_f32 v[110:111], v[178:179], v[78:79], v[114:115] op_sel:[1,0,0]
	s_nop 0
	v_pk_fma_f32 v[110:111], v[180:181], v[82:83], v[110:111] op_sel_hi:[0,1,1]
	v_mov_b32_e32 v112, v181
	v_pk_fma_f32 v[110:111], v[112:113], v[76:77], v[110:111] op_sel_hi:[0,1,1]
	ds_read_b128 v[228:231], v25 offset:63600
	s_waitcnt lgkmcnt(8)
	v_pk_fma_f32 v[80:81], v[80:81], v[182:183], v[120:121] op_sel_hi:[1,0,1]
	s_nop 0
	v_pk_fma_f32 v[78:79], v[182:183], v[78:79], v[80:81] op_sel:[1,0,0]
	v_mov_b32_e32 v80, v185
	v_pk_fma_f32 v[78:79], v[184:185], v[82:83], v[78:79] op_sel_hi:[0,1,1]
	v_pk_fma_f32 v[112:113], v[80:81], v[76:77], v[78:79] op_sel_hi:[0,1,1]
	ds_read_b128 v[232:235], v238 offset:6272
	s_waitcnt lgkmcnt(8)
	v_pk_fma_f32 v[80:81], v[72:73], v[186:187], v[84:85] op_sel_hi:[1,0,1]
	s_nop 0
	v_pk_fma_f32 v[76:77], v[186:187], v[70:71], v[80:81] op_sel:[1,0,0]
	s_nop 0
	v_pk_fma_f32 v[76:77], v[188:189], v[74:75], v[76:77] op_sel_hi:[0,1,1]
	v_mov_b32_e32 v78, v189
	v_pk_fma_f32 v[76:77], v[78:79], v[68:69], v[76:77] op_sel_hi:[0,1,1]
	ds_read_b128 v[242:245], v238 offset:14480
	s_waitcnt lgkmcnt(8)
	v_pk_fma_f32 v[82:83], v[72:73], v[158:159], v[122:123] op_sel_hi:[1,0,1]
	s_nop 0
	v_pk_fma_f32 v[78:79], v[158:159], v[70:71], v[82:83] op_sel:[1,0,0]
	s_nop 0
	v_pk_fma_f32 v[78:79], v[160:161], v[74:75], v[78:79] op_sel_hi:[0,1,1]
	v_mov_b32_e32 v80, v161
	v_pk_fma_f32 v[114:115], v[80:81], v[68:69], v[78:79] op_sel_hi:[0,1,1]
	ds_read_b128 v[246:249], v238 offset:22688
	s_waitcnt lgkmcnt(8)
	v_pk_fma_f32 v[82:83], v[72:73], v[198:199], v[86:87] op_sel_hi:[1,0,1]
	s_nop 0
	v_pk_fma_f32 v[78:79], v[198:199], v[70:71], v[82:83] op_sel:[1,0,0]
	s_nop 0
	v_pk_fma_f32 v[78:79], v[200:201], v[74:75], v[78:79] op_sel_hi:[0,1,1]
	v_mov_b32_e32 v80, v201
	v_pk_fma_f32 v[78:79], v[80:81], v[68:69], v[78:79] op_sel_hi:[0,1,1]
	ds_read_b128 v[250:253], v238 offset:30896
	s_waitcnt lgkmcnt(8)
	v_pk_fma_f32 v[84:85], v[72:73], v[202:203], v[88:89] op_sel_hi:[1,0,1]
	s_nop 0
	v_pk_fma_f32 v[80:81], v[202:203], v[70:71], v[84:85] op_sel:[1,0,0]
	s_nop 0
	v_pk_fma_f32 v[80:81], v[204:205], v[74:75], v[80:81] op_sel_hi:[0,1,1]
	v_mov_b32_e32 v82, v205
	v_pk_fma_f32 v[80:81], v[82:83], v[68:69], v[80:81] op_sel_hi:[0,1,1]
	ds_read_b128 v[162:165], v238 offset:39104
	s_waitcnt lgkmcnt(8)
; #define LAS __attribute__((address_space(3)))
; __global__ void __launch_bounds__(NTHREADS, 2) hybrid_fwd(Args a) {
;     ...
;                     for (int j = 0; j < 8; ++j) {
; #pragma unroll
;                         for (int e = 0; e < 16; ++e) { const f32x4 w = *(const LAS f32x4*)(rwT + e * 2052 + j * 256 + lane * 4);
;                             acc2[e] += y2[j][0] * (f32x2){w[0], w[0]}; acc2[e] += y2[j][1] * (f32x2){w[1], w[1]};
;                             acc2[e] += y2[j][2] * (f32x2){w[2], w[2]}; acc2[e] += y2[j][3] * (f32x2){w[3], w[3]}; }
;                         __builtin_amdgcn_sched_barrier(0);
;                     }
	v_pk_fma_f32 v[86:87], v[72:73], v[216:217], v[90:91] op_sel_hi:[1,0,1]
	s_nop 0
	v_pk_fma_f32 v[82:83], v[216:217], v[70:71], v[86:87] op_sel:[1,0,0]
	s_nop 0
	v_pk_fma_f32 v[82:83], v[218:219], v[74:75], v[82:83] op_sel_hi:[0,1,1]
	v_mov_b32_e32 v84, v219
	v_pk_fma_f32 v[82:83], v[84:85], v[68:69], v[82:83] op_sel_hi:[0,1,1]
	ds_read_b128 v[166:169], v238 offset:47312
	s_waitcnt lgkmcnt(8)
	v_pk_fma_f32 v[88:89], v[72:73], v[220:221], v[92:93] op_sel_hi:[1,0,1]
	s_nop 0
	v_pk_fma_f32 v[84:85], v[220:221], v[70:71], v[88:89] op_sel:[1,0,0]
	s_nop 0
	v_pk_fma_f32 v[84:85], v[222:223], v[74:75], v[84:85] op_sel_hi:[0,1,1]
	v_mov_b32_e32 v86, v223
	v_pk_fma_f32 v[84:85], v[86:87], v[68:69], v[84:85] op_sel_hi:[0,1,1]
	ds_read_b128 v[170:173], v238 offset:55520
	s_waitcnt lgkmcnt(8)
	v_pk_fma_f32 v[90:91], v[72:73], v[224:225], v[94:95] op_sel_hi:[1,0,1]
	s_nop 0
	v_pk_fma_f32 v[86:87], v[224:225], v[70:71], v[90:91] op_sel:[1,0,0]
	s_nop 0
	v_pk_fma_f32 v[86:87], v[226:227], v[74:75], v[86:87] op_sel_hi:[0,1,1]
	v_mov_b32_e32 v88, v227
	v_pk_fma_f32 v[86:87], v[88:89], v[68:69], v[86:87] op_sel_hi:[0,1,1]
	ds_read_b128 v[174:177], v238 offset:63728
	s_waitcnt lgkmcnt(8)
	v_pk_fma_f32 v[92:93], v[72:73], v[228:229], v[96:97] op_sel_hi:[1,0,1]
	s_nop 0
	v_pk_fma_f32 v[88:89], v[228:229], v[70:71], v[92:93] op_sel:[1,0,0]
	s_nop 0
	v_pk_fma_f32 v[88:89], v[230:231], v[74:75], v[88:89] op_sel_hi:[0,1,1]
	v_mov_b32_e32 v90, v231
	v_pk_fma_f32 v[88:89], v[90:91], v[68:69], v[88:89] op_sel_hi:[0,1,1]
	ds_read_b128 v[178:181], v25 offset:7168
	s_waitcnt lgkmcnt(8)
	v_pk_fma_f32 v[94:95], v[72:73], v[232:233], v[98:99] op_sel_hi:[1,0,1]
	s_nop 0
	v_pk_fma_f32 v[90:91], v[232:233], v[70:71], v[94:95] op_sel:[1,0,0]
	s_nop 0
	v_pk_fma_f32 v[90:91], v[234:235], v[74:75], v[90:91] op_sel_hi:[0,1,1]
	v_mov_b32_e32 v92, v235
	v_pk_fma_f32 v[90:91], v[92:93], v[68:69], v[90:91] op_sel_hi:[0,1,1]
	ds_read_b128 v[182:185], v25 offset:15376
	s_waitcnt lgkmcnt(8)
	v_pk_fma_f32 v[96:97], v[72:73], v[242:243], v[100:101] op_sel_hi:[1,0,1]
	s_nop 0
	v_pk_fma_f32 v[92:93], v[242:243], v[70:71], v[96:97] op_sel:[1,0,0]
	s_nop 0
	v_pk_fma_f32 v[92:93], v[244:245], v[74:75], v[92:93] op_sel_hi:[0,1,1]
	v_mov_b32_e32 v94, v245
	v_pk_fma_f32 v[92:93], v[94:95], v[68:69], v[92:93] op_sel_hi:[0,1,1]
	ds_read_b128 v[186:189], v25 offset:23584
	s_waitcnt lgkmcnt(8)
	v_pk_fma_f32 v[98:99], v[72:73], v[246:247], v[102:103] op_sel_hi:[1,0,1]
	s_nop 0
	v_pk_fma_f32 v[94:95], v[246:247], v[70:71], v[98:99] op_sel:[1,0,0]
	s_nop 0
	v_pk_fma_f32 v[94:95], v[248:249], v[74:75], v[94:95] op_sel_hi:[0,1,1]
	v_mov_b32_e32 v96, v249
	v_pk_fma_f32 v[94:95], v[96:97], v[68:69], v[94:95] op_sel_hi:[0,1,1]
	ds_read_b128 v[158:161], v25 offset:31792
	s_waitcnt lgkmcnt(8)
	v_pk_fma_f32 v[100:101], v[72:73], v[250:251], v[104:105] op_sel_hi:[1,0,1]
	s_nop 0
	v_pk_fma_f32 v[96:97], v[250:251], v[70:71], v[100:101] op_sel:[1,0,0]
	s_nop 0
	v_pk_fma_f32 v[96:97], v[252:253], v[74:75], v[96:97] op_sel_hi:[0,1,1]
	v_mov_b32_e32 v98, v253
	v_pk_fma_f32 v[96:97], v[98:99], v[68:69], v[96:97] op_sel_hi:[0,1,1]
	ds_read_b128 v[198:201], v25 offset:40000
	s_waitcnt lgkmcnt(8)
	v_pk_fma_f32 v[102:103], v[72:73], v[162:163], v[106:107] op_sel_hi:[1,0,1]
	s_nop 0
	v_pk_fma_f32 v[98:99], v[162:163], v[70:71], v[102:103] op_sel:[1,0,0]
	s_nop 0
	v_pk_fma_f32 v[98:99], v[164:165], v[74:75], v[98:99] op_sel_hi:[0,1,1]
	v_mov_b32_e32 v100, v165
	v_pk_fma_f32 v[98:99], v[100:101], v[68:69], v[98:99] op_sel_hi:[0,1,1]
	ds_read_b128 v[202:205], v25 offset:48208
	s_waitcnt lgkmcnt(8)
	v_pk_fma_f32 v[104:105], v[72:73], v[166:167], v[108:109] op_sel_hi:[1,0,1]
	s_nop 0
	v_pk_fma_f32 v[100:101], v[166:167], v[70:71], v[104:105] op_sel:[1,0,0]
	s_nop 0
	v_pk_fma_f32 v[100:101], v[168:169], v[74:75], v[100:101] op_sel_hi:[0,1,1]
	v_mov_b32_e32 v102, v169
	v_pk_fma_f32 v[100:101], v[102:103], v[68:69], v[100:101] op_sel_hi:[0,1,1]
	ds_read_b128 v[216:219], v25 offset:56416
	s_waitcnt lgkmcnt(8)
	v_pk_fma_f32 v[106:107], v[72:73], v[170:171], v[110:111] op_sel_hi:[1,0,1]
	s_nop 0
	v_pk_fma_f32 v[102:103], v[170:171], v[70:71], v[106:107] op_sel:[1,0,0]
	s_nop 0
	v_pk_fma_f32 v[102:103], v[172:173], v[74:75], v[102:103] op_sel_hi:[0,1,1]
	v_mov_b32_e32 v104, v173
	v_pk_fma_f32 v[102:103], v[104:105], v[68:69], v[102:103] op_sel_hi:[0,1,1]
	ds_read_b128 v[220:223], v25 offset:64624
	s_waitcnt lgkmcnt(8)
	v_pk_fma_f32 v[72:73], v[72:73], v[174:175], v[112:113] op_sel_hi:[1,0,1]
	s_nop 0
	v_pk_fma_f32 v[70:71], v[174:175], v[70:71], v[72:73] op_sel:[1,0,0]
	v_mov_b32_e32 v72, v177
	v_pk_fma_f32 v[70:71], v[176:177], v[74:75], v[70:71] op_sel_hi:[0,1,1]
	v_pk_fma_f32 v[104:105], v[72:73], v[68:69], v[70:71] op_sel_hi:[0,1,1]
	ds_read_b128 v[224:227], v238 offset:7296
	s_waitcnt lgkmcnt(8)
	v_pk_fma_f32 v[72:73], v[66:67], v[178:179], v[76:77] op_sel_hi:[1,0,1]
	s_nop 0
	v_pk_fma_f32 v[68:69], v[178:179], v[62:63], v[72:73] op_sel:[1,0,0]
	s_nop 0
	v_pk_fma_f32 v[68:69], v[180:181], v[64:65], v[68:69] op_sel_hi:[0,1,1]
	v_mov_b32_e32 v70, v181
	v_pk_fma_f32 v[68:69], v[70:71], v[60:61], v[68:69] op_sel_hi:[0,1,1]
	ds_read_b128 v[228:231], v238 offset:15504
	s_waitcnt lgkmcnt(8)
	v_pk_fma_f32 v[74:75], v[66:67], v[182:183], v[114:115] op_sel_hi:[1,0,1]
	s_nop 0
	v_pk_fma_f32 v[70:71], v[182:183], v[62:63], v[74:75] op_sel:[1,0,0]
	s_nop 0
	v_pk_fma_f32 v[70:71], v[184:185], v[64:65], v[70:71] op_sel_hi:[0,1,1]
	v_mov_b32_e32 v72, v185
	v_pk_fma_f32 v[70:71], v[72:73], v[60:61], v[70:71] op_sel_hi:[0,1,1]
	ds_read_b128 v[232:235], v238 offset:23712
	s_waitcnt lgkmcnt(8)
; #define LAS __attribute__((address_space(3)))
; __global__ void __launch_bounds__(NTHREADS, 2) hybrid_fwd(Args a) {
;     ...
;                     for (int j = 0; j < 8; ++j) {
; #pragma unroll
;                         for (int e = 0; e < 16; ++e) { const f32x4 w = *(const LAS f32x4*)(rwT + e * 2052 + j * 256 + lane * 4);
;                             acc2[e] += y2[j][0] * (f32x2){w[0], w[0]}; acc2[e] += y2[j][1] * (f32x2){w[1], w[1]};
;                             acc2[e] += y2[j][2] * (f32x2){w[2], w[2]}; acc2[e] += y2[j][3] * (f32x2){w[3], w[3]}; }
;                         __builtin_amdgcn_sched_barrier(0);
;                     }
	v_pk_fma_f32 v[76:77], v[66:67], v[186:187], v[78:79] op_sel_hi:[1,0,1]
	s_nop 0
	v_pk_fma_f32 v[72:73], v[186:187], v[62:63], v[76:77] op_sel:[1,0,0]
	s_nop 0
	v_pk_fma_f32 v[72:73], v[188:189], v[64:65], v[72:73] op_sel_hi:[0,1,1]
	v_mov_b32_e32 v74, v189
	v_pk_fma_f32 v[72:73], v[74:75], v[60:61], v[72:73] op_sel_hi:[0,1,1]
	ds_read_b128 v[242:245], v238 offset:31920
	s_waitcnt lgkmcnt(8)
	v_pk_fma_f32 v[78:79], v[66:67], v[158:159], v[80:81] op_sel_hi:[1,0,1]
	s_nop 0
	v_pk_fma_f32 v[74:75], v[158:159], v[62:63], v[78:79] op_sel:[1,0,0]
	ds_read_b128 v[246:249], v238 offset:40128
	v_pk_fma_f32 v[74:75], v[160:161], v[64:65], v[74:75] op_sel_hi:[0,1,1]
	v_mov_b32_e32 v76, v161
	v_pk_fma_f32 v[76:77], v[76:77], v[60:61], v[74:75] op_sel_hi:[0,1,1]
	s_waitcnt lgkmcnt(8)
	v_pk_fma_f32 v[74:75], v[66:67], v[198:199], v[82:83] op_sel_hi:[1,0,1]
	s_nop 0
	v_pk_fma_f32 v[74:75], v[198:199], v[62:63], v[74:75] op_sel:[1,0,0]
	v_mov_b32_e32 v78, v201
	v_pk_fma_f32 v[74:75], v[200:201], v[64:65], v[74:75] op_sel_hi:[0,1,1]
	v_pk_fma_f32 v[74:75], v[78:79], v[60:61], v[74:75] op_sel_hi:[0,1,1]
	ds_read_b128 v[250:253], v238 offset:48336
	s_waitcnt lgkmcnt(8)
	v_pk_fma_f32 v[82:83], v[66:67], v[202:203], v[84:85] op_sel_hi:[1,0,1]
	s_nop 0
	v_pk_fma_f32 v[78:79], v[202:203], v[62:63], v[82:83] op_sel:[1,0,0]
	s_nop 0
	v_pk_fma_f32 v[78:79], v[204:205], v[64:65], v[78:79] op_sel_hi:[0,1,1]
	v_mov_b32_e32 v80, v205
	v_pk_fma_f32 v[78:79], v[80:81], v[60:61], v[78:79] op_sel_hi:[0,1,1]
	ds_read_b128 v[162:165], v238 offset:56544
	s_waitcnt lgkmcnt(8)
	v_pk_fma_f32 v[84:85], v[66:67], v[216:217], v[86:87] op_sel_hi:[1,0,1]
	s_nop 0
	v_pk_fma_f32 v[80:81], v[216:217], v[62:63], v[84:85] op_sel:[1,0,0]
	s_nop 0
	v_pk_fma_f32 v[80:81], v[218:219], v[64:65], v[80:81] op_sel_hi:[0,1,1]
	v_mov_b32_e32 v82, v219
	v_pk_fma_f32 v[80:81], v[82:83], v[60:61], v[80:81] op_sel_hi:[0,1,1]
	ds_read_b128 v[166:169], v238 offset:64752
	s_waitcnt lgkmcnt(8)
	v_pk_fma_f32 v[86:87], v[66:67], v[220:221], v[88:89] op_sel_hi:[1,0,1]
	s_nop 0
	v_pk_fma_f32 v[82:83], v[220:221], v[62:63], v[86:87] op_sel:[1,0,0]
	s_nop 0
	v_pk_fma_f32 v[82:83], v[222:223], v[64:65], v[82:83] op_sel_hi:[0,1,1]
	v_mov_b32_e32 v84, v223
	v_pk_fma_f32 v[82:83], v[84:85], v[60:61], v[82:83] op_sel_hi:[0,1,1]
	s_waitcnt lgkmcnt(7)
	v_pk_fma_f32 v[88:89], v[66:67], v[224:225], v[90:91] op_sel_hi:[1,0,1]
	s_nop 0
	v_pk_fma_f32 v[84:85], v[224:225], v[62:63], v[88:89] op_sel:[1,0,0]
	s_nop 0
	v_pk_fma_f32 v[84:85], v[226:227], v[64:65], v[84:85] op_sel_hi:[0,1,1]
	v_mov_b32_e32 v86, v227
	v_pk_fma_f32 v[84:85], v[86:87], v[60:61], v[84:85] op_sel_hi:[0,1,1]
	s_waitcnt lgkmcnt(6)
	v_pk_fma_f32 v[90:91], v[66:67], v[228:229], v[92:93] op_sel_hi:[1,0,1]
	s_nop 0
	v_pk_fma_f32 v[86:87], v[228:229], v[62:63], v[90:91] op_sel:[1,0,0]
	s_nop 0
	v_pk_fma_f32 v[86:87], v[230:231], v[64:65], v[86:87] op_sel_hi:[0,1,1]
	v_mov_b32_e32 v88, v231
	v_pk_fma_f32 v[86:87], v[88:89], v[60:61], v[86:87] op_sel_hi:[0,1,1]
	s_waitcnt lgkmcnt(5)
	v_pk_fma_f32 v[92:93], v[66:67], v[232:233], v[94:95] op_sel_hi:[1,0,1]
	s_nop 0
	v_pk_fma_f32 v[88:89], v[232:233], v[62:63], v[92:93] op_sel:[1,0,0]
	s_nop 0
	v_pk_fma_f32 v[88:89], v[234:235], v[64:65], v[88:89] op_sel_hi:[0,1,1]
	v_mov_b32_e32 v90, v235
	v_pk_fma_f32 v[88:89], v[90:91], v[60:61], v[88:89] op_sel_hi:[0,1,1]
	s_waitcnt lgkmcnt(4)
	v_pk_fma_f32 v[94:95], v[66:67], v[242:243], v[96:97] op_sel_hi:[1,0,1]
	s_nop 0
	v_pk_fma_f32 v[90:91], v[242:243], v[62:63], v[94:95] op_sel:[1,0,0]
	s_nop 0
	v_pk_fma_f32 v[90:91], v[244:245], v[64:65], v[90:91] op_sel_hi:[0,1,1]
	v_mov_b32_e32 v92, v245
	v_pk_fma_f32 v[90:91], v[92:93], v[60:61], v[90:91] op_sel_hi:[0,1,1]
	s_waitcnt lgkmcnt(3)
	v_pk_fma_f32 v[96:97], v[66:67], v[246:247], v[98:99] op_sel_hi:[1,0,1]
	s_nop 0
	v_pk_fma_f32 v[92:93], v[246:247], v[62:63], v[96:97] op_sel:[1,0,0]
	s_nop 0
	v_pk_fma_f32 v[92:93], v[248:249], v[64:65], v[92:93] op_sel_hi:[0,1,1]
	v_mov_b32_e32 v94, v249
	v_pk_fma_f32 v[92:93], v[94:95], v[60:61], v[92:93] op_sel_hi:[0,1,1]
	s_waitcnt lgkmcnt(2)
	v_pk_fma_f32 v[98:99], v[66:67], v[250:251], v[100:101] op_sel_hi:[1,0,1]
	s_nop 0
	v_pk_fma_f32 v[94:95], v[250:251], v[62:63], v[98:99] op_sel:[1,0,0]
	s_nop 0
	v_pk_fma_f32 v[94:95], v[252:253], v[64:65], v[94:95] op_sel_hi:[0,1,1]
	v_mov_b32_e32 v96, v253
	v_pk_fma_f32 v[94:95], v[96:97], v[60:61], v[94:95] op_sel_hi:[0,1,1]
	s_waitcnt lgkmcnt(1)
	v_pk_fma_f32 v[100:101], v[66:67], v[162:163], v[102:103] op_sel_hi:[1,0,1]
	s_nop 0
	v_pk_fma_f32 v[96:97], v[162:163], v[62:63], v[100:101] op_sel:[1,0,0]
	s_nop 0
	v_pk_fma_f32 v[96:97], v[164:165], v[64:65], v[96:97] op_sel_hi:[0,1,1]
	v_mov_b32_e32 v98, v165
	v_pk_fma_f32 v[96:97], v[98:99], v[60:61], v[96:97] op_sel_hi:[0,1,1]
	s_waitcnt lgkmcnt(0)
; #define WS_STEP(ctrl) v += __int_as_float(__builtin_amdgcn_update_dpp(0, __float_as_int(v), (ctrl), 0xf, 0xf, true))
; __device__ __forceinline__ float wave_sum(float v) {
;     ...
;     WS_STEP(0xB1); WS_STEP(0x4E); WS_STEP(0x124); WS_STEP(0x128);
;     ...
;     const auto r16 = __builtin_amdgcn_permlane16_swap(__float_as_uint(v), __float_as_uint(v), false, false);
;     v = __uint_as_float(r16[0]) + __uint_as_float(r16[1]);
;     const auto rr = __builtin_amdgcn_permlane32_swap(__float_as_uint(v), __float_as_uint(v), false, false);
;     return __uint_as_float(rr[0]) + __uint_as_float(rr[1]);
; }
	v_pk_fma_f32 v[66:67], v[66:67], v[166:167], v[104:105] op_sel_hi:[1,0,1]
	s_nop 0
	v_pk_fma_f32 v[62:63], v[166:167], v[62:63], v[66:67] op_sel:[1,0,0]
	s_nop 0
	v_pk_fma_f32 v[62:63], v[168:169], v[64:65], v[62:63] op_sel_hi:[0,1,1]
	v_mov_b32_e32 v64, v169
	v_pk_fma_f32 v[60:61], v[64:65], v[60:61], v[62:63] op_sel_hi:[0,1,1]
	v_add_f32_dpp v62, v68, v68 quad_perm:[1,0,3,2] row_mask:0xf bank_mask:0xf bound_ctrl:1
	s_nop 0
	v_add_f32_dpp v60, v60, v60 quad_perm:[1,0,3,2] row_mask:0xf bank_mask:0xf bound_ctrl:1
	v_add_f32_dpp v68, v94, v94 quad_perm:[1,0,3,2] row_mask:0xf bank_mask:0xf bound_ctrl:1
	v_add_f32_dpp v62, v62, v62 quad_perm:[2,3,0,1] row_mask:0xf bank_mask:0xf bound_ctrl:1
	v_add_f32_dpp v60, v60, v60 quad_perm:[2,3,0,1] row_mask:0xf bank_mask:0xf bound_ctrl:1
	v_add_f32_dpp v68, v68, v68 quad_perm:[2,3,0,1] row_mask:0xf bank_mask:0xf bound_ctrl:1
	v_add_f32_dpp v62, v62, v62 row_ror:4 row_mask:0xf bank_mask:0xf bound_ctrl:1
	v_add_f32_dpp v60, v60, v60 row_ror:4 row_mask:0xf bank_mask:0xf bound_ctrl:1
	v_add_f32_dpp v68, v68, v68 row_ror:4 row_mask:0xf bank_mask:0xf bound_ctrl:1
	v_add_f32_dpp v62, v62, v62 row_ror:8 row_mask:0xf bank_mask:0xf bound_ctrl:1
	v_mov_b32_e32 v63, v62
	s_nop 1
	v_permlane16_swap_b32_e32 v62, v63
	v_add_f32_e32 v62, v62, v63
	v_mov_b32_e32 v63, v62
	s_nop 1
	v_permlane32_swap_b32_e32 v62, v63
	v_add_f32_e32 v62, v62, v63
	s_nop 0
	v_add_f32_dpp v63, v70, v70 quad_perm:[1,0,3,2] row_mask:0xf bank_mask:0xf bound_ctrl:1
	v_mul_f32_e32 v62, 0xbfb8aa3b, v62
	v_exp_f32_e32 v62, v62
	v_add_f32_dpp v63, v63, v63 quad_perm:[2,3,0,1] row_mask:0xf bank_mask:0xf bound_ctrl:1
	v_add_f32_dpp v60, v60, v60 row_ror:8 row_mask:0xf bank_mask:0xf bound_ctrl:1
	v_add_f32_dpp v68, v68, v68 row_ror:8 row_mask:0xf bank_mask:0xf bound_ctrl:1
	v_add_f32_dpp v63, v63, v63 row_ror:4 row_mask:0xf bank_mask:0xf bound_ctrl:1
	v_add_f32_e32 v62, 1.0, v62
	v_rcp_f32_e32 v62, v62
	v_add_f32_dpp v63, v63, v63 row_ror:8 row_mask:0xf bank_mask:0xf bound_ctrl:1
	v_mov_b32_e32 v64, v63
	s_nop 1
	v_permlane16_swap_b32_e32 v63, v64
	v_add_f32_e32 v63, v63, v64
	v_mov_b32_e32 v64, v63
	s_nop 1
	v_permlane32_swap_b32_e32 v63, v64
	v_add_f32_e32 v63, v63, v64
	s_nop 0
	v_add_f32_dpp v64, v72, v72 quad_perm:[1,0,3,2] row_mask:0xf bank_mask:0xf bound_ctrl:1
	v_mul_f32_e32 v63, 0xbfb8aa3b, v63
	v_exp_f32_e32 v63, v63
	v_add_f32_dpp v64, v64, v64 quad_perm:[2,3,0,1] row_mask:0xf bank_mask:0xf bound_ctrl:1
	v_add_f32_dpp v72, v96, v96 quad_perm:[1,0,3,2] row_mask:0xf bank_mask:0xf bound_ctrl:1
	v_mov_b32_e32 v70, v68
	v_add_f32_dpp v64, v64, v64 row_ror:4 row_mask:0xf bank_mask:0xf bound_ctrl:1
	v_add_f32_e32 v63, 1.0, v63
	v_rcp_f32_e32 v63, v63
	v_add_f32_dpp v64, v64, v64 row_ror:8 row_mask:0xf bank_mask:0xf bound_ctrl:1
	v_mov_b32_e32 v65, v64
	s_nop 1
	v_permlane16_swap_b32_e32 v64, v65
	v_add_f32_e32 v64, v64, v65
	v_mov_b32_e32 v65, v64
	s_nop 1
	v_permlane32_swap_b32_e32 v64, v65
	v_add_f32_e32 v64, v64, v65
	s_nop 0
	v_add_f32_dpp v65, v76, v76 quad_perm:[1,0,3,2] row_mask:0xf bank_mask:0xf bound_ctrl:1
	v_mul_f32_e32 v64, 0xbfb8aa3b, v64
	v_exp_f32_e32 v64, v64
	v_add_f32_dpp v65, v65, v65 quad_perm:[2,3,0,1] row_mask:0xf bank_mask:0xf bound_ctrl:1
	v_mov_b32_e32 v76, v60
	s_nop 1
	v_permlane16_swap_b32_e32 v60, v76
	v_add_f32_dpp v65, v65, v65 row_ror:4 row_mask:0xf bank_mask:0xf bound_ctrl:1
	v_add_f32_e32 v64, 1.0, v64
	v_rcp_f32_e32 v102, v64
	v_add_f32_dpp v65, v65, v65 row_ror:8 row_mask:0xf bank_mask:0xf bound_ctrl:1
	v_mov_b32_e32 v66, v65
	s_nop 1
	v_permlane16_swap_b32_e32 v65, v66
	v_add_f32_e32 v65, v65, v66
	v_mov_b32_e32 v66, v65
	s_nop 1
	v_permlane32_swap_b32_e32 v65, v66
	v_add_f32_e32 v65, v65, v66
	s_nop 0
	v_add_f32_dpp v66, v74, v74 quad_perm:[1,0,3,2] row_mask:0xf bank_mask:0xf bound_ctrl:1
	v_mul_f32_e32 v65, 0xbfb8aa3b, v65
	v_exp_f32_e32 v65, v65
	v_add_f32_dpp v66, v66, v66 quad_perm:[2,3,0,1] row_mask:0xf bank_mask:0xf bound_ctrl:1
	v_add_f32_e32 v111, v14, v102
	v_add_f32_e32 v76, v60, v76
	v_add_f32_dpp v66, v66, v66 row_ror:4 row_mask:0xf bank_mask:0xf bound_ctrl:1
	v_add_f32_e32 v64, 1.0, v65
	v_rcp_f32_e32 v104, v64
	v_add_f32_dpp v66, v66, v66 row_ror:8 row_mask:0xf bank_mask:0xf bound_ctrl:1
	v_mov_b32_e32 v67, v66
	s_nop 1
	v_permlane16_swap_b32_e32 v66, v67
	v_add_f32_e32 v101, v66, v67
	s_nop 0
	v_add_f32_dpp v66, v78, v78 quad_perm:[1,0,3,2] row_mask:0xf bank_mask:0xf bound_ctrl:1
	v_pk_add_f32 v[64:65], v[12:13], v[62:63]
	v_add_f32_e32 v112, v15, v104
	v_add_f32_dpp v66, v66, v66 quad_perm:[2,3,0,1] row_mask:0xf bank_mask:0xf bound_ctrl:1
	v_cmp_gt_f32_e32 vcc, v65, v64
	v_add_f32_dpp v72, v72, v72 quad_perm:[2,3,0,1] row_mask:0xf bank_mask:0xf bound_ctrl:1
	v_add_f32_dpp v66, v66, v66 row_ror:4 row_mask:0xf bank_mask:0xf bound_ctrl:1
	v_cndmask_b32_e32 v60, v64, v65, vcc
	v_cmp_gt_f32_e64 s[6:7], v111, v60
	v_add_f32_dpp v66, v66, v66 row_ror:8 row_mask:0xf bank_mask:0xf bound_ctrl:1
	v_mov_b32_e32 v67, v66
	s_nop 1
	v_permlane16_swap_b32_e32 v66, v67
	v_add_f32_e32 v105, v66, v67
	s_nop 0
	v_add_f32_dpp v66, v80, v80 quad_perm:[1,0,3,2] row_mask:0xf bank_mask:0xf bound_ctrl:1
	v_cndmask_b32_e64 v80, 0, 1, vcc
	v_cndmask_b32_e64 v60, v60, v111, s[6:7]
	v_add_f32_dpp v66, v66, v66 quad_perm:[2,3,0,1] row_mask:0xf bank_mask:0xf bound_ctrl:1
	v_cndmask_b32_e64 v80, v80, 2, s[6:7]
	v_cmp_ngt_f32_e64 s[8:9], v112, v60
; #define WS_STEP(ctrl) v += __int_as_float(__builtin_amdgcn_update_dpp(0, __float_as_int(v), (ctrl), 0xf, 0xf, true))
; __device__ __forceinline__ float wave_sum(float v) {
;     ...
;     WS_STEP(0xB1); WS_STEP(0x4E); WS_STEP(0x124); WS_STEP(0x128);
;     ...
;     const auto r16 = __builtin_amdgcn_permlane16_swap(__float_as_uint(v), __float_as_uint(v), false, false);
;     v = __uint_as_float(r16[0]) + __uint_as_float(r16[1]);
;     const auto rr = __builtin_amdgcn_permlane32_swap(__float_as_uint(v), __float_as_uint(v), false, false);
;     return __uint_as_float(rr[0]) + __uint_as_float(rr[1]);
; }
	v_add_f32_dpp v66, v66, v66 row_ror:4 row_mask:0xf bank_mask:0xf bound_ctrl:1
	v_add_f32_dpp v72, v72, v72 row_ror:4 row_mask:0xf bank_mask:0xf bound_ctrl:1
	v_permlane16_swap_b32_e32 v68, v70
	v_add_f32_dpp v66, v66, v66 row_ror:8 row_mask:0xf bank_mask:0xf bound_ctrl:1
	v_mov_b32_e32 v67, v66
	s_nop 1
	v_permlane16_swap_b32_e32 v66, v67
	v_add_f32_e32 v107, v66, v67
	s_nop 0
	v_add_f32_dpp v66, v82, v82 quad_perm:[1,0,3,2] row_mask:0xf bank_mask:0xf bound_ctrl:1
	v_add_f32_dpp v72, v72, v72 row_ror:8 row_mask:0xf bank_mask:0xf bound_ctrl:1
	v_mov_b32_e32 v74, v72
	v_add_f32_dpp v66, v66, v66 quad_perm:[2,3,0,1] row_mask:0xf bank_mask:0xf bound_ctrl:1
	s_nop 0
	v_permlane16_swap_b32_e32 v72, v74
	v_add_f32_dpp v66, v66, v66 row_ror:4 row_mask:0xf bank_mask:0xf bound_ctrl:1
	v_add_f32_e32 v68, v68, v70
	v_add_f32_e32 v72, v72, v74
	v_add_f32_dpp v66, v66, v66 row_ror:8 row_mask:0xf bank_mask:0xf bound_ctrl:1
	v_mov_b32_e32 v67, v66
	s_nop 1
	v_permlane16_swap_b32_e32 v66, v67
	v_add_f32_e32 v109, v66, v67
	s_nop 0
	v_add_f32_dpp v66, v84, v84 quad_perm:[1,0,3,2] row_mask:0xf bank_mask:0xf bound_ctrl:1
	v_cndmask_b32_e64 v94, v112, v60, s[8:9]
	v_mov_b32_e32 v103, v101
	v_add_f32_dpp v66, v66, v66 quad_perm:[2,3,0,1] row_mask:0xf bank_mask:0xf bound_ctrl:1
	v_mov_b32_e32 v106, v105
	v_mov_b32_e32 v108, v107
	v_add_f32_dpp v66, v66, v66 row_ror:4 row_mask:0xf bank_mask:0xf bound_ctrl:1
	v_mov_b32_e32 v110, v109
	v_mov_b32_e32 v70, v68
	v_add_f32_dpp v66, v66, v66 row_ror:8 row_mask:0xf bank_mask:0xf bound_ctrl:1
	v_mov_b32_e32 v67, v66
	s_nop 1
	v_permlane16_swap_b32_e32 v66, v67
	v_add_f32_e32 v82, v66, v67
	s_nop 0
	v_add_f32_dpp v66, v86, v86 quad_perm:[1,0,3,2] row_mask:0xf bank_mask:0xf bound_ctrl:1
	v_mov_b32_e32 v84, v82
	v_mov_b32_e32 v74, v72
	v_add_f32_dpp v66, v66, v66 quad_perm:[2,3,0,1] row_mask:0xf bank_mask:0xf bound_ctrl:1
	v_mov_b32_e32 v78, v76
	v_permlane32_swap_b32_e32 v101, v103
	v_add_f32_dpp v66, v66, v66 row_ror:4 row_mask:0xf bank_mask:0xf bound_ctrl:1
	v_permlane32_swap_b32_e32 v105, v106
	s_nop 0
	v_add_f32_dpp v66, v66, v66 row_ror:8 row_mask:0xf bank_mask:0xf bound_ctrl:1
	v_mov_b32_e32 v67, v66
	s_nop 1
	v_permlane16_swap_b32_e32 v66, v67
	v_add_f32_e32 v86, v66, v67
	s_nop 0
	v_add_f32_dpp v66, v88, v88 quad_perm:[1,0,3,2] row_mask:0xf bank_mask:0xf bound_ctrl:1
	v_mov_b32_e32 v98, v86
	v_permlane32_swap_b32_e32 v107, v108
	v_add_f32_dpp v66, v66, v66 quad_perm:[2,3,0,1] row_mask:0xf bank_mask:0xf bound_ctrl:1
	v_permlane32_swap_b32_e32 v109, v110
	s_nop 0
	v_add_f32_dpp v66, v66, v66 row_ror:4 row_mask:0xf bank_mask:0xf bound_ctrl:1
	v_permlane32_swap_b32_e32 v82, v84
	s_nop 0
	v_add_f32_dpp v66, v66, v66 row_ror:8 row_mask:0xf bank_mask:0xf bound_ctrl:1
	v_mov_b32_e32 v67, v66
	s_nop 1
	v_permlane16_swap_b32_e32 v66, v67
	v_add_f32_e32 v88, v66, v67
	s_nop 0
	v_add_f32_dpp v66, v90, v90 quad_perm:[1,0,3,2] row_mask:0xf bank_mask:0xf bound_ctrl:1
	v_mov_b32_e32 v99, v88
	v_permlane32_swap_b32_e32 v86, v98
	v_add_f32_dpp v66, v66, v66 quad_perm:[2,3,0,1] row_mask:0xf bank_mask:0xf bound_ctrl:1
	v_permlane32_swap_b32_e32 v88, v99
	s_nop 0
	v_add_f32_dpp v66, v66, v66 row_ror:4 row_mask:0xf bank_mask:0xf bound_ctrl:1
	v_permlane32_swap_b32_e32 v68, v70
	s_nop 0
	v_add_f32_dpp v66, v66, v66 row_ror:8 row_mask:0xf bank_mask:0xf bound_ctrl:1
	v_mov_b32_e32 v67, v66
	s_nop 1
	v_permlane16_swap_b32_e32 v66, v67
	v_add_f32_e32 v90, v66, v67
	s_nop 0
	v_add_f32_dpp v66, v92, v92 quad_perm:[1,0,3,2] row_mask:0xf bank_mask:0xf bound_ctrl:1
	v_cndmask_b32_e64 v92, 3, v80, s[8:9]
	v_mov_b32_e32 v80, 0xff800000
	v_cmp_eq_u32_e64 s[10:11], 0, v92
	v_cmp_nlg_f32_e64 s[12:13], v64, v80
	s_or_b64 s[10:11], s[10:11], s[12:13]
	v_cndmask_b32_e64 v64, v64, v80, s[10:11]
	v_cmp_ne_u32_e64 s[12:13], 1, v92
	v_cmp_gt_f32_e64 s[14:15], v65, v64
	s_and_b64 s[12:13], s[12:13], s[14:15]
	v_cndmask_b32_e64 v64, v64, v65, s[12:13]
	v_add_f32_dpp v66, v66, v66 quad_perm:[2,3,0,1] row_mask:0xf bank_mask:0xf bound_ctrl:1
	v_cmp_ne_u32_e64 s[14:15], 2, v92
	v_cmp_gt_f32_e64 s[16:17], v111, v64
	v_add_f32_dpp v66, v66, v66 row_ror:4 row_mask:0xf bank_mask:0xf bound_ctrl:1
	s_and_b64 s[14:15], s[14:15], s[16:17]
	v_cndmask_b32_e64 v64, v64, v111, s[14:15]
	v_add_f32_dpp v66, v66, v66 row_ror:8 row_mask:0xf bank_mask:0xf bound_ctrl:1
	v_mov_b32_e32 v67, v66
	v_cmp_gt_f32_e64 s[16:17], v112, v64
	s_nop 0
	v_permlane16_swap_b32_e32 v66, v67
	s_and_b64 s[16:17], s[8:9], s[16:17]
	v_add_f32_e32 v66, v66, v67
	v_cndmask_b32_e64 v64, v64, v112, s[16:17]
	v_mov_b32_e32 v100, v90
	v_mov_b32_e32 v67, v66
	v_add_f32_e32 v94, v94, v64
	v_permlane32_swap_b32_e32 v90, v100
	v_permlane32_swap_b32_e32 v66, v67
	v_permlane32_swap_b32_e32 v72, v74
	v_permlane32_swap_b32_e32 v76, v78
	v_mov_b32_e32 v60, 1
	v_cmp_lg_f32_e64 s[18:19], v94, v80
	v_mov_b32_e32 v65, 0
	v_mov_b32_e32 v64, 0
	s_and_saveexec_b64 s[46:47], s[18:19]
	s_cbranch_execz .LBB0_891
	v_cndmask_b32_e64 v35, 0, 1, s[12:13]
	v_cndmask_b32_e64 v35, v35, 2, s[14:15]
	v_cndmask_b32_e64 v60, v35, 3, s[16:17]
	v_cndmask_b32_e64 v35, v62, 0, s[10:11]
	v_cndmask_b32_e64 v35, v35, v63, s[12:13]
	v_cndmask_b32_e32 v62, v62, v63, vcc
	v_cndmask_b32_e64 v35, v35, v102, s[14:15]
	v_cndmask_b32_e64 v62, v62, v102, s[6:7]
	v_cndmask_b32_e64 v35, v35, v104, s[16:17]
	v_cndmask_b32_e64 v65, v104, v62, s[8:9]
	v_mov_b32_e32 v64, v92
	v_mov_b32_e32 v80, v94

; #define AIN(k) ldptr(lds, (k))
; __global__ void __launch_bounds__(NTHREADS, 2) hybrid_fwd(Args a) {
;     ...
;             const float* lg = AIN(I_LN1G) + l * DM; const float* lb = AIN(I_LN1B) + l * DM;
.LBB0_909:
	s_or_b64 exec, exec, s[6:7]
	v_mbcnt_lo_u32_b32 v242, -1, 0
	v_mbcnt_hi_u32_b32 v242, -1, v242
	v_lshlrev_b32_e32 v242, 4, v242
	v_mov_b32_e32 v243, 0
	v_lshl_add_u64 v[244:245], s[34:35], 0, v[242:243]
	global_load_dwordx4 v[158:161], v[244:245], off
	global_load_dwordx4 v[162:165], v[244:245], off offset:1024
	global_load_dwordx4 v[166:169], v[244:245], off offset:2048
	global_load_dwordx4 v[170:173], v[244:245], off offset:3072
	v_add_co_u32_e32 v244, vcc, 0x1000, v244
	s_nop 1
	v_addc_co_u32_e32 v245, vcc, 0, v245, vcc
	global_load_dwordx4 v[174:177], v[244:245], off
	global_load_dwordx4 v[178:181], v[244:245], off offset:1024
	global_load_dwordx4 v[182:185], v[244:245], off offset:2048
	global_load_dwordx4 v[186:189], v[244:245], off offset:3072
	v_lshl_add_u64 v[244:245], s[36:37], 0, v[242:243]
	global_load_dwordx4 v[198:201], v[244:245], off
	global_load_dwordx4 v[202:205], v[244:245], off offset:1024
	global_load_dwordx4 v[216:219], v[244:245], off offset:2048
	global_load_dwordx4 v[220:223], v[244:245], off offset:3072
	v_add_co_u32_e32 v244, vcc, 0x1000, v244
	s_nop 1
	v_addc_co_u32_e32 v245, vcc, 0, v245, vcc
	global_load_dwordx4 v[224:227], v[244:245], off
	global_load_dwordx4 v[228:231], v[244:245], off offset:1024
	global_load_dwordx4 v[232:235], v[244:245], off offset:2048
	global_load_dwordx4 v[246:249], v[244:245], off offset:3072
	s_waitcnt vmcnt(0)
	v_lshlrev_b32_e32 v80, 16, v58
	v_and_b32_e32 v81, 0xffff0000, v58
	v_lshlrev_b32_e32 v78, 16, v59
	v_and_b32_e32 v79, 0xffff0000, v59
	v_add_f32_e32 v35, v80, v81
	v_add_f32_e32 v58, v78, v79
	v_lshlrev_b32_e32 v62, 16, v56
	v_and_b32_e32 v63, 0xffff0000, v56
	v_lshlrev_b32_e32 v60, 16, v57
	v_and_b32_e32 v61, 0xffff0000, v57
	v_add_f32_e32 v35, v35, v58
	v_add_f32_e32 v56, v62, v63
	v_add_f32_e32 v57, v60, v61
	v_lshlrev_b32_e32 v68, 16, v54
	v_and_b32_e32 v69, 0xffff0000, v54
	v_lshlrev_b32_e32 v70, 16, v55
	v_and_b32_e32 v71, 0xffff0000, v55
	v_add_f32_e32 v35, 0, v35
	v_add_f32_e32 v56, v56, v57
	v_add_f32_e32 v54, v68, v69
	v_add_f32_e32 v55, v70, v71
	v_lshlrev_b32_e32 v72, 16, v52
	v_and_b32_e32 v73, 0xffff0000, v52
	v_lshlrev_b32_e32 v74, 16, v53
	v_and_b32_e32 v75, 0xffff0000, v53
	v_add_f32_e32 v35, v35, v56
	v_add_f32_e32 v54, v54, v55
	v_add_f32_e32 v52, v72, v73
	v_add_f32_e32 v53, v74, v75
	v_lshlrev_b32_e32 v64, 16, v50
	v_and_b32_e32 v65, 0xffff0000, v50
	v_lshlrev_b32_e32 v66, 16, v51
	v_and_b32_e32 v67, 0xffff0000, v51
	v_add_f32_e32 v35, v35, v54
	v_add_f32_e32 v52, v52, v53
	v_add_f32_e32 v50, v64, v65
	v_add_f32_e32 v51, v66, v67
	v_lshlrev_b32_e32 v56, 16, v48
	v_and_b32_e32 v57, 0xffff0000, v48
	v_lshlrev_b32_e32 v58, 16, v49
	v_and_b32_e32 v59, 0xffff0000, v49
	v_add_f32_e32 v35, v35, v52
	v_add_f32_e32 v50, v50, v51
	v_add_f32_e32 v48, v56, v57
	v_add_f32_e32 v49, v58, v59
	v_lshlrev_b32_e32 v52, 16, v46
	v_and_b32_e32 v53, 0xffff0000, v46
	v_lshlrev_b32_e32 v54, 16, v47
	v_and_b32_e32 v55, 0xffff0000, v47
	v_add_f32_e32 v35, v35, v50
	v_add_f32_e32 v48, v48, v49
	v_add_f32_e32 v46, v52, v53
	v_add_f32_e32 v47, v54, v55
	v_add_f32_e32 v35, v35, v48
	v_add_f32_e32 v46, v46, v47
	v_add_f32_e32 v35, v35, v46
	v_lshlrev_b32_e32 v46, 16, v44
	v_and_b32_e32 v47, 0xffff0000, v44
	v_lshlrev_b32_e32 v44, 16, v45
	v_and_b32_e32 v45, 0xffff0000, v45
	v_add_f32_e32 v48, v46, v47
	v_add_f32_e32 v49, v44, v45
	v_add_f32_e32 v48, v48, v49
	v_add_f32_e32 v35, v35, v48
	s_mov_b64 s[6:7], s[34:35]
	s_mov_b64 s[8:9], s[36:37]
	v_add_f32_dpp v35, v35, v35 quad_perm:[1,0,3,2] row_mask:0xf bank_mask:0xf bound_ctrl:1
	v_lshl_add_u64 v[92:93], s[6:7], 0, v[192:193]
	s_lshl_b64 s[6:7], s[38:39], 11
	v_add_f32_dpp v35, v35, v35 quad_perm:[2,3,0,1] row_mask:0xf bank_mask:0xf bound_ctrl:1
	v_lshl_add_u64 v[94:95], s[8:9], 0, v[192:193]
	v_add_co_u32_e32 v98, vcc, s33, v92
	v_add_f32_dpp v35, v35, v35 row_ror:4 row_mask:0xf bank_mask:0xf bound_ctrl:1
	s_nop 0
	v_addc_co_u32_e32 v99, vcc, 0, v93, vcc
	v_add_f32_dpp v35, v35, v35 row_ror:8 row_mask:0xf bank_mask:0xf bound_ctrl:1
	v_mov_b32_e32 v48, v35
	s_nop 1
	v_permlane16_swap_b32_e32 v35, v48
	v_add_f32_e32 v35, v35, v48
	v_mov_b32_e32 v48, v35
	s_nop 1
	v_permlane32_swap_b32_e32 v35, v48
	v_add_f32_e32 v35, v35, v48
	v_fmac_f32_e32 v79, 0xba000000, v35
	v_fmac_f32_e32 v81, 0xba000000, v35
	v_fmac_f32_e32 v78, 0xba000000, v35
	v_fmac_f32_e32 v80, 0xba000000, v35
	v_mul_f32_e32 v48, v81, v81
	v_mul_f32_e32 v49, v79, v79
	v_fmac_f32_e32 v48, v80, v80
	v_fmac_f32_e32 v49, v78, v78
	v_fmac_f32_e32 v61, 0xba000000, v35
	v_fmac_f32_e32 v63, 0xba000000, v35
	v_add_f32_e32 v48, v48, v49
	v_fmac_f32_e32 v60, 0xba000000, v35
	v_fmac_f32_e32 v62, 0xba000000, v35
	v_mul_f32_e32 v49, v63, v63
	v_mul_f32_e32 v50, v61, v61
	v_fmac_f32_e32 v49, v62, v62
	v_fmac_f32_e32 v50, v60, v60
	v_add_f32_e32 v49, v49, v50
	v_add_f32_e32 v76, v48, v49
	s_nop 0
	v_fmac_f32_e32 v71, 0xba000000, v35
	v_fmac_f32_e32 v69, 0xba000000, v35
	v_fmac_f32_e32 v70, 0xba000000, v35
	v_fmac_f32_e32 v68, 0xba000000, v35
	v_mul_f32_e32 v77, v69, v69
	v_mul_f32_e32 v82, v71, v71
	v_fmac_f32_e32 v77, v68, v68
	v_fmac_f32_e32 v82, v70, v70
	v_add_f32_e32 v77, v77, v82
	v_fmac_f32_e32 v75, 0xba000000, v35
	v_fmac_f32_e32 v73, 0xba000000, v35
	v_add_f32_e32 v76, v76, v77
	v_fmac_f32_e32 v74, 0xba000000, v35
	v_fmac_f32_e32 v72, 0xba000000, v35
	v_mul_f32_e32 v77, v73, v73
	v_mul_f32_e32 v82, v75, v75
	v_fmac_f32_e32 v77, v72, v72
	v_fmac_f32_e32 v82, v74, v74
	v_add_f32_e32 v77, v77, v82
	v_fmac_f32_e32 v67, 0xba000000, v35
	v_fmac_f32_e32 v65, 0xba000000, v35
	v_add_f32_e32 v76, v76, v77
	v_fmac_f32_e32 v66, 0xba000000, v35
	v_fmac_f32_e32 v64, 0xba000000, v35
	v_mul_f32_e32 v77, v65, v65
	v_mul_f32_e32 v82, v67, v67
	v_fmac_f32_e32 v77, v64, v64
	v_fmac_f32_e32 v82, v66, v66
	v_add_f32_e32 v77, v77, v82
	v_fmac_f32_e32 v59, 0xba000000, v35
	v_fmac_f32_e32 v57, 0xba000000, v35
	v_add_f32_e32 v76, v76, v77
	v_fmac_f32_e32 v58, 0xba000000, v35
	v_fmac_f32_e32 v56, 0xba000000, v35
	v_mul_f32_e32 v77, v57, v57
	v_mul_f32_e32 v82, v59, v59
	v_fmac_f32_e32 v77, v56, v56
	v_fmac_f32_e32 v82, v58, v58
	v_add_f32_e32 v77, v77, v82
	v_fmac_f32_e32 v55, 0xba000000, v35
	v_fmac_f32_e32 v53, 0xba000000, v35
	v_add_f32_e32 v76, v76, v77
	v_fmac_f32_e32 v54, 0xba000000, v35
	v_fmac_f32_e32 v52, 0xba000000, v35
	v_mul_f32_e32 v77, v53, v53
	v_mul_f32_e32 v82, v55, v55
	v_fmac_f32_e32 v77, v52, v52
	v_fmac_f32_e32 v82, v54, v54
	v_add_f32_e32 v77, v77, v82
	v_fmac_f32_e32 v45, 0xba000000, v35
	v_fmac_f32_e32 v47, 0xba000000, v35
	v_add_f32_e32 v76, v76, v77
	v_fmac_f32_e32 v44, 0xba000000, v35
	v_fmac_f32_e32 v46, 0xba000000, v35
	v_mul_f32_e32 v35, v47, v47
	v_mul_f32_e32 v77, v45, v45
	v_fmac_f32_e32 v35, v46, v46
	v_fmac_f32_e32 v77, v44, v44
	v_add_f32_e32 v35, v35, v77
	v_add_f32_e32 v35, v76, v35
	v_lshl_add_u64 v[82:83], v[30:31], 0, s[6:7]
	v_add_co_u32_e32 v100, vcc, s33, v94
	v_add_f32_dpp v35, v35, v35 quad_perm:[1,0,3,2] row_mask:0xf bank_mask:0xf bound_ctrl:1
	s_nop 0
	v_addc_co_u32_e32 v101, vcc, 0, v95, vcc
	v_add_f32_dpp v35, v35, v35 quad_perm:[2,3,0,1] row_mask:0xf bank_mask:0xf bound_ctrl:1
	s_nop 1
	v_add_f32_dpp v35, v35, v35 row_ror:4 row_mask:0xf bank_mask:0xf bound_ctrl:1
	s_nop 1
	v_add_f32_dpp v35, v35, v35 row_ror:8 row_mask:0xf bank_mask:0xf bound_ctrl:1
	v_mov_b32_e32 v76, v35
	s_nop 1
	v_permlane16_swap_b32_e32 v35, v76
	v_add_f32_e32 v35, v35, v76
	v_mov_b32_e32 v76, v35
	s_nop 1
	v_permlane32_swap_b32_e32 v35, v76
	v_add_f32_e32 v35, v35, v76
	v_fmamk_f32 v35, v35, 0x3a000000, v207
	v_rsq_f32_e32 v96, v35
	v_lshl_add_u64 v[76:77], v[28:29], 0, s[44:45]
	v_pk_mul_f32 v[80:81], v[96:97], v[80:81] op_sel_hi:[0,1]
	s_waitcnt vmcnt(0) lgkmcnt(0)
	v_pk_fma_f32 v[48:49], v[158:159], v[80:81], v[198:199]
	v_mov_b32_e32 v81, 0
	v_med3_f32 v35, v48, s69, v208
	v_med3_f32 v80, v49, s69, v208
	v_cvt_pk_fp8_f32 v81, v35, v80
	v_pk_mul_f32 v[78:79], v[96:97], v[78:79] op_sel_hi:[0,1]
	v_pk_fma_f32 v[50:51], v[160:161], v[78:79], v[200:201]
	v_pk_mul_f32 v[62:63], v[96:97], v[62:63] op_sel_hi:[0,1]
	v_med3_f32 v35, v50, s69, v208
	v_med3_f32 v78, v51, s69, v208
	v_cvt_pk_fp8_f32 v81, v35, v78 op_sel:[0,0,1]
	v_cvt_pk_bf16_f32 v78, v48, v49
	v_cvt_pk_bf16_f32 v79, v50, v51
	global_store_dwordx2 v[76:77], v[78:79], off nt
	global_store_dword v[82:83], v81, off nt
	s_nop 0
	s_nop 0
	v_pk_mul_f32 v[88:89], v[96:97], v[60:61] op_sel_hi:[0,1]
	v_pk_mul_f32 v[68:69], v[96:97], v[68:69] op_sel_hi:[0,1]
	v_pk_mul_f32 v[72:73], v[96:97], v[72:73] op_sel_hi:[0,1]
	v_pk_mul_f32 v[74:75], v[96:97], v[74:75] op_sel_hi:[0,1]
	v_pk_mul_f32 v[64:65], v[96:97], v[64:65] op_sel_hi:[0,1]
	v_pk_mul_f32 v[66:67], v[96:97], v[66:67] op_sel_hi:[0,1]
	v_pk_mul_f32 v[56:57], v[96:97], v[56:57] op_sel_hi:[0,1]
	v_pk_mul_f32 v[58:59], v[96:97], v[58:59] op_sel_hi:[0,1]
	v_pk_mul_f32 v[52:53], v[96:97], v[52:53] op_sel_hi:[0,1]
	v_pk_mul_f32 v[54:55], v[96:97], v[54:55] op_sel_hi:[0,1]
	v_pk_mul_f32 v[46:47], v[96:97], v[46:47] op_sel_hi:[0,1]
	v_pk_mul_f32 v[44:45], v[96:97], v[44:45] op_sel_hi:[0,1]
	s_nop 0
	v_pk_fma_f32 v[60:61], v[162:163], v[62:63], v[202:203]
	s_nop 0
	v_med3_f32 v35, v60, s69, v208
	v_med3_f32 v62, v61, s69, v208
	v_mov_b32_e32 v84, 0
	v_cvt_pk_fp8_f32 v84, v35, v62
	v_pk_fma_f32 v[62:63], v[164:165], v[88:89], v[204:205]
	v_pk_mul_f32 v[88:89], v[96:97], v[70:71] op_sel_hi:[0,1]
	v_med3_f32 v35, v62, s69, v208
	v_med3_f32 v78, v63, s69, v208
	v_cvt_pk_fp8_f32 v84, v35, v78 op_sel:[0,0,1]
	v_cvt_pk_bf16_f32 v78, v60, v61
	v_cvt_pk_bf16_f32 v79, v62, v63
	global_store_dwordx2 v[76:77], v[78:79], off offset:512 nt
	global_store_dword v[82:83], v84, off offset:256 nt
	s_nop 0
	s_nop 0
	v_mov_b32_e32 v35, 0
	s_nop 0
	v_pk_fma_f32 v[70:71], v[166:167], v[68:69], v[216:217]
	s_nop 0
	v_med3_f32 v68, v70, s69, v208
	v_med3_f32 v69, v71, s69, v208
	v_cvt_pk_fp8_f32 v35, v68, v69
	v_pk_fma_f32 v[68:69], v[168:169], v[88:89], v[218:219]
	s_nop 0
	v_med3_f32 v78, v68, s69, v208
	v_med3_f32 v79, v69, s69, v208
	v_cvt_pk_fp8_f32 v35, v78, v79 op_sel:[0,0,1]
	v_cvt_pk_bf16_f32 v78, v70, v71
	v_cvt_pk_bf16_f32 v79, v68, v69
	global_store_dwordx2 v[76:77], v[78:79], off offset:1024 nt
	global_store_dword v[82:83], v35, off offset:512 nt
	s_nop 0
	v_mov_b32_e32 v35, 0
	s_nop 0
	v_pk_fma_f32 v[80:81], v[170:171], v[72:73], v[220:221]
	s_nop 0
	v_med3_f32 v72, v80, s69, v208
	v_med3_f32 v73, v81, s69, v208
	v_cvt_pk_fp8_f32 v35, v72, v73
	v_pk_fma_f32 v[78:79], v[172:173], v[74:75], v[222:223]
	s_nop 0
	v_med3_f32 v72, v78, s69, v208
	v_med3_f32 v73, v79, s69, v208
	v_cvt_pk_fp8_f32 v35, v72, v73 op_sel:[0,0,1]
	v_cvt_pk_bf16_f32 v72, v80, v81
	v_cvt_pk_bf16_f32 v73, v78, v79
	global_store_dwordx2 v[76:77], v[72:73], off offset:1536 nt
	global_store_dword v[82:83], v35, off offset:768 nt
	s_nop 0
	s_nop 0
	v_mov_b32_e32 v35, 0
	s_nop 0
	v_pk_fma_f32 v[86:87], v[174:175], v[64:65], v[224:225]
	s_nop 0
	v_med3_f32 v64, v86, s69, v208
	v_med3_f32 v65, v87, s69, v208
	v_cvt_pk_fp8_f32 v35, v64, v65
	v_pk_fma_f32 v[84:85], v[176:177], v[66:67], v[226:227]
	s_nop 0
	v_med3_f32 v64, v84, s69, v208
	v_med3_f32 v65, v85, s69, v208
	v_cvt_pk_fp8_f32 v35, v64, v65 op_sel:[0,0,1]
	v_cvt_pk_bf16_f32 v64, v86, v87
	v_cvt_pk_bf16_f32 v65, v84, v85
	global_store_dwordx2 v[76:77], v[64:65], off offset:2048 nt
	global_store_dword v[82:83], v35, off offset:1024 nt
	s_nop 0
	s_nop 0
	v_mov_b32_e32 v35, 0
	s_nop 0
	v_pk_fma_f32 v[90:91], v[178:179], v[56:57], v[228:229]
	s_nop 0
	v_med3_f32 v56, v90, s69, v208
	v_med3_f32 v57, v91, s69, v208
	v_cvt_pk_fp8_f32 v35, v56, v57
	v_pk_fma_f32 v[88:89], v[180:181], v[58:59], v[230:231]
	s_nop 0
	v_med3_f32 v56, v88, s69, v208
	v_med3_f32 v57, v89, s69, v208
	v_cvt_pk_fp8_f32 v35, v56, v57 op_sel:[0,0,1]
	v_cvt_pk_bf16_f32 v56, v90, v91
	v_cvt_pk_bf16_f32 v57, v88, v89
	global_store_dwordx2 v[76:77], v[56:57], off offset:2560 nt
	global_store_dword v[82:83], v35, off offset:1280 nt
	s_nop 0
	s_nop 0
	v_mov_b32_e32 v35, 0
	s_nop 0
	v_pk_fma_f32 v[94:95], v[182:183], v[52:53], v[232:233]
	s_nop 0
	v_med3_f32 v52, v94, s69, v208
	v_med3_f32 v53, v95, s69, v208
	v_cvt_pk_fp8_f32 v35, v52, v53
	v_pk_fma_f32 v[92:93], v[184:185], v[54:55], v[234:235]
	s_nop 0
	v_med3_f32 v52, v92, s69, v208
	v_med3_f32 v53, v93, s69, v208
	v_cvt_pk_fp8_f32 v35, v52, v53 op_sel:[0,0,1]
	v_cvt_pk_bf16_f32 v52, v94, v95
	v_cvt_pk_bf16_f32 v53, v92, v93
	global_store_dwordx2 v[76:77], v[52:53], off offset:3072 nt
	global_store_dword v[82:83], v35, off offset:1536 nt
	s_nop 0
	s_nop 0
	v_mov_b32_e32 v35, 0
	s_nop 0
	v_pk_fma_f32 v[96:97], v[186:187], v[46:47], v[246:247]
	s_nop 0
	v_med3_f32 v46, v96, s69, v208
	v_med3_f32 v47, v97, s69, v208
	v_mov_b32_e32 v52, 0
	v_cvt_pk_fp8_f32 v52, v46, v47
	v_pk_fma_f32 v[98:99], v[188:189], v[44:45], v[248:249]
	s_nop 0
	v_med3_f32 v44, v98, s69, v208
	v_med3_f32 v45, v99, s69, v208
	v_cvt_pk_fp8_f32 v52, v44, v45 op_sel:[0,0,1]
	v_cvt_pk_bf16_f32 v44, v96, v97
	v_cvt_pk_bf16_f32 v45, v98, v99
	global_store_dwordx2 v[76:77], v[44:45], off offset:3584 nt
	global_store_dword v[82:83], v52, off offset:1792 nt
	v_lshlrev_b32_e32 v102, 16, v42
	v_and_b32_e32 v103, 0xffff0000, v42
	v_lshlrev_b32_e32 v100, 16, v43
	v_and_b32_e32 v101, 0xffff0000, v43
	v_add_f32_e32 v42, v102, v103
	v_add_f32_e32 v43, v100, v101
	v_lshlrev_b32_e32 v74, 16, v40
	v_and_b32_e32 v75, 0xffff0000, v40
	v_lshlrev_b32_e32 v72, 16, v41
	v_and_b32_e32 v73, 0xffff0000, v41
	v_add_f32_e32 v42, v42, v43
	v_add_f32_e32 v40, v74, v75
	v_add_f32_e32 v41, v72, v73
	v_lshlrev_b32_e32 v64, 16, v38
	v_and_b32_e32 v65, 0xffff0000, v38
	v_lshlrev_b32_e32 v66, 16, v39
	v_and_b32_e32 v67, 0xffff0000, v39
	v_add_f32_e32 v42, 0, v42
	v_add_f32_e32 v40, v40, v41
	v_add_f32_e32 v38, v64, v65
	v_add_f32_e32 v39, v66, v67
	v_lshlrev_b32_e32 v56, 16, v36
	v_and_b32_e32 v57, 0xffff0000, v36
	v_lshlrev_b32_e32 v58, 16, v37
	v_and_b32_e32 v59, 0xffff0000, v37
	v_add_f32_e32 v40, v42, v40
	v_add_f32_e32 v38, v38, v39
	v_add_f32_e32 v36, v56, v57
	v_add_f32_e32 v37, v58, v59
	v_lshlrev_b32_e32 v52, 16, v22
	v_and_b32_e32 v53, 0xffff0000, v22
	v_lshlrev_b32_e32 v54, 16, v23
	v_and_b32_e32 v55, 0xffff0000, v23
	v_add_f32_e32 v38, v40, v38
	v_add_f32_e32 v36, v36, v37
	v_add_f32_e32 v22, v52, v53
	v_add_f32_e32 v23, v54, v55
	v_add_f32_e32 v36, v38, v36
	v_add_f32_e32 v22, v22, v23
	v_lshlrev_b32_e32 v44, 16, v20
	v_and_b32_e32 v45, 0xffff0000, v20
	v_lshlrev_b32_e32 v46, 16, v21
	v_and_b32_e32 v47, 0xffff0000, v21
	v_add_f32_e32 v22, v36, v22
	v_add_f32_e32 v20, v44, v45
	v_add_f32_e32 v21, v46, v47
	v_lshlrev_b32_e32 v36, 16, v18
	v_and_b32_e32 v37, 0xffff0000, v18
	v_lshlrev_b32_e32 v38, 16, v19
	v_and_b32_e32 v39, 0xffff0000, v19
	v_add_f32_e32 v20, v20, v21
	v_add_f32_e32 v18, v36, v37
	v_add_f32_e32 v19, v38, v39
	v_lshlrev_b32_e32 v42, 16, v16
	v_and_b32_e32 v43, 0xffff0000, v16
	v_lshlrev_b32_e32 v40, 16, v17
	v_and_b32_e32 v41, 0xffff0000, v17
	v_add_f32_e32 v20, v22, v20
	v_add_f32_e32 v18, v18, v19
	v_add_f32_e32 v16, v42, v43
	v_add_f32_e32 v17, v40, v41
	v_add_f32_e32 v18, v20, v18
	v_add_f32_e32 v16, v16, v17
	v_add_f32_e32 v16, v18, v16
	s_mov_b64 s[6:7], s[34:35]
	s_mov_b64 s[8:9], s[36:37]
	v_add_f32_dpp v16, v16, v16 quad_perm:[1,0,3,2] row_mask:0xf bank_mask:0xf bound_ctrl:1
	v_lshl_add_u64 v[108:109], s[6:7], 0, v[192:193]
	v_lshl_add_u64 v[104:105], v[28:29], 0, s[42:43]
	v_add_f32_dpp v16, v16, v16 quad_perm:[2,3,0,1] row_mask:0xf bank_mask:0xf bound_ctrl:1
	v_lshl_add_u64 v[106:107], s[8:9], 0, v[192:193]
	s_lshl_b64 s[6:7], s[40:41], 11
	v_add_f32_dpp v16, v16, v16 row_ror:4 row_mask:0xf bank_mask:0xf bound_ctrl:1
	v_lshl_add_u64 v[82:83], v[30:31], 0, s[6:7]
	s_nop 0
	v_add_f32_dpp v16, v16, v16 row_ror:8 row_mask:0xf bank_mask:0xf bound_ctrl:1
	v_mov_b32_e32 v17, v16
	s_nop 1
	v_permlane16_swap_b32_e32 v16, v17
	v_add_f32_e32 v16, v16, v17
	v_mov_b32_e32 v17, v16
	s_nop 1
	v_permlane32_swap_b32_e32 v16, v17
	v_add_f32_e32 v16, v16, v17
	v_fmac_f32_e32 v101, 0xba000000, v16
	v_fmac_f32_e32 v103, 0xba000000, v16
	v_fmac_f32_e32 v100, 0xba000000, v16
	v_fmac_f32_e32 v102, 0xba000000, v16
	v_mul_f32_e32 v17, v103, v103
	v_mul_f32_e32 v18, v101, v101
	v_fmac_f32_e32 v17, v102, v102
	v_fmac_f32_e32 v18, v100, v100
	v_fmac_f32_e32 v73, 0xba000000, v16
	v_fmac_f32_e32 v75, 0xba000000, v16
	v_add_f32_e32 v17, v17, v18
	v_fmac_f32_e32 v72, 0xba000000, v16
	v_fmac_f32_e32 v74, 0xba000000, v16
	v_mul_f32_e32 v18, v75, v75
	v_mul_f32_e32 v19, v73, v73
	v_fmac_f32_e32 v18, v74, v74
	v_fmac_f32_e32 v19, v72, v72
	v_add_f32_e32 v18, v18, v19
	v_fmac_f32_e32 v67, 0xba000000, v16
	v_fmac_f32_e32 v65, 0xba000000, v16
	v_add_f32_e32 v17, v17, v18
	v_fmac_f32_e32 v66, 0xba000000, v16
	v_fmac_f32_e32 v64, 0xba000000, v16
	v_mul_f32_e32 v18, v65, v65
	v_mul_f32_e32 v19, v67, v67
	v_fmac_f32_e32 v18, v64, v64
	v_fmac_f32_e32 v19, v66, v66
	v_add_f32_e32 v18, v18, v19
	v_fmac_f32_e32 v59, 0xba000000, v16
	v_fmac_f32_e32 v57, 0xba000000, v16
	v_add_f32_e32 v17, v17, v18
	v_fmac_f32_e32 v58, 0xba000000, v16
	v_fmac_f32_e32 v56, 0xba000000, v16
	v_mul_f32_e32 v18, v57, v57
	v_mul_f32_e32 v19, v59, v59
	v_fmac_f32_e32 v18, v56, v56
	v_fmac_f32_e32 v19, v58, v58
	v_add_f32_e32 v18, v18, v19
	v_fmac_f32_e32 v55, 0xba000000, v16
	v_fmac_f32_e32 v53, 0xba000000, v16
	v_add_f32_e32 v17, v17, v18
	v_fmac_f32_e32 v54, 0xba000000, v16
	v_fmac_f32_e32 v52, 0xba000000, v16
	v_mul_f32_e32 v18, v53, v53
	v_mul_f32_e32 v19, v55, v55
	v_fmac_f32_e32 v18, v52, v52
	v_fmac_f32_e32 v19, v54, v54
	v_add_f32_e32 v18, v18, v19
	v_fmac_f32_e32 v47, 0xba000000, v16
	v_fmac_f32_e32 v45, 0xba000000, v16
	v_add_f32_e32 v17, v17, v18
	v_fmac_f32_e32 v46, 0xba000000, v16
	v_fmac_f32_e32 v44, 0xba000000, v16
	v_mul_f32_e32 v18, v45, v45
	v_mul_f32_e32 v19, v47, v47
	v_fmac_f32_e32 v18, v44, v44
	v_fmac_f32_e32 v19, v46, v46
	v_add_f32_e32 v18, v18, v19
	v_fmac_f32_e32 v39, 0xba000000, v16
	v_fmac_f32_e32 v37, 0xba000000, v16
	v_add_f32_e32 v17, v17, v18
	v_fmac_f32_e32 v38, 0xba000000, v16
	v_fmac_f32_e32 v36, 0xba000000, v16
	v_mul_f32_e32 v18, v37, v37
	v_mul_f32_e32 v19, v39, v39
	v_fmac_f32_e32 v18, v36, v36
	v_fmac_f32_e32 v19, v38, v38
	v_add_f32_e32 v18, v18, v19
	v_fmac_f32_e32 v41, 0xba000000, v16
	v_fmac_f32_e32 v43, 0xba000000, v16
	v_add_f32_e32 v17, v17, v18
	v_fmac_f32_e32 v40, 0xba000000, v16
	v_fmac_f32_e32 v42, 0xba000000, v16
	v_mul_f32_e32 v16, v43, v43
	v_mul_f32_e32 v18, v41, v41
	v_fmac_f32_e32 v16, v42, v42
	v_fmac_f32_e32 v18, v40, v40
	v_add_f32_e32 v16, v16, v18
	v_add_f32_e32 v16, v17, v16
	s_nop 1
	v_add_f32_dpp v16, v16, v16 quad_perm:[1,0,3,2] row_mask:0xf bank_mask:0xf bound_ctrl:1
	s_nop 1
	v_add_f32_dpp v16, v16, v16 quad_perm:[2,3,0,1] row_mask:0xf bank_mask:0xf bound_ctrl:1
	s_nop 1
	v_add_f32_dpp v16, v16, v16 row_ror:4 row_mask:0xf bank_mask:0xf bound_ctrl:1
	s_nop 1
	v_add_f32_dpp v16, v16, v16 row_ror:8 row_mask:0xf bank_mask:0xf bound_ctrl:1
	v_mov_b32_e32 v17, v16
	s_nop 1
	v_permlane16_swap_b32_e32 v16, v17
	v_add_f32_e32 v16, v16, v17
	v_mov_b32_e32 v17, v16
	s_nop 1
	v_permlane32_swap_b32_e32 v16, v17
	v_add_f32_e32 v16, v16, v17
	v_fmamk_f32 v16, v16, 0x3a000000, v207
	v_rsq_f32_e32 v76, v16
	s_nop 0
	v_pk_mul_f32 v[102:103], v[76:77], v[102:103] op_sel_hi:[0,1]
	v_pk_mul_f32 v[100:101], v[76:77], v[100:101] op_sel_hi:[0,1]
	v_pk_mul_f32 v[74:75], v[76:77], v[74:75] op_sel_hi:[0,1]
	v_pk_mul_f32 v[72:73], v[76:77], v[72:73] op_sel_hi:[0,1]
	v_pk_mul_f32 v[110:111], v[76:77], v[64:65] op_sel_hi:[0,1]
	v_pk_mul_f32 v[64:65], v[76:77], v[66:67] op_sel_hi:[0,1]
	s_waitcnt vmcnt(0) lgkmcnt(0)
	v_pk_fma_f32 v[100:101], v[160:161], v[100:101], v[200:201]
	v_pk_fma_f32 v[102:103], v[158:159], v[102:103], v[198:199]
	v_mov_b32_e32 v20, 0
	v_cvt_pk_bf16_f32 v16, v102, v103
	v_cvt_pk_bf16_f32 v17, v100, v101
	global_store_dwordx2 v[104:105], v[16:17], off nt
	v_med3_f32 v16, v102, s69, v208
	v_med3_f32 v17, v103, s69, v208
	v_cvt_pk_fp8_f32 v20, v16, v17
	v_med3_f32 v18, v100, s69, v208
	v_med3_f32 v19, v101, s69, v208
	v_cvt_pk_fp8_f32 v20, v18, v19 op_sel:[0,0,1]
	global_store_dword v[82:83], v20, off nt
	s_nop 0
	s_nop 0
	s_nop 0
	v_pk_fma_f32 v[72:73], v[164:165], v[72:73], v[204:205]
	v_pk_fma_f32 v[74:75], v[162:163], v[74:75], v[202:203]
	v_mov_b32_e32 v20, 0
	v_cvt_pk_bf16_f32 v16, v74, v75
	v_cvt_pk_bf16_f32 v17, v72, v73
	global_store_dwordx2 v[104:105], v[16:17], off offset:512 nt
	v_med3_f32 v16, v74, s69, v208
	v_med3_f32 v17, v75, s69, v208
	v_cvt_pk_fp8_f32 v20, v16, v17
	v_med3_f32 v18, v72, s69, v208
	v_med3_f32 v19, v73, s69, v208
	v_cvt_pk_fp8_f32 v20, v18, v19 op_sel:[0,0,1]
	global_store_dword v[82:83], v20, off offset:256 nt
	s_nop 0
	s_nop 0
	s_nop 0
	v_pk_fma_f32 v[64:65], v[168:169], v[64:65], v[218:219]
	v_pk_fma_f32 v[66:67], v[166:167], v[110:111], v[216:217]
	v_mov_b32_e32 v20, 0
	v_cvt_pk_bf16_f32 v16, v66, v67
	v_cvt_pk_bf16_f32 v17, v64, v65
	global_store_dwordx2 v[104:105], v[16:17], off offset:1024 nt
	v_med3_f32 v16, v66, s69, v208
	v_med3_f32 v17, v67, s69, v208
	v_cvt_pk_fp8_f32 v20, v16, v17
	v_med3_f32 v18, v64, s69, v208
	v_med3_f32 v19, v65, s69, v208
	v_pk_mul_f32 v[110:111], v[76:77], v[56:57] op_sel_hi:[0,1]
	v_cvt_pk_fp8_f32 v20, v18, v19 op_sel:[0,0,1]
	v_pk_mul_f32 v[56:57], v[76:77], v[58:59] op_sel_hi:[0,1]
	global_store_dword v[82:83], v20, off offset:512 nt
	s_nop 0
	s_nop 0
	s_nop 0
	v_pk_fma_f32 v[56:57], v[172:173], v[56:57], v[222:223]
	v_pk_fma_f32 v[58:59], v[170:171], v[110:111], v[220:221]
	v_mov_b32_e32 v20, 0
	v_cvt_pk_bf16_f32 v16, v58, v59
	v_cvt_pk_bf16_f32 v17, v56, v57
	global_store_dwordx2 v[104:105], v[16:17], off offset:1536 nt
	v_med3_f32 v16, v58, s69, v208
	v_med3_f32 v17, v59, s69, v208
	v_cvt_pk_fp8_f32 v20, v16, v17
	v_med3_f32 v18, v56, s69, v208
	v_med3_f32 v19, v57, s69, v208
	v_add_co_u32_e32 v16, vcc, s33, v108
	v_cvt_pk_fp8_f32 v20, v18, v19 op_sel:[0,0,1]
	s_nop 0
	v_addc_co_u32_e32 v17, vcc, 0, v109, vcc
	v_add_co_u32_e32 v18, vcc, s33, v106
	global_store_dword v[82:83], v20, off offset:768 nt
	s_nop 0
	v_addc_co_u32_e32 v19, vcc, 0, v107, vcc
	s_nop 0
	v_pk_mul_f32 v[110:111], v[76:77], v[52:53] op_sel_hi:[0,1]
	v_pk_mul_f32 v[52:53], v[76:77], v[54:55] op_sel_hi:[0,1]
	v_mov_b32_e32 v77, 0
	s_nop 0
	v_pk_fma_f32 v[52:53], v[176:177], v[52:53], v[226:227]
	v_pk_fma_f32 v[54:55], v[174:175], v[110:111], v[224:225]
	v_med3_f32 v22, v52, s69, v208
	v_cvt_pk_bf16_f32 v20, v54, v55
	v_cvt_pk_bf16_f32 v21, v52, v53
	global_store_dwordx2 v[104:105], v[20:21], off offset:2048 nt
	v_med3_f32 v20, v54, s69, v208
	v_med3_f32 v21, v55, s69, v208
	v_cvt_pk_fp8_f32 v77, v20, v21
	v_med3_f32 v23, v53, s69, v208
; #define LAS __attribute__((address_space(3)))
; __global__ void __launch_bounds__(NTHREADS, 2) hybrid_fwd(Args a) {
;     ...
;                     f32x2 y2[8][4];
; #pragma unroll
;                     for (int j = 0; j < 8; ++j)
; #pragma unroll
;                         for (int c = 0; c < 4; ++c) y2[j][c] = (f32x2){ya[j][c], yb[j][c]};
;                     f32x2 acc2[16];
; #pragma unroll
;                     for (int e = 0; e < 16; ++e) acc2[e] = (f32x2){0.f, 0.f};
; #pragma unroll
;                     for (int j = 0; j < 8; ++j) {
; #pragma unroll
;                         for (int e = 0; e < 16; ++e) { const f32x4 w = *(const LAS f32x4*)(rwT + e * 2052 + j * 256 + lane * 4);
;                             acc2[e] += y2[j][0] * (f32x2){w[0], w[0]}; acc2[e] += y2[j][1] * (f32x2){w[1], w[1]};
;                             acc2[e] += y2[j][2] * (f32x2){w[2], w[2]}; acc2[e] += y2[j][3] * (f32x2){w[3], w[3]}; }
;                         __builtin_amdgcn_sched_barrier(0);
;                     }
	v_cvt_pk_fp8_f32 v77, v22, v23 op_sel:[0,0,1]
	global_store_dword v[82:83], v77, off offset:1024 nt
	s_nop 0
	v_pk_mul_f32 v[110:111], v[76:77], v[44:45] op_sel_hi:[0,1]
	v_pk_mul_f32 v[44:45], v[76:77], v[46:47] op_sel_hi:[0,1]
	v_mov_b32_e32 v77, 0
	s_nop 0
	v_pk_fma_f32 v[44:45], v[180:181], v[44:45], v[230:231]
	v_pk_fma_f32 v[46:47], v[178:179], v[110:111], v[228:229]
	v_med3_f32 v22, v44, s69, v208
	v_cvt_pk_bf16_f32 v20, v46, v47
	v_cvt_pk_bf16_f32 v21, v44, v45
	global_store_dwordx2 v[104:105], v[20:21], off offset:2560 nt
	v_med3_f32 v20, v46, s69, v208
	v_med3_f32 v21, v47, s69, v208
	v_cvt_pk_fp8_f32 v77, v20, v21
	v_med3_f32 v23, v45, s69, v208
	v_cvt_pk_fp8_f32 v77, v22, v23 op_sel:[0,0,1]
	global_store_dword v[82:83], v77, off offset:1280 nt
	s_nop 0
	v_pk_mul_f32 v[110:111], v[76:77], v[36:37] op_sel_hi:[0,1]
	v_pk_mul_f32 v[36:37], v[76:77], v[38:39] op_sel_hi:[0,1]
	v_mov_b32_e32 v77, 0
	s_nop 0
	v_pk_fma_f32 v[36:37], v[184:185], v[36:37], v[234:235]
	v_pk_fma_f32 v[38:39], v[182:183], v[110:111], v[232:233]
	v_med3_f32 v22, v36, s69, v208
	v_cvt_pk_bf16_f32 v20, v38, v39
	v_cvt_pk_bf16_f32 v21, v36, v37
	global_store_dwordx2 v[104:105], v[20:21], off offset:3072 nt
	v_med3_f32 v20, v38, s69, v208
	v_med3_f32 v21, v39, s69, v208
	v_cvt_pk_fp8_f32 v77, v20, v21
	v_med3_f32 v23, v37, s69, v208
	v_cvt_pk_fp8_f32 v77, v22, v23 op_sel:[0,0,1]
	global_store_dword v[82:83], v77, off offset:1536 nt
	s_nop 0
	v_pk_mul_f32 v[18:19], v[76:77], v[42:43] op_sel_hi:[0,1]
	v_pk_mul_f32 v[16:17], v[76:77], v[40:41] op_sel_hi:[0,1]
	v_mov_b32_e32 v40, 0
	s_nop 0
	v_pk_fma_f32 v[16:17], v[188:189], v[16:17], v[248:249]
	v_pk_fma_f32 v[18:19], v[186:187], v[18:19], v[246:247]
	v_med3_f32 v22, v16, s69, v208
	v_cvt_pk_bf16_f32 v20, v18, v19
	v_cvt_pk_bf16_f32 v21, v16, v17
	global_store_dwordx2 v[104:105], v[20:21], off offset:3584 nt
	v_med3_f32 v20, v18, s69, v208
	v_med3_f32 v21, v19, s69, v208
	v_cvt_pk_fp8_f32 v40, v20, v21
	v_med3_f32 v23, v17, s69, v208
	v_cvt_pk_fp8_f32 v40, v22, v23 op_sel:[0,0,1]
	global_store_dword v[82:83], v40, off offset:1792 nt
	v_add_u32_e32 v238, 0x10000, v25
	ds_read_b128 v[158:161], v25 offset:0
	ds_read_b128 v[162:165], v25 offset:8208
	ds_read_b128 v[166:169], v25 offset:16416
	ds_read_b128 v[170:173], v25 offset:24624
	ds_read_b128 v[174:177], v25 offset:32832
	ds_read_b128 v[178:181], v25 offset:41040
	ds_read_b128 v[182:185], v25 offset:49248
	ds_read_b128 v[186:189], v25 offset:57456
	v_mov_b32_e32 v76, v70
	v_mov_b32_e32 v77, v66
	v_mov_b32_e32 v66, v71
	v_mov_b32_e32 v82, v68
	v_mov_b32_e32 v83, v64
	v_mov_b32_e32 v64, v69
	v_mov_b32_e32 v68, v80
	v_mov_b32_e32 v69, v58
	v_mov_b32_e32 v58, v81
	v_mov_b32_e32 v70, v78
	v_mov_b32_e32 v71, v56
	v_mov_b32_e32 v56, v79
	ds_read_b128 v[198:201], v238 offset:128
	v_mov_b32_e32 v108, v48
	v_mov_b32_e32 v109, v102
	v_mov_b32_e32 v102, v49
	v_mov_b32_e32 v106, v62
	v_mov_b32_e32 v107, v72
	v_mov_b32_e32 v72, v63
	v_mov_b32_e32 v62, v84
	v_mov_b32_e32 v63, v52
	v_mov_b32_e32 v52, v85
	s_waitcnt lgkmcnt(8)
	v_pk_fma_f32 v[84:85], v[108:109], v[158:159], 0 op_sel_hi:[1,0,0]
	v_mov_b32_e32 v104, v60
	v_mov_b32_e32 v105, v74
	v_mov_b32_e32 v74, v61
	v_mov_b32_e32 v60, v86
	v_mov_b32_e32 v61, v54
	v_mov_b32_e32 v54, v87
	v_pk_fma_f32 v[78:79], v[158:159], v[102:103], v[84:85] op_sel:[1,0,0]
	ds_read_b128 v[202:205], v238 offset:8336
	v_mov_b32_e32 v110, v50
	v_mov_b32_e32 v111, v100
	v_mov_b32_e32 v100, v51
	v_pk_fma_f32 v[78:79], v[160:161], v[110:111], v[78:79] op_sel_hi:[0,1,1]
	v_mov_b32_e32 v80, v161
	v_pk_fma_f32 v[78:79], v[80:81], v[100:101], v[78:79] op_sel_hi:[0,1,1]
	s_waitcnt lgkmcnt(8)
	v_pk_fma_f32 v[80:81], v[108:109], v[162:163], 0 op_sel_hi:[1,0,0]
	v_mov_b32_e32 v50, v88
	v_pk_fma_f32 v[80:81], v[162:163], v[102:103], v[80:81] op_sel:[1,0,0]
	v_mov_b32_e32 v84, v165
	v_pk_fma_f32 v[80:81], v[164:165], v[110:111], v[80:81] op_sel_hi:[0,1,1]
	v_pk_fma_f32 v[120:121], v[84:85], v[100:101], v[80:81] op_sel_hi:[0,1,1]
	ds_read_b128 v[216:219], v238 offset:16544
	v_mov_b32_e32 v51, v44
	v_mov_b32_e32 v44, v89
	v_mov_b32_e32 v48, v90
	v_mov_b32_e32 v49, v46
	s_waitcnt lgkmcnt(8)
	v_pk_fma_f32 v[80:81], v[108:109], v[166:167], 0 op_sel_hi:[1,0,0]
	v_mov_b32_e32 v46, v91
	v_pk_fma_f32 v[80:81], v[166:167], v[102:103], v[80:81] op_sel:[1,0,0]
	v_mov_b32_e32 v84, v169
	v_pk_fma_f32 v[80:81], v[168:169], v[110:111], v[80:81] op_sel_hi:[0,1,1]
	v_pk_fma_f32 v[122:123], v[84:85], v[100:101], v[80:81] op_sel_hi:[0,1,1]
	ds_read_b128 v[220:223], v238 offset:24752
	v_mov_b32_e32 v42, v92
	v_mov_b32_e32 v43, v36
	v_mov_b32_e32 v36, v93
	v_mov_b32_e32 v40, v94
	s_waitcnt lgkmcnt(8)
	v_pk_fma_f32 v[80:81], v[108:109], v[170:171], 0 op_sel_hi:[1,0,0]
	v_mov_b32_e32 v41, v38
	v_pk_fma_f32 v[80:81], v[170:171], v[102:103], v[80:81] op_sel:[1,0,0]
	v_mov_b32_e32 v84, v173
	v_pk_fma_f32 v[80:81], v[172:173], v[110:111], v[80:81] op_sel_hi:[0,1,1]
	v_pk_fma_f32 v[80:81], v[84:85], v[100:101], v[80:81] op_sel_hi:[0,1,1]
	ds_read_b128 v[224:227], v238 offset:32960
	v_mov_b32_e32 v38, v95
	v_mov_b32_e32 v22, v96
	v_mov_b32_e32 v23, v18
	v_mov_b32_e32 v18, v97
	s_waitcnt lgkmcnt(8)
	v_pk_fma_f32 v[88:89], v[108:109], v[174:175], 0 op_sel_hi:[1,0,0]
	v_mov_b32_e32 v20, v98
	v_pk_fma_f32 v[84:85], v[174:175], v[102:103], v[88:89] op_sel:[1,0,0]
	v_mov_b32_e32 v21, v16
	v_pk_fma_f32 v[84:85], v[176:177], v[110:111], v[84:85] op_sel_hi:[0,1,1]
	v_mov_b32_e32 v86, v177
	v_pk_fma_f32 v[84:85], v[86:87], v[100:101], v[84:85] op_sel_hi:[0,1,1]
	ds_read_b128 v[228:231], v238 offset:41168
	v_mov_b32_e32 v16, v99
	s_waitcnt lgkmcnt(8)
; #define LAS __attribute__((address_space(3)))
; __global__ void __launch_bounds__(NTHREADS, 2) hybrid_fwd(Args a) {
;     ...
;                     for (int j = 0; j < 8; ++j) {
; #pragma unroll
;                         for (int e = 0; e < 16; ++e) { const f32x4 w = *(const LAS f32x4*)(rwT + e * 2052 + j * 256 + lane * 4);
;                             acc2[e] += y2[j][0] * (f32x2){w[0], w[0]}; acc2[e] += y2[j][1] * (f32x2){w[1], w[1]};
;                             acc2[e] += y2[j][2] * (f32x2){w[2], w[2]}; acc2[e] += y2[j][3] * (f32x2){w[3], w[3]}; }
;                         __builtin_amdgcn_sched_barrier(0);
;                     }
	v_pk_fma_f32 v[90:91], v[108:109], v[178:179], 0 op_sel_hi:[1,0,0]
	s_nop 0
	v_pk_fma_f32 v[86:87], v[178:179], v[102:103], v[90:91] op_sel:[1,0,0]
	s_nop 0
	v_pk_fma_f32 v[86:87], v[180:181], v[110:111], v[86:87] op_sel_hi:[0,1,1]
	v_mov_b32_e32 v88, v181
	v_pk_fma_f32 v[86:87], v[88:89], v[100:101], v[86:87] op_sel_hi:[0,1,1]
	ds_read_b128 v[232:235], v238 offset:49376
	s_waitcnt lgkmcnt(8)
	v_pk_fma_f32 v[92:93], v[108:109], v[182:183], 0 op_sel_hi:[1,0,0]
	s_nop 0
	v_pk_fma_f32 v[88:89], v[182:183], v[102:103], v[92:93] op_sel:[1,0,0]
	s_nop 0
	v_pk_fma_f32 v[88:89], v[184:185], v[110:111], v[88:89] op_sel_hi:[0,1,1]
	v_mov_b32_e32 v90, v185
	v_pk_fma_f32 v[88:89], v[90:91], v[100:101], v[88:89] op_sel_hi:[0,1,1]
	ds_read_b128 v[242:245], v238 offset:57584
	s_waitcnt lgkmcnt(8)
	v_pk_fma_f32 v[94:95], v[108:109], v[186:187], 0 op_sel_hi:[1,0,0]
	s_nop 0
	v_pk_fma_f32 v[90:91], v[186:187], v[102:103], v[94:95] op_sel:[1,0,0]
	s_nop 0
	v_pk_fma_f32 v[90:91], v[188:189], v[110:111], v[90:91] op_sel_hi:[0,1,1]
	v_mov_b32_e32 v92, v189
	v_pk_fma_f32 v[90:91], v[92:93], v[100:101], v[90:91] op_sel_hi:[0,1,1]
	ds_read_b128 v[246:249], v25 offset:1024
	s_waitcnt lgkmcnt(8)
	v_pk_fma_f32 v[96:97], v[108:109], v[198:199], 0 op_sel_hi:[1,0,0]
	s_nop 0
	v_pk_fma_f32 v[92:93], v[198:199], v[102:103], v[96:97] op_sel:[1,0,0]
	s_nop 0
	v_pk_fma_f32 v[92:93], v[200:201], v[110:111], v[92:93] op_sel_hi:[0,1,1]
	v_mov_b32_e32 v94, v201
	v_pk_fma_f32 v[92:93], v[94:95], v[100:101], v[92:93] op_sel_hi:[0,1,1]
	ds_read_b128 v[250:253], v25 offset:9232
	s_waitcnt lgkmcnt(8)
	v_pk_fma_f32 v[98:99], v[108:109], v[202:203], 0 op_sel_hi:[1,0,0]
	s_nop 0
	v_pk_fma_f32 v[94:95], v[202:203], v[102:103], v[98:99] op_sel:[1,0,0]
	s_nop 0
	v_pk_fma_f32 v[94:95], v[204:205], v[110:111], v[94:95] op_sel_hi:[0,1,1]
	v_mov_b32_e32 v96, v205
	v_pk_fma_f32 v[94:95], v[96:97], v[100:101], v[94:95] op_sel_hi:[0,1,1]
	ds_read_b128 v[158:161], v25 offset:17440
	s_waitcnt lgkmcnt(8)
	v_pk_fma_f32 v[112:113], v[108:109], v[216:217], 0 op_sel_hi:[1,0,0]
	s_nop 0
	v_pk_fma_f32 v[96:97], v[216:217], v[102:103], v[112:113] op_sel:[1,0,0]
	ds_read_b128 v[162:165], v25 offset:25648
	v_pk_fma_f32 v[96:97], v[218:219], v[110:111], v[96:97] op_sel_hi:[0,1,1]
	v_mov_b32_e32 v98, v219
	v_pk_fma_f32 v[96:97], v[98:99], v[100:101], v[96:97] op_sel_hi:[0,1,1]
	s_waitcnt lgkmcnt(8)
	v_pk_fma_f32 v[98:99], v[108:109], v[220:221], 0 op_sel_hi:[1,0,0]
	s_nop 0
	v_pk_fma_f32 v[98:99], v[220:221], v[102:103], v[98:99] op_sel:[1,0,0]
	v_mov_b32_e32 v112, v223
	v_pk_fma_f32 v[98:99], v[222:223], v[110:111], v[98:99] op_sel_hi:[0,1,1]
	v_pk_fma_f32 v[98:99], v[112:113], v[100:101], v[98:99] op_sel_hi:[0,1,1]
	ds_read_b128 v[166:169], v25 offset:33856
	s_waitcnt lgkmcnt(8)
	v_pk_fma_f32 v[116:117], v[108:109], v[224:225], 0 op_sel_hi:[1,0,0]
	s_nop 0
	v_pk_fma_f32 v[112:113], v[224:225], v[102:103], v[116:117] op_sel:[1,0,0]
	s_nop 0
	v_pk_fma_f32 v[112:113], v[226:227], v[110:111], v[112:113] op_sel_hi:[0,1,1]
	v_mov_b32_e32 v114, v227
	v_pk_fma_f32 v[112:113], v[114:115], v[100:101], v[112:113] op_sel_hi:[0,1,1]
	ds_read_b128 v[170:173], v25 offset:42064
	s_waitcnt lgkmcnt(8)
	v_pk_fma_f32 v[118:119], v[108:109], v[228:229], 0 op_sel_hi:[1,0,0]
	s_nop 0
	v_pk_fma_f32 v[114:115], v[228:229], v[102:103], v[118:119] op_sel:[1,0,0]
	s_nop 0
	v_pk_fma_f32 v[114:115], v[230:231], v[110:111], v[114:115] op_sel_hi:[0,1,1]
	v_mov_b32_e32 v116, v231
	v_pk_fma_f32 v[114:115], v[116:117], v[100:101], v[114:115] op_sel_hi:[0,1,1]
	ds_read_b128 v[174:177], v25 offset:50272
	s_waitcnt lgkmcnt(8)
	v_pk_fma_f32 v[124:125], v[108:109], v[232:233], 0 op_sel_hi:[1,0,0]
	s_nop 0
	v_pk_fma_f32 v[116:117], v[232:233], v[102:103], v[124:125] op_sel:[1,0,0]
	ds_read_b128 v[178:181], v25 offset:58480
	v_pk_fma_f32 v[116:117], v[234:235], v[110:111], v[116:117] op_sel_hi:[0,1,1]
	v_mov_b32_e32 v118, v235
	v_pk_fma_f32 v[116:117], v[118:119], v[100:101], v[116:117] op_sel_hi:[0,1,1]
	s_waitcnt lgkmcnt(8)
	v_pk_fma_f32 v[108:109], v[108:109], v[242:243], 0 op_sel_hi:[1,0,0]
	s_nop 0
	v_pk_fma_f32 v[102:103], v[242:243], v[102:103], v[108:109] op_sel:[1,0,0]
	v_mov_b32_e32 v108, v245
	v_pk_fma_f32 v[102:103], v[244:245], v[110:111], v[102:103] op_sel_hi:[0,1,1]
	v_pk_fma_f32 v[118:119], v[108:109], v[100:101], v[102:103] op_sel_hi:[0,1,1]
	ds_read_b128 v[182:185], v238 offset:1152
	s_waitcnt lgkmcnt(8)
	v_pk_fma_f32 v[78:79], v[104:105], v[246:247], v[78:79] op_sel_hi:[1,0,1]
	s_nop 0
	v_pk_fma_f32 v[78:79], v[246:247], v[74:75], v[78:79] op_sel:[1,0,0]
	v_mov_b32_e32 v100, v249
	v_pk_fma_f32 v[78:79], v[248:249], v[106:107], v[78:79] op_sel_hi:[0,1,1]
	v_pk_fma_f32 v[78:79], v[100:101], v[72:73], v[78:79] op_sel_hi:[0,1,1]
	ds_read_b128 v[186:189], v238 offset:9360
	s_waitcnt lgkmcnt(8)
	v_pk_fma_f32 v[108:109], v[104:105], v[250:251], v[120:121] op_sel_hi:[1,0,1]
	s_nop 0
	v_pk_fma_f32 v[100:101], v[250:251], v[74:75], v[108:109] op_sel:[1,0,0]
	s_nop 0
	v_pk_fma_f32 v[100:101], v[252:253], v[106:107], v[100:101] op_sel_hi:[0,1,1]
	v_mov_b32_e32 v102, v253
	v_pk_fma_f32 v[120:121], v[102:103], v[72:73], v[100:101] op_sel_hi:[0,1,1]
	ds_read_b128 v[198:201], v238 offset:17568
	s_waitcnt lgkmcnt(8)
	v_pk_fma_f32 v[108:109], v[104:105], v[158:159], v[122:123] op_sel_hi:[1,0,1]
	s_nop 0
	v_pk_fma_f32 v[100:101], v[158:159], v[74:75], v[108:109] op_sel:[1,0,0]
	ds_read_b128 v[202:205], v238 offset:25776
	v_pk_fma_f32 v[100:101], v[160:161], v[106:107], v[100:101] op_sel_hi:[0,1,1]
	v_mov_b32_e32 v102, v161
	v_pk_fma_f32 v[100:101], v[102:103], v[72:73], v[100:101] op_sel_hi:[0,1,1]
	s_waitcnt lgkmcnt(8)
; #define LAS __attribute__((address_space(3)))
; __global__ void __launch_bounds__(NTHREADS, 2) hybrid_fwd(Args a) {
;     ...
;                     for (int j = 0; j < 8; ++j) {
; #pragma unroll
;                         for (int e = 0; e < 16; ++e) { const f32x4 w = *(const LAS f32x4*)(rwT + e * 2052 + j * 256 + lane * 4);
;                             acc2[e] += y2[j][0] * (f32x2){w[0], w[0]}; acc2[e] += y2[j][1] * (f32x2){w[1], w[1]};
;                             acc2[e] += y2[j][2] * (f32x2){w[2], w[2]}; acc2[e] += y2[j][3] * (f32x2){w[3], w[3]}; }
;                         __builtin_amdgcn_sched_barrier(0);
;                     }
	v_pk_fma_f32 v[80:81], v[104:105], v[162:163], v[80:81] op_sel_hi:[1,0,1]
	s_nop 0
	v_pk_fma_f32 v[80:81], v[162:163], v[74:75], v[80:81] op_sel:[1,0,0]
	v_mov_b32_e32 v102, v165
	v_pk_fma_f32 v[80:81], v[164:165], v[106:107], v[80:81] op_sel_hi:[0,1,1]
	ds_read_b128 v[216:219], v238 offset:33984
	v_pk_fma_f32 v[80:81], v[102:103], v[72:73], v[80:81] op_sel_hi:[0,1,1]
	s_waitcnt lgkmcnt(8)
	v_pk_fma_f32 v[84:85], v[104:105], v[166:167], v[84:85] op_sel_hi:[1,0,1]
	s_nop 0
	v_pk_fma_f32 v[84:85], v[166:167], v[74:75], v[84:85] op_sel:[1,0,0]
	v_mov_b32_e32 v102, v169
	v_pk_fma_f32 v[84:85], v[168:169], v[106:107], v[84:85] op_sel_hi:[0,1,1]
	ds_read_b128 v[220:223], v238 offset:42192
	v_pk_fma_f32 v[84:85], v[102:103], v[72:73], v[84:85] op_sel_hi:[0,1,1]
	s_waitcnt lgkmcnt(8)
	v_pk_fma_f32 v[86:87], v[104:105], v[170:171], v[86:87] op_sel_hi:[1,0,1]
	s_nop 0
	v_pk_fma_f32 v[86:87], v[170:171], v[74:75], v[86:87] op_sel:[1,0,0]
	v_mov_b32_e32 v102, v173
	v_pk_fma_f32 v[86:87], v[172:173], v[106:107], v[86:87] op_sel_hi:[0,1,1]
	ds_read_b128 v[224:227], v238 offset:50400
	v_pk_fma_f32 v[86:87], v[102:103], v[72:73], v[86:87] op_sel_hi:[0,1,1]
	s_waitcnt lgkmcnt(8)
	v_pk_fma_f32 v[88:89], v[104:105], v[174:175], v[88:89] op_sel_hi:[1,0,1]
	s_nop 0
	v_pk_fma_f32 v[88:89], v[174:175], v[74:75], v[88:89] op_sel:[1,0,0]
	v_mov_b32_e32 v102, v177
	v_pk_fma_f32 v[88:89], v[176:177], v[106:107], v[88:89] op_sel_hi:[0,1,1]
	ds_read_b128 v[228:231], v238 offset:58608
	v_pk_fma_f32 v[88:89], v[102:103], v[72:73], v[88:89] op_sel_hi:[0,1,1]
	s_waitcnt lgkmcnt(8)
	v_pk_fma_f32 v[90:91], v[104:105], v[178:179], v[90:91] op_sel_hi:[1,0,1]
	s_nop 0
	v_pk_fma_f32 v[90:91], v[178:179], v[74:75], v[90:91] op_sel:[1,0,0]
	v_mov_b32_e32 v102, v181
	v_pk_fma_f32 v[90:91], v[180:181], v[106:107], v[90:91] op_sel_hi:[0,1,1]
	ds_read_b128 v[232:235], v25 offset:2048
	v_pk_fma_f32 v[90:91], v[102:103], v[72:73], v[90:91] op_sel_hi:[0,1,1]
	s_waitcnt lgkmcnt(8)
	v_pk_fma_f32 v[92:93], v[104:105], v[182:183], v[92:93] op_sel_hi:[1,0,1]
	s_nop 0
	v_pk_fma_f32 v[92:93], v[182:183], v[74:75], v[92:93] op_sel:[1,0,0]
	v_mov_b32_e32 v102, v185
	v_pk_fma_f32 v[92:93], v[184:185], v[106:107], v[92:93] op_sel_hi:[0,1,1]
	ds_read_b128 v[242:245], v25 offset:10256
	v_pk_fma_f32 v[92:93], v[102:103], v[72:73], v[92:93] op_sel_hi:[0,1,1]
	s_waitcnt lgkmcnt(8)
	v_pk_fma_f32 v[94:95], v[104:105], v[186:187], v[94:95] op_sel_hi:[1,0,1]
	s_nop 0
	v_pk_fma_f32 v[94:95], v[186:187], v[74:75], v[94:95] op_sel:[1,0,0]
	v_mov_b32_e32 v102, v189
	v_pk_fma_f32 v[94:95], v[188:189], v[106:107], v[94:95] op_sel_hi:[0,1,1]
	ds_read_b128 v[246:249], v25 offset:18464
	v_pk_fma_f32 v[94:95], v[102:103], v[72:73], v[94:95] op_sel_hi:[0,1,1]
	s_waitcnt lgkmcnt(8)
	v_pk_fma_f32 v[96:97], v[104:105], v[198:199], v[96:97] op_sel_hi:[1,0,1]
	s_nop 0
	v_pk_fma_f32 v[96:97], v[198:199], v[74:75], v[96:97] op_sel:[1,0,0]
	v_mov_b32_e32 v102, v201
	v_pk_fma_f32 v[96:97], v[200:201], v[106:107], v[96:97] op_sel_hi:[0,1,1]
	ds_read_b128 v[250:253], v25 offset:26672
	v_pk_fma_f32 v[96:97], v[102:103], v[72:73], v[96:97] op_sel_hi:[0,1,1]
	s_waitcnt lgkmcnt(8)
	v_pk_fma_f32 v[98:99], v[104:105], v[202:203], v[98:99] op_sel_hi:[1,0,1]
	s_nop 0
	v_pk_fma_f32 v[98:99], v[202:203], v[74:75], v[98:99] op_sel:[1,0,0]
	v_mov_b32_e32 v102, v205
	v_pk_fma_f32 v[98:99], v[204:205], v[106:107], v[98:99] op_sel_hi:[0,1,1]
	ds_read_b128 v[162:165], v25 offset:34880
	v_pk_fma_f32 v[98:99], v[102:103], v[72:73], v[98:99] op_sel_hi:[0,1,1]
	s_waitcnt lgkmcnt(8)
	v_pk_fma_f32 v[102:103], v[104:105], v[216:217], v[112:113] op_sel_hi:[1,0,1]
	s_nop 0
	v_pk_fma_f32 v[102:103], v[216:217], v[74:75], v[102:103] op_sel:[1,0,0]
	v_mov_b32_e32 v108, v219
	v_pk_fma_f32 v[102:103], v[218:219], v[106:107], v[102:103] op_sel_hi:[0,1,1]
	v_pk_fma_f32 v[102:103], v[108:109], v[72:73], v[102:103] op_sel_hi:[0,1,1]
	ds_read_b128 v[166:169], v25 offset:43088
	s_waitcnt lgkmcnt(8)
	v_pk_fma_f32 v[112:113], v[104:105], v[220:221], v[114:115] op_sel_hi:[1,0,1]
	s_nop 0
	v_pk_fma_f32 v[108:109], v[220:221], v[74:75], v[112:113] op_sel:[1,0,0]
	s_nop 0
	v_pk_fma_f32 v[108:109], v[222:223], v[106:107], v[108:109] op_sel_hi:[0,1,1]
	v_mov_b32_e32 v110, v223
	v_pk_fma_f32 v[108:109], v[110:111], v[72:73], v[108:109] op_sel_hi:[0,1,1]
	ds_read_b128 v[170:173], v25 offset:51296
	s_waitcnt lgkmcnt(8)
	v_pk_fma_f32 v[114:115], v[104:105], v[224:225], v[116:117] op_sel_hi:[1,0,1]
	s_nop 0
	v_pk_fma_f32 v[110:111], v[224:225], v[74:75], v[114:115] op_sel:[1,0,0]
	s_nop 0
	v_pk_fma_f32 v[110:111], v[226:227], v[106:107], v[110:111] op_sel_hi:[0,1,1]
	v_mov_b32_e32 v112, v227
	v_pk_fma_f32 v[110:111], v[112:113], v[72:73], v[110:111] op_sel_hi:[0,1,1]
	ds_read_b128 v[174:177], v25 offset:59504
	s_waitcnt lgkmcnt(8)
	v_pk_fma_f32 v[104:105], v[104:105], v[228:229], v[118:119] op_sel_hi:[1,0,1]
	s_nop 0
	v_pk_fma_f32 v[74:75], v[228:229], v[74:75], v[104:105] op_sel:[1,0,0]
	v_mov_b32_e32 v104, v231
	v_pk_fma_f32 v[74:75], v[230:231], v[106:107], v[74:75] op_sel_hi:[0,1,1]
	v_pk_fma_f32 v[104:105], v[104:105], v[72:73], v[74:75] op_sel_hi:[0,1,1]
	ds_read_b128 v[178:181], v238 offset:2176
	ds_read_b128 v[182:185], v238 offset:10384
	s_waitcnt lgkmcnt(8)
	v_pk_fma_f32 v[78:79], v[76:77], v[232:233], v[78:79] op_sel_hi:[1,0,1]
	s_nop 0
	v_pk_fma_f32 v[72:73], v[232:233], v[66:67], v[78:79] op_sel:[1,0,0]
	v_mov_b32_e32 v78, v245
	v_pk_fma_f32 v[72:73], v[234:235], v[82:83], v[72:73] op_sel_hi:[0,1,1]
	v_mov_b32_e32 v74, v235
	v_pk_fma_f32 v[72:73], v[74:75], v[64:65], v[72:73] op_sel_hi:[0,1,1]
	v_pk_fma_f32 v[74:75], v[76:77], v[242:243], v[120:121] op_sel_hi:[1,0,1]
	s_nop 0
	v_pk_fma_f32 v[74:75], v[242:243], v[66:67], v[74:75] op_sel:[1,0,0]
	s_nop 0
	v_pk_fma_f32 v[74:75], v[244:245], v[82:83], v[74:75] op_sel_hi:[0,1,1]
	ds_read_b128 v[186:189], v238 offset:18592
	v_pk_fma_f32 v[106:107], v[78:79], v[64:65], v[74:75] op_sel_hi:[0,1,1]
	s_waitcnt lgkmcnt(8)
; #define LAS __attribute__((address_space(3)))
; __global__ void __launch_bounds__(NTHREADS, 2) hybrid_fwd(Args a) {
;     ...
;                     for (int j = 0; j < 8; ++j) {
; #pragma unroll
;                         for (int e = 0; e < 16; ++e) { const f32x4 w = *(const LAS f32x4*)(rwT + e * 2052 + j * 256 + lane * 4);
;                             acc2[e] += y2[j][0] * (f32x2){w[0], w[0]}; acc2[e] += y2[j][1] * (f32x2){w[1], w[1]};
;                             acc2[e] += y2[j][2] * (f32x2){w[2], w[2]}; acc2[e] += y2[j][3] * (f32x2){w[3], w[3]}; }
;                         __builtin_amdgcn_sched_barrier(0);
;                     }
	v_pk_fma_f32 v[74:75], v[76:77], v[246:247], v[100:101] op_sel_hi:[1,0,1]
	s_nop 0
	v_pk_fma_f32 v[74:75], v[246:247], v[66:67], v[74:75] op_sel:[1,0,0]
	v_mov_b32_e32 v78, v249
	v_pk_fma_f32 v[74:75], v[248:249], v[82:83], v[74:75] op_sel_hi:[0,1,1]
	ds_read_b128 v[198:201], v238 offset:26800
	v_pk_fma_f32 v[74:75], v[78:79], v[64:65], v[74:75] op_sel_hi:[0,1,1]
	s_waitcnt lgkmcnt(8)
	v_pk_fma_f32 v[78:79], v[76:77], v[250:251], v[80:81] op_sel_hi:[1,0,1]
	s_nop 0
	v_pk_fma_f32 v[78:79], v[250:251], v[66:67], v[78:79] op_sel:[1,0,0]
	v_mov_b32_e32 v80, v253
	v_pk_fma_f32 v[78:79], v[252:253], v[82:83], v[78:79] op_sel_hi:[0,1,1]
	ds_read_b128 v[202:205], v238 offset:35008
	v_pk_fma_f32 v[78:79], v[80:81], v[64:65], v[78:79] op_sel_hi:[0,1,1]
	s_waitcnt lgkmcnt(8)
	v_pk_fma_f32 v[80:81], v[76:77], v[162:163], v[84:85] op_sel_hi:[1,0,1]
	s_nop 0
	v_pk_fma_f32 v[80:81], v[162:163], v[66:67], v[80:81] op_sel:[1,0,0]
	v_mov_b32_e32 v84, v165
	v_pk_fma_f32 v[80:81], v[164:165], v[82:83], v[80:81] op_sel_hi:[0,1,1]
	ds_read_b128 v[158:161], v238 offset:51424
	v_pk_fma_f32 v[80:81], v[84:85], v[64:65], v[80:81] op_sel_hi:[0,1,1]
	s_waitcnt lgkmcnt(8)
	v_pk_fma_f32 v[84:85], v[76:77], v[166:167], v[86:87] op_sel_hi:[1,0,1]
	s_nop 0
	v_pk_fma_f32 v[84:85], v[166:167], v[66:67], v[84:85] op_sel:[1,0,0]
	v_mov_b32_e32 v86, v169
	v_pk_fma_f32 v[84:85], v[168:169], v[82:83], v[84:85] op_sel_hi:[0,1,1]
	ds_read_b128 v[216:219], v238 offset:43216
	v_pk_fma_f32 v[84:85], v[86:87], v[64:65], v[84:85] op_sel_hi:[0,1,1]
	s_waitcnt lgkmcnt(8)
	v_pk_fma_f32 v[86:87], v[76:77], v[170:171], v[88:89] op_sel_hi:[1,0,1]
	s_nop 0
	v_pk_fma_f32 v[86:87], v[170:171], v[66:67], v[86:87] op_sel:[1,0,0]
	v_mov_b32_e32 v88, v173
	v_pk_fma_f32 v[86:87], v[172:173], v[82:83], v[86:87] op_sel_hi:[0,1,1]
	ds_read_b128 v[220:223], v238 offset:59632
	v_pk_fma_f32 v[86:87], v[88:89], v[64:65], v[86:87] op_sel_hi:[0,1,1]
	s_waitcnt lgkmcnt(8)
	v_pk_fma_f32 v[88:89], v[76:77], v[174:175], v[90:91] op_sel_hi:[1,0,1]
	s_nop 0
	v_pk_fma_f32 v[88:89], v[174:175], v[66:67], v[88:89] op_sel:[1,0,0]
	v_mov_b32_e32 v90, v177
	v_pk_fma_f32 v[88:89], v[176:177], v[82:83], v[88:89] op_sel_hi:[0,1,1]
	ds_read_b128 v[224:227], v25 offset:3072
	v_pk_fma_f32 v[88:89], v[90:91], v[64:65], v[88:89] op_sel_hi:[0,1,1]
	s_waitcnt lgkmcnt(8)
	v_pk_fma_f32 v[90:91], v[76:77], v[178:179], v[92:93] op_sel_hi:[1,0,1]
	s_nop 0
	v_pk_fma_f32 v[90:91], v[178:179], v[66:67], v[90:91] op_sel:[1,0,0]
	v_mov_b32_e32 v92, v181
	v_pk_fma_f32 v[90:91], v[180:181], v[82:83], v[90:91] op_sel_hi:[0,1,1]
	ds_read_b128 v[228:231], v25 offset:11280
	v_pk_fma_f32 v[90:91], v[92:93], v[64:65], v[90:91] op_sel_hi:[0,1,1]
	s_waitcnt lgkmcnt(8)
	v_pk_fma_f32 v[92:93], v[76:77], v[182:183], v[94:95] op_sel_hi:[1,0,1]
	s_nop 0
	v_pk_fma_f32 v[92:93], v[182:183], v[66:67], v[92:93] op_sel:[1,0,0]
	v_mov_b32_e32 v94, v185
	v_pk_fma_f32 v[92:93], v[184:185], v[82:83], v[92:93] op_sel_hi:[0,1,1]
	ds_read_b128 v[232:235], v25 offset:19488
	v_pk_fma_f32 v[92:93], v[94:95], v[64:65], v[92:93] op_sel_hi:[0,1,1]
	s_waitcnt lgkmcnt(8)
	v_pk_fma_f32 v[94:95], v[76:77], v[186:187], v[96:97] op_sel_hi:[1,0,1]
	s_nop 0
	v_pk_fma_f32 v[94:95], v[186:187], v[66:67], v[94:95] op_sel:[1,0,0]
	v_mov_b32_e32 v96, v189
	v_pk_fma_f32 v[94:95], v[188:189], v[82:83], v[94:95] op_sel_hi:[0,1,1]
	ds_read_b128 v[242:245], v25 offset:27696
	v_pk_fma_f32 v[94:95], v[96:97], v[64:65], v[94:95] op_sel_hi:[0,1,1]
	s_waitcnt lgkmcnt(8)
	v_pk_fma_f32 v[96:97], v[76:77], v[198:199], v[98:99] op_sel_hi:[1,0,1]
	s_nop 0
	v_pk_fma_f32 v[96:97], v[198:199], v[66:67], v[96:97] op_sel:[1,0,0]
	v_mov_b32_e32 v98, v201
	v_pk_fma_f32 v[96:97], v[200:201], v[82:83], v[96:97] op_sel_hi:[0,1,1]
	v_pk_fma_f32 v[96:97], v[98:99], v[64:65], v[96:97] op_sel_hi:[0,1,1]
	ds_read_b128 v[246:249], v25 offset:35904
	ds_read_b128 v[250:253], v25 offset:44112
	s_waitcnt lgkmcnt(8)
	v_pk_fma_f32 v[102:103], v[76:77], v[202:203], v[102:103] op_sel_hi:[1,0,1]
	s_nop 0
	v_pk_fma_f32 v[98:99], v[202:203], v[66:67], v[102:103] op_sel:[1,0,0]
	s_nop 0
	v_pk_fma_f32 v[98:99], v[204:205], v[82:83], v[98:99] op_sel_hi:[0,1,1]
	v_mov_b32_e32 v100, v205
	v_pk_fma_f32 v[98:99], v[100:101], v[64:65], v[98:99] op_sel_hi:[0,1,1]
	ds_read_b128 v[162:165], v25 offset:52320
	s_waitcnt lgkmcnt(8)
	v_pk_fma_f32 v[108:109], v[76:77], v[216:217], v[108:109] op_sel_hi:[1,0,1]
	s_nop 0
	v_pk_fma_f32 v[100:101], v[216:217], v[66:67], v[108:109] op_sel:[1,0,0]
	v_mov_b32_e32 v108, v161
	v_pk_fma_f32 v[100:101], v[218:219], v[82:83], v[100:101] op_sel_hi:[0,1,1]
	v_mov_b32_e32 v102, v219
	v_pk_fma_f32 v[100:101], v[102:103], v[64:65], v[100:101] op_sel_hi:[0,1,1]
	v_pk_fma_f32 v[102:103], v[76:77], v[158:159], v[110:111] op_sel_hi:[1,0,1]
	s_nop 0
	v_pk_fma_f32 v[102:103], v[158:159], v[66:67], v[102:103] op_sel:[1,0,0]
	s_nop 0
	v_pk_fma_f32 v[102:103], v[160:161], v[82:83], v[102:103] op_sel_hi:[0,1,1]
	v_pk_fma_f32 v[102:103], v[108:109], v[64:65], v[102:103] op_sel_hi:[0,1,1]
	ds_read_b128 v[166:169], v25 offset:60528
	s_waitcnt lgkmcnt(8)
	v_pk_fma_f32 v[76:77], v[76:77], v[220:221], v[104:105] op_sel_hi:[1,0,1]
	s_nop 0
	v_pk_fma_f32 v[66:67], v[220:221], v[66:67], v[76:77] op_sel:[1,0,0]
	v_mov_b32_e32 v76, v223
	v_pk_fma_f32 v[66:67], v[222:223], v[82:83], v[66:67] op_sel_hi:[0,1,1]
	v_pk_fma_f32 v[104:105], v[76:77], v[64:65], v[66:67] op_sel_hi:[0,1,1]
	ds_read_b128 v[170:173], v238 offset:3200
	ds_read_b128 v[174:177], v238 offset:11408
	s_waitcnt lgkmcnt(8)
; #define LAS __attribute__((address_space(3)))
; __global__ void __launch_bounds__(NTHREADS, 2) hybrid_fwd(Args a) {
;     ...
;                     for (int j = 0; j < 8; ++j) {
; #pragma unroll
;                         for (int e = 0; e < 16; ++e) { const f32x4 w = *(const LAS f32x4*)(rwT + e * 2052 + j * 256 + lane * 4);
;                             acc2[e] += y2[j][0] * (f32x2){w[0], w[0]}; acc2[e] += y2[j][1] * (f32x2){w[1], w[1]};
;                             acc2[e] += y2[j][2] * (f32x2){w[2], w[2]}; acc2[e] += y2[j][3] * (f32x2){w[3], w[3]}; }
;                         __builtin_amdgcn_sched_barrier(0);
;                     }
	v_pk_fma_f32 v[72:73], v[68:69], v[224:225], v[72:73] op_sel_hi:[1,0,1]
	s_nop 0
	v_pk_fma_f32 v[64:65], v[224:225], v[58:59], v[72:73] op_sel:[1,0,0]
	v_mov_b32_e32 v72, v231
	v_pk_fma_f32 v[64:65], v[226:227], v[70:71], v[64:65] op_sel_hi:[0,1,1]
	v_mov_b32_e32 v66, v227
	v_pk_fma_f32 v[64:65], v[66:67], v[56:57], v[64:65] op_sel_hi:[0,1,1]
	v_pk_fma_f32 v[66:67], v[68:69], v[228:229], v[106:107] op_sel_hi:[1,0,1]
	s_nop 0
	v_pk_fma_f32 v[66:67], v[228:229], v[58:59], v[66:67] op_sel:[1,0,0]
	s_nop 0
	v_pk_fma_f32 v[66:67], v[230:231], v[70:71], v[66:67] op_sel_hi:[0,1,1]
	ds_read_b128 v[178:181], v238 offset:19616
	v_pk_fma_f32 v[106:107], v[72:73], v[56:57], v[66:67] op_sel_hi:[0,1,1]
	s_waitcnt lgkmcnt(8)
	v_pk_fma_f32 v[66:67], v[68:69], v[232:233], v[74:75] op_sel_hi:[1,0,1]
	s_nop 0
	v_pk_fma_f32 v[66:67], v[232:233], v[58:59], v[66:67] op_sel:[1,0,0]
	v_mov_b32_e32 v72, v235
	v_pk_fma_f32 v[66:67], v[234:235], v[70:71], v[66:67] op_sel_hi:[0,1,1]
	v_pk_fma_f32 v[66:67], v[72:73], v[56:57], v[66:67] op_sel_hi:[0,1,1]
	ds_read_b128 v[182:185], v238 offset:27824
	s_waitcnt lgkmcnt(8)
	v_pk_fma_f32 v[76:77], v[68:69], v[242:243], v[78:79] op_sel_hi:[1,0,1]
	s_nop 0
	v_pk_fma_f32 v[72:73], v[242:243], v[58:59], v[76:77] op_sel:[1,0,0]
	s_nop 0
	v_pk_fma_f32 v[72:73], v[244:245], v[70:71], v[72:73] op_sel_hi:[0,1,1]
	v_mov_b32_e32 v74, v245
	v_pk_fma_f32 v[72:73], v[74:75], v[56:57], v[72:73] op_sel_hi:[0,1,1]
	ds_read_b128 v[186:189], v238 offset:36032
	s_waitcnt lgkmcnt(8)
	v_pk_fma_f32 v[78:79], v[68:69], v[246:247], v[80:81] op_sel_hi:[1,0,1]
	s_nop 0
	v_pk_fma_f32 v[74:75], v[246:247], v[58:59], v[78:79] op_sel:[1,0,0]
	s_nop 0
	v_pk_fma_f32 v[74:75], v[248:249], v[70:71], v[74:75] op_sel_hi:[0,1,1]
	v_mov_b32_e32 v76, v249
	v_pk_fma_f32 v[74:75], v[76:77], v[56:57], v[74:75] op_sel_hi:[0,1,1]
	ds_read_b128 v[198:201], v238 offset:44240
	s_waitcnt lgkmcnt(8)
	v_pk_fma_f32 v[80:81], v[68:69], v[250:251], v[84:85] op_sel_hi:[1,0,1]
	s_nop 0
	v_pk_fma_f32 v[76:77], v[250:251], v[58:59], v[80:81] op_sel:[1,0,0]
	s_nop 0
	v_pk_fma_f32 v[76:77], v[252:253], v[70:71], v[76:77] op_sel_hi:[0,1,1]
	v_mov_b32_e32 v78, v253
	v_pk_fma_f32 v[76:77], v[78:79], v[56:57], v[76:77] op_sel_hi:[0,1,1]
	ds_read_b128 v[202:205], v238 offset:52448
	s_waitcnt lgkmcnt(8)
	v_pk_fma_f32 v[82:83], v[68:69], v[162:163], v[86:87] op_sel_hi:[1,0,1]
	s_nop 0
	v_pk_fma_f32 v[78:79], v[162:163], v[58:59], v[82:83] op_sel:[1,0,0]
	s_nop 0
	v_pk_fma_f32 v[78:79], v[164:165], v[70:71], v[78:79] op_sel_hi:[0,1,1]
	v_mov_b32_e32 v80, v165
	v_pk_fma_f32 v[78:79], v[80:81], v[56:57], v[78:79] op_sel_hi:[0,1,1]
	ds_read_b128 v[216:219], v238 offset:60656
	s_waitcnt lgkmcnt(8)
	v_pk_fma_f32 v[84:85], v[68:69], v[166:167], v[88:89] op_sel_hi:[1,0,1]
	s_nop 0
	v_pk_fma_f32 v[80:81], v[166:167], v[58:59], v[84:85] op_sel:[1,0,0]
	s_nop 0
	v_pk_fma_f32 v[80:81], v[168:169], v[70:71], v[80:81] op_sel_hi:[0,1,1]
	v_mov_b32_e32 v82, v169
	v_pk_fma_f32 v[80:81], v[82:83], v[56:57], v[80:81] op_sel_hi:[0,1,1]
	ds_read_b128 v[158:161], v25 offset:4096
	s_waitcnt lgkmcnt(8)
	v_pk_fma_f32 v[86:87], v[68:69], v[170:171], v[90:91] op_sel_hi:[1,0,1]
	s_nop 0
	v_pk_fma_f32 v[82:83], v[170:171], v[58:59], v[86:87] op_sel:[1,0,0]
	s_nop 0
	v_pk_fma_f32 v[82:83], v[172:173], v[70:71], v[82:83] op_sel_hi:[0,1,1]
	v_mov_b32_e32 v84, v173
	v_pk_fma_f32 v[82:83], v[84:85], v[56:57], v[82:83] op_sel_hi:[0,1,1]
	ds_read_b128 v[220:223], v25 offset:12304
	s_waitcnt lgkmcnt(8)
	v_pk_fma_f32 v[88:89], v[68:69], v[174:175], v[92:93] op_sel_hi:[1,0,1]
	s_nop 0
	v_pk_fma_f32 v[84:85], v[174:175], v[58:59], v[88:89] op_sel:[1,0,0]
	s_nop 0
	v_pk_fma_f32 v[84:85], v[176:177], v[70:71], v[84:85] op_sel_hi:[0,1,1]
	v_mov_b32_e32 v86, v177
	v_pk_fma_f32 v[84:85], v[86:87], v[56:57], v[84:85] op_sel_hi:[0,1,1]
	ds_read_b128 v[224:227], v25 offset:20512
	s_waitcnt lgkmcnt(8)
	v_pk_fma_f32 v[90:91], v[68:69], v[178:179], v[94:95] op_sel_hi:[1,0,1]
	s_nop 0
	v_pk_fma_f32 v[86:87], v[178:179], v[58:59], v[90:91] op_sel:[1,0,0]
	s_nop 0
	v_pk_fma_f32 v[86:87], v[180:181], v[70:71], v[86:87] op_sel_hi:[0,1,1]
	v_mov_b32_e32 v88, v181
	v_pk_fma_f32 v[86:87], v[88:89], v[56:57], v[86:87] op_sel_hi:[0,1,1]
	ds_read_b128 v[228:231], v25 offset:28720
	s_waitcnt lgkmcnt(8)
	v_pk_fma_f32 v[92:93], v[68:69], v[182:183], v[96:97] op_sel_hi:[1,0,1]
	s_nop 0
	v_pk_fma_f32 v[88:89], v[182:183], v[58:59], v[92:93] op_sel:[1,0,0]
	s_nop 0
	v_pk_fma_f32 v[88:89], v[184:185], v[70:71], v[88:89] op_sel_hi:[0,1,1]
	v_mov_b32_e32 v90, v185
	v_pk_fma_f32 v[88:89], v[90:91], v[56:57], v[88:89] op_sel_hi:[0,1,1]
	ds_read_b128 v[232:235], v25 offset:36928
	s_waitcnt lgkmcnt(8)
	v_pk_fma_f32 v[94:95], v[68:69], v[186:187], v[98:99] op_sel_hi:[1,0,1]
	s_nop 0
	v_pk_fma_f32 v[90:91], v[186:187], v[58:59], v[94:95] op_sel:[1,0,0]
	s_nop 0
	v_pk_fma_f32 v[90:91], v[188:189], v[70:71], v[90:91] op_sel_hi:[0,1,1]
	v_mov_b32_e32 v92, v189
	v_pk_fma_f32 v[90:91], v[92:93], v[56:57], v[90:91] op_sel_hi:[0,1,1]
	ds_read_b128 v[242:245], v25 offset:45136
	s_waitcnt lgkmcnt(8)
	v_pk_fma_f32 v[96:97], v[68:69], v[198:199], v[100:101] op_sel_hi:[1,0,1]
	s_nop 0
	v_pk_fma_f32 v[92:93], v[198:199], v[58:59], v[96:97] op_sel:[1,0,0]
	s_nop 0
	v_pk_fma_f32 v[92:93], v[200:201], v[70:71], v[92:93] op_sel_hi:[0,1,1]
	v_mov_b32_e32 v94, v201
	v_pk_fma_f32 v[92:93], v[94:95], v[56:57], v[92:93] op_sel_hi:[0,1,1]
	ds_read_b128 v[246:249], v25 offset:53344
	s_waitcnt lgkmcnt(8)
; #define LAS __attribute__((address_space(3)))
; __global__ void __launch_bounds__(NTHREADS, 2) hybrid_fwd(Args a) {
;     ...
;                     for (int j = 0; j < 8; ++j) {
; #pragma unroll
;                         for (int e = 0; e < 16; ++e) { const f32x4 w = *(const LAS f32x4*)(rwT + e * 2052 + j * 256 + lane * 4);
;                             acc2[e] += y2[j][0] * (f32x2){w[0], w[0]}; acc2[e] += y2[j][1] * (f32x2){w[1], w[1]};
;                             acc2[e] += y2[j][2] * (f32x2){w[2], w[2]}; acc2[e] += y2[j][3] * (f32x2){w[3], w[3]}; }
;                         __builtin_amdgcn_sched_barrier(0);
;                     }
	v_pk_fma_f32 v[98:99], v[68:69], v[202:203], v[102:103] op_sel_hi:[1,0,1]
	s_nop 0
	v_pk_fma_f32 v[94:95], v[202:203], v[58:59], v[98:99] op_sel:[1,0,0]
	s_nop 0
	v_pk_fma_f32 v[94:95], v[204:205], v[70:71], v[94:95] op_sel_hi:[0,1,1]
	v_mov_b32_e32 v96, v205
	v_pk_fma_f32 v[94:95], v[96:97], v[56:57], v[94:95] op_sel_hi:[0,1,1]
	ds_read_b128 v[250:253], v25 offset:61552
	s_waitcnt lgkmcnt(8)
	v_pk_fma_f32 v[68:69], v[68:69], v[216:217], v[104:105] op_sel_hi:[1,0,1]
	s_nop 0
	v_pk_fma_f32 v[58:59], v[216:217], v[58:59], v[68:69] op_sel:[1,0,0]
	v_mov_b32_e32 v68, v219
	v_pk_fma_f32 v[58:59], v[218:219], v[70:71], v[58:59] op_sel_hi:[0,1,1]
	v_pk_fma_f32 v[96:97], v[68:69], v[56:57], v[58:59] op_sel_hi:[0,1,1]
	ds_read_b128 v[162:165], v238 offset:4224
	ds_read_b128 v[166:169], v238 offset:12432
	s_waitcnt lgkmcnt(8)
	v_pk_fma_f32 v[64:65], v[60:61], v[158:159], v[64:65] op_sel_hi:[1,0,1]
	s_nop 0
	v_pk_fma_f32 v[56:57], v[158:159], v[54:55], v[64:65] op_sel:[1,0,0]
	v_mov_b32_e32 v64, v223
	v_pk_fma_f32 v[56:57], v[160:161], v[62:63], v[56:57] op_sel_hi:[0,1,1]
	v_mov_b32_e32 v58, v161
	v_pk_fma_f32 v[56:57], v[58:59], v[52:53], v[56:57] op_sel_hi:[0,1,1]
	v_pk_fma_f32 v[58:59], v[60:61], v[220:221], v[106:107] op_sel_hi:[1,0,1]
	s_nop 0
	v_pk_fma_f32 v[58:59], v[220:221], v[54:55], v[58:59] op_sel:[1,0,0]
	s_nop 0
	v_pk_fma_f32 v[58:59], v[222:223], v[62:63], v[58:59] op_sel_hi:[0,1,1]
	ds_read_b128 v[170:173], v238 offset:20640
	v_pk_fma_f32 v[98:99], v[64:65], v[52:53], v[58:59] op_sel_hi:[0,1,1]
	s_waitcnt lgkmcnt(8)
	v_pk_fma_f32 v[58:59], v[60:61], v[224:225], v[66:67] op_sel_hi:[1,0,1]
	s_nop 0
	v_pk_fma_f32 v[58:59], v[224:225], v[54:55], v[58:59] op_sel:[1,0,0]
	v_mov_b32_e32 v64, v227
	v_pk_fma_f32 v[58:59], v[226:227], v[62:63], v[58:59] op_sel_hi:[0,1,1]
	v_pk_fma_f32 v[58:59], v[64:65], v[52:53], v[58:59] op_sel_hi:[0,1,1]
	ds_read_b128 v[174:177], v238 offset:28848
	s_waitcnt lgkmcnt(8)
	v_pk_fma_f32 v[68:69], v[60:61], v[228:229], v[72:73] op_sel_hi:[1,0,1]
	s_nop 0
	v_pk_fma_f32 v[64:65], v[228:229], v[54:55], v[68:69] op_sel:[1,0,0]
	s_nop 0
	v_pk_fma_f32 v[64:65], v[230:231], v[62:63], v[64:65] op_sel_hi:[0,1,1]
	v_mov_b32_e32 v66, v231
	v_pk_fma_f32 v[64:65], v[66:67], v[52:53], v[64:65] op_sel_hi:[0,1,1]
	ds_read_b128 v[178:181], v238 offset:37056
	s_waitcnt lgkmcnt(8)
	v_pk_fma_f32 v[70:71], v[60:61], v[232:233], v[74:75] op_sel_hi:[1,0,1]
	s_nop 0
	v_pk_fma_f32 v[66:67], v[232:233], v[54:55], v[70:71] op_sel:[1,0,0]
	s_nop 0
	v_pk_fma_f32 v[66:67], v[234:235], v[62:63], v[66:67] op_sel_hi:[0,1,1]
	v_mov_b32_e32 v68, v235
	v_pk_fma_f32 v[66:67], v[68:69], v[52:53], v[66:67] op_sel_hi:[0,1,1]
	ds_read_b128 v[182:185], v238 offset:45264
	s_waitcnt lgkmcnt(8)
	v_pk_fma_f32 v[72:73], v[60:61], v[242:243], v[76:77] op_sel_hi:[1,0,1]
	s_nop 0
	v_pk_fma_f32 v[68:69], v[242:243], v[54:55], v[72:73] op_sel:[1,0,0]
	s_nop 0
	v_pk_fma_f32 v[68:69], v[244:245], v[62:63], v[68:69] op_sel_hi:[0,1,1]
	v_mov_b32_e32 v70, v245
	v_pk_fma_f32 v[68:69], v[70:71], v[52:53], v[68:69] op_sel_hi:[0,1,1]
	ds_read_b128 v[186:189], v238 offset:53472
	s_waitcnt lgkmcnt(8)
	v_pk_fma_f32 v[74:75], v[60:61], v[246:247], v[78:79] op_sel_hi:[1,0,1]
	s_nop 0
	v_pk_fma_f32 v[70:71], v[246:247], v[54:55], v[74:75] op_sel:[1,0,0]
	s_nop 0
	v_pk_fma_f32 v[70:71], v[248:249], v[62:63], v[70:71] op_sel_hi:[0,1,1]
	v_mov_b32_e32 v72, v249
	v_pk_fma_f32 v[70:71], v[72:73], v[52:53], v[70:71] op_sel_hi:[0,1,1]
	ds_read_b128 v[198:201], v238 offset:61680
	s_waitcnt lgkmcnt(8)
	v_pk_fma_f32 v[76:77], v[60:61], v[250:251], v[80:81] op_sel_hi:[1,0,1]
	s_nop 0
	v_pk_fma_f32 v[72:73], v[250:251], v[54:55], v[76:77] op_sel:[1,0,0]
	s_nop 0
	v_pk_fma_f32 v[72:73], v[252:253], v[62:63], v[72:73] op_sel_hi:[0,1,1]
	v_mov_b32_e32 v74, v253
	v_pk_fma_f32 v[72:73], v[74:75], v[52:53], v[72:73] op_sel_hi:[0,1,1]
	ds_read_b128 v[202:205], v25 offset:5120
	s_waitcnt lgkmcnt(8)
	v_pk_fma_f32 v[78:79], v[60:61], v[162:163], v[82:83] op_sel_hi:[1,0,1]
	s_nop 0
	v_pk_fma_f32 v[74:75], v[162:163], v[54:55], v[78:79] op_sel:[1,0,0]
	s_nop 0
	v_pk_fma_f32 v[74:75], v[164:165], v[62:63], v[74:75] op_sel_hi:[0,1,1]
	v_mov_b32_e32 v76, v165
	v_pk_fma_f32 v[74:75], v[76:77], v[52:53], v[74:75] op_sel_hi:[0,1,1]
	ds_read_b128 v[216:219], v25 offset:13328
	s_waitcnt lgkmcnt(8)
	v_pk_fma_f32 v[80:81], v[60:61], v[166:167], v[84:85] op_sel_hi:[1,0,1]
	s_nop 0
	v_pk_fma_f32 v[76:77], v[166:167], v[54:55], v[80:81] op_sel:[1,0,0]
	s_nop 0
	v_pk_fma_f32 v[76:77], v[168:169], v[62:63], v[76:77] op_sel_hi:[0,1,1]
	v_mov_b32_e32 v78, v169
	v_pk_fma_f32 v[76:77], v[78:79], v[52:53], v[76:77] op_sel_hi:[0,1,1]
	ds_read_b128 v[158:161], v25 offset:21536
	s_waitcnt lgkmcnt(8)
	v_pk_fma_f32 v[82:83], v[60:61], v[170:171], v[86:87] op_sel_hi:[1,0,1]
	s_nop 0
	v_pk_fma_f32 v[78:79], v[170:171], v[54:55], v[82:83] op_sel:[1,0,0]
	s_nop 0
	v_pk_fma_f32 v[78:79], v[172:173], v[62:63], v[78:79] op_sel_hi:[0,1,1]
	v_mov_b32_e32 v80, v173
	v_pk_fma_f32 v[78:79], v[80:81], v[52:53], v[78:79] op_sel_hi:[0,1,1]
	ds_read_b128 v[220:223], v25 offset:29744
	s_waitcnt lgkmcnt(8)
	v_pk_fma_f32 v[84:85], v[60:61], v[174:175], v[88:89] op_sel_hi:[1,0,1]
	s_nop 0
	v_pk_fma_f32 v[80:81], v[174:175], v[54:55], v[84:85] op_sel:[1,0,0]
	s_nop 0
	v_pk_fma_f32 v[80:81], v[176:177], v[62:63], v[80:81] op_sel_hi:[0,1,1]
	v_mov_b32_e32 v82, v177
	v_pk_fma_f32 v[80:81], v[82:83], v[52:53], v[80:81] op_sel_hi:[0,1,1]
	ds_read_b128 v[224:227], v25 offset:37952
	s_waitcnt lgkmcnt(8)
; #define LAS __attribute__((address_space(3)))
; __global__ void __launch_bounds__(NTHREADS, 2) hybrid_fwd(Args a) {
;     ...
;                     for (int j = 0; j < 8; ++j) {
; #pragma unroll
;                         for (int e = 0; e < 16; ++e) { const f32x4 w = *(const LAS f32x4*)(rwT + e * 2052 + j * 256 + lane * 4);
;                             acc2[e] += y2[j][0] * (f32x2){w[0], w[0]}; acc2[e] += y2[j][1] * (f32x2){w[1], w[1]};
;                             acc2[e] += y2[j][2] * (f32x2){w[2], w[2]}; acc2[e] += y2[j][3] * (f32x2){w[3], w[3]}; }
;                         __builtin_amdgcn_sched_barrier(0);
;                     }
	v_pk_fma_f32 v[86:87], v[60:61], v[178:179], v[90:91] op_sel_hi:[1,0,1]
	s_nop 0
	v_pk_fma_f32 v[82:83], v[178:179], v[54:55], v[86:87] op_sel:[1,0,0]
	s_nop 0
	v_pk_fma_f32 v[82:83], v[180:181], v[62:63], v[82:83] op_sel_hi:[0,1,1]
	v_mov_b32_e32 v84, v181
	v_pk_fma_f32 v[82:83], v[84:85], v[52:53], v[82:83] op_sel_hi:[0,1,1]
	ds_read_b128 v[228:231], v25 offset:46160
	s_waitcnt lgkmcnt(8)
	v_pk_fma_f32 v[88:89], v[60:61], v[182:183], v[92:93] op_sel_hi:[1,0,1]
	s_nop 0
	v_pk_fma_f32 v[84:85], v[182:183], v[54:55], v[88:89] op_sel:[1,0,0]
	s_nop 0
	v_pk_fma_f32 v[84:85], v[184:185], v[62:63], v[84:85] op_sel_hi:[0,1,1]
	v_mov_b32_e32 v86, v185
	v_pk_fma_f32 v[84:85], v[86:87], v[52:53], v[84:85] op_sel_hi:[0,1,1]
	ds_read_b128 v[232:235], v25 offset:54368
	s_waitcnt lgkmcnt(8)
	v_pk_fma_f32 v[90:91], v[60:61], v[186:187], v[94:95] op_sel_hi:[1,0,1]
	s_nop 0
	v_pk_fma_f32 v[86:87], v[186:187], v[54:55], v[90:91] op_sel:[1,0,0]
	s_nop 0
	v_pk_fma_f32 v[86:87], v[188:189], v[62:63], v[86:87] op_sel_hi:[0,1,1]
	v_mov_b32_e32 v88, v189
	v_pk_fma_f32 v[86:87], v[88:89], v[52:53], v[86:87] op_sel_hi:[0,1,1]
	ds_read_b128 v[242:245], v25 offset:62576
	s_waitcnt lgkmcnt(8)
	v_pk_fma_f32 v[60:61], v[60:61], v[198:199], v[96:97] op_sel_hi:[1,0,1]
	s_nop 0
	v_pk_fma_f32 v[54:55], v[198:199], v[54:55], v[60:61] op_sel:[1,0,0]
	v_mov_b32_e32 v60, v201
	v_pk_fma_f32 v[54:55], v[200:201], v[62:63], v[54:55] op_sel_hi:[0,1,1]
	v_pk_fma_f32 v[88:89], v[60:61], v[52:53], v[54:55] op_sel_hi:[0,1,1]
	ds_read_b128 v[246:249], v238 offset:5248
	s_waitcnt lgkmcnt(8)
	v_pk_fma_f32 v[56:57], v[48:49], v[202:203], v[56:57] op_sel_hi:[1,0,1]
	s_nop 0
	v_pk_fma_f32 v[52:53], v[202:203], v[46:47], v[56:57] op_sel:[1,0,0]
	s_nop 0
	v_pk_fma_f32 v[52:53], v[204:205], v[50:51], v[52:53] op_sel_hi:[0,1,1]
	v_mov_b32_e32 v54, v205
	v_pk_fma_f32 v[52:53], v[54:55], v[44:45], v[52:53] op_sel_hi:[0,1,1]
	ds_read_b128 v[250:253], v238 offset:13456
	s_waitcnt lgkmcnt(8)
	v_pk_fma_f32 v[60:61], v[48:49], v[216:217], v[98:99] op_sel_hi:[1,0,1]
	s_nop 0
	v_pk_fma_f32 v[54:55], v[216:217], v[46:47], v[60:61] op_sel:[1,0,0]
	s_nop 0
	v_pk_fma_f32 v[54:55], v[218:219], v[50:51], v[54:55] op_sel_hi:[0,1,1]
	v_mov_b32_e32 v56, v219
	v_pk_fma_f32 v[90:91], v[56:57], v[44:45], v[54:55] op_sel_hi:[0,1,1]
	ds_read_b128 v[162:165], v238 offset:21664
	s_waitcnt lgkmcnt(8)
	v_pk_fma_f32 v[58:59], v[48:49], v[158:159], v[58:59] op_sel_hi:[1,0,1]
	s_nop 0
	v_pk_fma_f32 v[54:55], v[158:159], v[46:47], v[58:59] op_sel:[1,0,0]
	s_nop 0
	v_pk_fma_f32 v[54:55], v[160:161], v[50:51], v[54:55] op_sel_hi:[0,1,1]
	v_mov_b32_e32 v56, v161
	v_pk_fma_f32 v[54:55], v[56:57], v[44:45], v[54:55] op_sel_hi:[0,1,1]
	ds_read_b128 v[166:169], v238 offset:29872
	s_waitcnt lgkmcnt(8)
	v_pk_fma_f32 v[60:61], v[48:49], v[220:221], v[64:65] op_sel_hi:[1,0,1]
	s_nop 0
	v_pk_fma_f32 v[56:57], v[220:221], v[46:47], v[60:61] op_sel:[1,0,0]
	s_nop 0
	v_pk_fma_f32 v[56:57], v[222:223], v[50:51], v[56:57] op_sel_hi:[0,1,1]
	v_mov_b32_e32 v58, v223
	v_pk_fma_f32 v[56:57], v[58:59], v[44:45], v[56:57] op_sel_hi:[0,1,1]
	ds_read_b128 v[170:173], v238 offset:38080
	s_waitcnt lgkmcnt(8)
	v_pk_fma_f32 v[62:63], v[48:49], v[224:225], v[66:67] op_sel_hi:[1,0,1]
	s_nop 0
	v_pk_fma_f32 v[58:59], v[224:225], v[46:47], v[62:63] op_sel:[1,0,0]
	s_nop 0
	v_pk_fma_f32 v[58:59], v[226:227], v[50:51], v[58:59] op_sel_hi:[0,1,1]
	v_mov_b32_e32 v60, v227
	v_pk_fma_f32 v[58:59], v[60:61], v[44:45], v[58:59] op_sel_hi:[0,1,1]
	ds_read_b128 v[174:177], v238 offset:46288
	s_waitcnt lgkmcnt(8)
	v_pk_fma_f32 v[64:65], v[48:49], v[228:229], v[68:69] op_sel_hi:[1,0,1]
	s_nop 0
	v_pk_fma_f32 v[60:61], v[228:229], v[46:47], v[64:65] op_sel:[1,0,0]
	s_nop 0
	v_pk_fma_f32 v[60:61], v[230:231], v[50:51], v[60:61] op_sel_hi:[0,1,1]
	v_mov_b32_e32 v62, v231
	v_pk_fma_f32 v[60:61], v[62:63], v[44:45], v[60:61] op_sel_hi:[0,1,1]
	ds_read_b128 v[178:181], v238 offset:54496
	s_waitcnt lgkmcnt(8)
	v_pk_fma_f32 v[66:67], v[48:49], v[232:233], v[70:71] op_sel_hi:[1,0,1]
	s_nop 0
	v_pk_fma_f32 v[62:63], v[232:233], v[46:47], v[66:67] op_sel:[1,0,0]
	s_nop 0
	v_pk_fma_f32 v[62:63], v[234:235], v[50:51], v[62:63] op_sel_hi:[0,1,1]
	v_mov_b32_e32 v64, v235
	v_pk_fma_f32 v[62:63], v[64:65], v[44:45], v[62:63] op_sel_hi:[0,1,1]
	ds_read_b128 v[182:185], v238 offset:62704
	s_waitcnt lgkmcnt(8)
	v_pk_fma_f32 v[68:69], v[48:49], v[242:243], v[72:73] op_sel_hi:[1,0,1]
	s_nop 0
	v_pk_fma_f32 v[64:65], v[242:243], v[46:47], v[68:69] op_sel:[1,0,0]
	s_nop 0
	v_pk_fma_f32 v[64:65], v[244:245], v[50:51], v[64:65] op_sel_hi:[0,1,1]
	v_mov_b32_e32 v66, v245
	v_pk_fma_f32 v[64:65], v[66:67], v[44:45], v[64:65] op_sel_hi:[0,1,1]
	ds_read_b128 v[186:189], v25 offset:6144
	s_waitcnt lgkmcnt(8)
	v_pk_fma_f32 v[70:71], v[48:49], v[246:247], v[74:75] op_sel_hi:[1,0,1]
	s_nop 0
	v_pk_fma_f32 v[66:67], v[246:247], v[46:47], v[70:71] op_sel:[1,0,0]
	s_nop 0
	v_pk_fma_f32 v[66:67], v[248:249], v[50:51], v[66:67] op_sel_hi:[0,1,1]
	v_mov_b32_e32 v68, v249
	v_pk_fma_f32 v[66:67], v[68:69], v[44:45], v[66:67] op_sel_hi:[0,1,1]
	ds_read_b128 v[198:201], v25 offset:14352
	s_waitcnt lgkmcnt(8)
	v_pk_fma_f32 v[72:73], v[48:49], v[250:251], v[76:77] op_sel_hi:[1,0,1]
	s_nop 0
	v_pk_fma_f32 v[68:69], v[250:251], v[46:47], v[72:73] op_sel:[1,0,0]
	s_nop 0
	v_pk_fma_f32 v[68:69], v[252:253], v[50:51], v[68:69] op_sel_hi:[0,1,1]
	v_mov_b32_e32 v70, v253
	v_pk_fma_f32 v[68:69], v[70:71], v[44:45], v[68:69] op_sel_hi:[0,1,1]
	ds_read_b128 v[202:205], v25 offset:22560
	s_waitcnt lgkmcnt(8)
; #define LAS __attribute__((address_space(3)))
; __global__ void __launch_bounds__(NTHREADS, 2) hybrid_fwd(Args a) {
;     ...
;                     for (int j = 0; j < 8; ++j) {
; #pragma unroll
;                         for (int e = 0; e < 16; ++e) { const f32x4 w = *(const LAS f32x4*)(rwT + e * 2052 + j * 256 + lane * 4);
;                             acc2[e] += y2[j][0] * (f32x2){w[0], w[0]}; acc2[e] += y2[j][1] * (f32x2){w[1], w[1]};
;                             acc2[e] += y2[j][2] * (f32x2){w[2], w[2]}; acc2[e] += y2[j][3] * (f32x2){w[3], w[3]}; }
;                         __builtin_amdgcn_sched_barrier(0);
;                     }
	v_pk_fma_f32 v[74:75], v[48:49], v[162:163], v[78:79] op_sel_hi:[1,0,1]
	s_nop 0
	v_pk_fma_f32 v[70:71], v[162:163], v[46:47], v[74:75] op_sel:[1,0,0]
	s_nop 0
	v_pk_fma_f32 v[70:71], v[164:165], v[50:51], v[70:71] op_sel_hi:[0,1,1]
	v_mov_b32_e32 v72, v165
	v_pk_fma_f32 v[70:71], v[72:73], v[44:45], v[70:71] op_sel_hi:[0,1,1]
	ds_read_b128 v[216:219], v25 offset:30768
	s_waitcnt lgkmcnt(8)
	v_pk_fma_f32 v[76:77], v[48:49], v[166:167], v[80:81] op_sel_hi:[1,0,1]
	s_nop 0
	v_pk_fma_f32 v[72:73], v[166:167], v[46:47], v[76:77] op_sel:[1,0,0]
	s_nop 0
	v_pk_fma_f32 v[72:73], v[168:169], v[50:51], v[72:73] op_sel_hi:[0,1,1]
	v_mov_b32_e32 v74, v169
	v_pk_fma_f32 v[72:73], v[74:75], v[44:45], v[72:73] op_sel_hi:[0,1,1]
	ds_read_b128 v[158:161], v25 offset:38976
	s_waitcnt lgkmcnt(8)
	v_pk_fma_f32 v[78:79], v[48:49], v[170:171], v[82:83] op_sel_hi:[1,0,1]
	s_nop 0
	v_pk_fma_f32 v[74:75], v[170:171], v[46:47], v[78:79] op_sel:[1,0,0]
	s_nop 0
	v_pk_fma_f32 v[74:75], v[172:173], v[50:51], v[74:75] op_sel_hi:[0,1,1]
	v_mov_b32_e32 v76, v173
	v_pk_fma_f32 v[74:75], v[76:77], v[44:45], v[74:75] op_sel_hi:[0,1,1]
	ds_read_b128 v[220:223], v25 offset:47184
	s_waitcnt lgkmcnt(8)
	v_pk_fma_f32 v[80:81], v[48:49], v[174:175], v[84:85] op_sel_hi:[1,0,1]
	s_nop 0
	v_pk_fma_f32 v[76:77], v[174:175], v[46:47], v[80:81] op_sel:[1,0,0]
	s_nop 0
	v_pk_fma_f32 v[76:77], v[176:177], v[50:51], v[76:77] op_sel_hi:[0,1,1]
	v_mov_b32_e32 v78, v177
	v_pk_fma_f32 v[76:77], v[78:79], v[44:45], v[76:77] op_sel_hi:[0,1,1]
	ds_read_b128 v[224:227], v25 offset:55392
	s_waitcnt lgkmcnt(8)
	v_pk_fma_f32 v[82:83], v[48:49], v[178:179], v[86:87] op_sel_hi:[1,0,1]
	s_nop 0
	v_pk_fma_f32 v[78:79], v[178:179], v[46:47], v[82:83] op_sel:[1,0,0]
	s_nop 0
	v_pk_fma_f32 v[78:79], v[180:181], v[50:51], v[78:79] op_sel_hi:[0,1,1]
	v_mov_b32_e32 v80, v181
	v_pk_fma_f32 v[78:79], v[80:81], v[44:45], v[78:79] op_sel_hi:[0,1,1]
	ds_read_b128 v[228:231], v25 offset:63600
	s_waitcnt lgkmcnt(8)
	v_pk_fma_f32 v[48:49], v[48:49], v[182:183], v[88:89] op_sel_hi:[1,0,1]
	s_nop 0
	v_pk_fma_f32 v[46:47], v[182:183], v[46:47], v[48:49] op_sel:[1,0,0]
	v_mov_b32_e32 v48, v185
	v_pk_fma_f32 v[46:47], v[184:185], v[50:51], v[46:47] op_sel_hi:[0,1,1]
	v_pk_fma_f32 v[80:81], v[48:49], v[44:45], v[46:47] op_sel_hi:[0,1,1]
	ds_read_b128 v[232:235], v238 offset:6272
	s_waitcnt lgkmcnt(8)
	v_pk_fma_f32 v[48:49], v[40:41], v[186:187], v[52:53] op_sel_hi:[1,0,1]
	s_nop 0
	v_pk_fma_f32 v[44:45], v[186:187], v[38:39], v[48:49] op_sel:[1,0,0]
	s_nop 0
	v_pk_fma_f32 v[44:45], v[188:189], v[42:43], v[44:45] op_sel_hi:[0,1,1]
	v_mov_b32_e32 v46, v189
	v_pk_fma_f32 v[44:45], v[46:47], v[36:37], v[44:45] op_sel_hi:[0,1,1]
	ds_read_b128 v[242:245], v238 offset:14480
	s_waitcnt lgkmcnt(8)
	v_pk_fma_f32 v[50:51], v[40:41], v[198:199], v[90:91] op_sel_hi:[1,0,1]
	s_nop 0
	v_pk_fma_f32 v[46:47], v[198:199], v[38:39], v[50:51] op_sel:[1,0,0]
	s_nop 0
	v_pk_fma_f32 v[46:47], v[200:201], v[42:43], v[46:47] op_sel_hi:[0,1,1]
	v_mov_b32_e32 v48, v201
	v_pk_fma_f32 v[82:83], v[48:49], v[36:37], v[46:47] op_sel_hi:[0,1,1]
	ds_read_b128 v[246:249], v238 offset:22688
	s_waitcnt lgkmcnt(8)
	v_pk_fma_f32 v[50:51], v[40:41], v[202:203], v[54:55] op_sel_hi:[1,0,1]
	s_nop 0
	v_pk_fma_f32 v[46:47], v[202:203], v[38:39], v[50:51] op_sel:[1,0,0]
	s_nop 0
	v_pk_fma_f32 v[46:47], v[204:205], v[42:43], v[46:47] op_sel_hi:[0,1,1]
	v_mov_b32_e32 v48, v205
	v_pk_fma_f32 v[46:47], v[48:49], v[36:37], v[46:47] op_sel_hi:[0,1,1]
	ds_read_b128 v[250:253], v238 offset:30896
	s_waitcnt lgkmcnt(8)
	v_pk_fma_f32 v[52:53], v[40:41], v[216:217], v[56:57] op_sel_hi:[1,0,1]
	s_nop 0
	v_pk_fma_f32 v[48:49], v[216:217], v[38:39], v[52:53] op_sel:[1,0,0]
	s_nop 0
	v_pk_fma_f32 v[48:49], v[218:219], v[42:43], v[48:49] op_sel_hi:[0,1,1]
	v_mov_b32_e32 v50, v219
	v_pk_fma_f32 v[48:49], v[50:51], v[36:37], v[48:49] op_sel_hi:[0,1,1]
	ds_read_b128 v[162:165], v238 offset:39104
	s_waitcnt lgkmcnt(8)
	v_pk_fma_f32 v[54:55], v[40:41], v[158:159], v[58:59] op_sel_hi:[1,0,1]
	s_nop 0
	v_pk_fma_f32 v[50:51], v[158:159], v[38:39], v[54:55] op_sel:[1,0,0]
	s_nop 0
	v_pk_fma_f32 v[50:51], v[160:161], v[42:43], v[50:51] op_sel_hi:[0,1,1]
	v_mov_b32_e32 v52, v161
	v_pk_fma_f32 v[50:51], v[52:53], v[36:37], v[50:51] op_sel_hi:[0,1,1]
	ds_read_b128 v[166:169], v238 offset:47312
	s_waitcnt lgkmcnt(8)
	v_pk_fma_f32 v[56:57], v[40:41], v[220:221], v[60:61] op_sel_hi:[1,0,1]
	s_nop 0
	v_pk_fma_f32 v[52:53], v[220:221], v[38:39], v[56:57] op_sel:[1,0,0]
	s_nop 0
	v_pk_fma_f32 v[52:53], v[222:223], v[42:43], v[52:53] op_sel_hi:[0,1,1]
	v_mov_b32_e32 v54, v223
	v_pk_fma_f32 v[52:53], v[54:55], v[36:37], v[52:53] op_sel_hi:[0,1,1]
	ds_read_b128 v[170:173], v238 offset:55520
	s_waitcnt lgkmcnt(8)
	v_pk_fma_f32 v[58:59], v[40:41], v[224:225], v[62:63] op_sel_hi:[1,0,1]
	s_nop 0
	v_pk_fma_f32 v[54:55], v[224:225], v[38:39], v[58:59] op_sel:[1,0,0]
	s_nop 0
	v_pk_fma_f32 v[54:55], v[226:227], v[42:43], v[54:55] op_sel_hi:[0,1,1]
	v_mov_b32_e32 v56, v227
	v_pk_fma_f32 v[54:55], v[56:57], v[36:37], v[54:55] op_sel_hi:[0,1,1]
	ds_read_b128 v[174:177], v238 offset:63728
	s_waitcnt lgkmcnt(8)
	v_pk_fma_f32 v[60:61], v[40:41], v[228:229], v[64:65] op_sel_hi:[1,0,1]
	s_nop 0
	v_pk_fma_f32 v[56:57], v[228:229], v[38:39], v[60:61] op_sel:[1,0,0]
	s_nop 0
	v_pk_fma_f32 v[56:57], v[230:231], v[42:43], v[56:57] op_sel_hi:[0,1,1]
	v_mov_b32_e32 v58, v231
	v_pk_fma_f32 v[56:57], v[58:59], v[36:37], v[56:57] op_sel_hi:[0,1,1]
	ds_read_b128 v[178:181], v25 offset:7168
	s_waitcnt lgkmcnt(8)
; #define LAS __attribute__((address_space(3)))
; __global__ void __launch_bounds__(NTHREADS, 2) hybrid_fwd(Args a) {
;     ...
;                     for (int j = 0; j < 8; ++j) {
; #pragma unroll
;                         for (int e = 0; e < 16; ++e) { const f32x4 w = *(const LAS f32x4*)(rwT + e * 2052 + j * 256 + lane * 4);
;                             acc2[e] += y2[j][0] * (f32x2){w[0], w[0]}; acc2[e] += y2[j][1] * (f32x2){w[1], w[1]};
;                             acc2[e] += y2[j][2] * (f32x2){w[2], w[2]}; acc2[e] += y2[j][3] * (f32x2){w[3], w[3]}; }
;                         __builtin_amdgcn_sched_barrier(0);
;                     }
	v_pk_fma_f32 v[62:63], v[40:41], v[232:233], v[66:67] op_sel_hi:[1,0,1]
	s_nop 0
	v_pk_fma_f32 v[58:59], v[232:233], v[38:39], v[62:63] op_sel:[1,0,0]
	s_nop 0
	v_pk_fma_f32 v[58:59], v[234:235], v[42:43], v[58:59] op_sel_hi:[0,1,1]
	v_mov_b32_e32 v60, v235
	v_pk_fma_f32 v[58:59], v[60:61], v[36:37], v[58:59] op_sel_hi:[0,1,1]
	ds_read_b128 v[182:185], v25 offset:15376
	s_waitcnt lgkmcnt(8)
	v_pk_fma_f32 v[64:65], v[40:41], v[242:243], v[68:69] op_sel_hi:[1,0,1]
	s_nop 0
	v_pk_fma_f32 v[60:61], v[242:243], v[38:39], v[64:65] op_sel:[1,0,0]
	s_nop 0
	v_pk_fma_f32 v[60:61], v[244:245], v[42:43], v[60:61] op_sel_hi:[0,1,1]
	v_mov_b32_e32 v62, v245
	v_pk_fma_f32 v[60:61], v[62:63], v[36:37], v[60:61] op_sel_hi:[0,1,1]
	ds_read_b128 v[186:189], v25 offset:23584
	s_waitcnt lgkmcnt(8)
	v_pk_fma_f32 v[66:67], v[40:41], v[246:247], v[70:71] op_sel_hi:[1,0,1]
	s_nop 0
	v_pk_fma_f32 v[62:63], v[246:247], v[38:39], v[66:67] op_sel:[1,0,0]
	s_nop 0
	v_pk_fma_f32 v[62:63], v[248:249], v[42:43], v[62:63] op_sel_hi:[0,1,1]
	v_mov_b32_e32 v64, v249
	v_pk_fma_f32 v[62:63], v[64:65], v[36:37], v[62:63] op_sel_hi:[0,1,1]
	ds_read_b128 v[198:201], v25 offset:31792
	s_waitcnt lgkmcnt(8)
	v_pk_fma_f32 v[68:69], v[40:41], v[250:251], v[72:73] op_sel_hi:[1,0,1]
	s_nop 0
	v_pk_fma_f32 v[64:65], v[250:251], v[38:39], v[68:69] op_sel:[1,0,0]
	s_nop 0
	v_pk_fma_f32 v[64:65], v[252:253], v[42:43], v[64:65] op_sel_hi:[0,1,1]
	v_mov_b32_e32 v66, v253
	v_pk_fma_f32 v[64:65], v[66:67], v[36:37], v[64:65] op_sel_hi:[0,1,1]
	ds_read_b128 v[202:205], v25 offset:40000
	s_waitcnt lgkmcnt(8)
	v_pk_fma_f32 v[70:71], v[40:41], v[162:163], v[74:75] op_sel_hi:[1,0,1]
	s_nop 0
	v_pk_fma_f32 v[66:67], v[162:163], v[38:39], v[70:71] op_sel:[1,0,0]
	s_nop 0
	v_pk_fma_f32 v[66:67], v[164:165], v[42:43], v[66:67] op_sel_hi:[0,1,1]
	v_mov_b32_e32 v68, v165
	v_pk_fma_f32 v[66:67], v[68:69], v[36:37], v[66:67] op_sel_hi:[0,1,1]
	ds_read_b128 v[216:219], v25 offset:48208
	s_waitcnt lgkmcnt(8)
	v_pk_fma_f32 v[72:73], v[40:41], v[166:167], v[76:77] op_sel_hi:[1,0,1]
	s_nop 0
	v_pk_fma_f32 v[68:69], v[166:167], v[38:39], v[72:73] op_sel:[1,0,0]
	s_nop 0
	v_pk_fma_f32 v[68:69], v[168:169], v[42:43], v[68:69] op_sel_hi:[0,1,1]
	v_mov_b32_e32 v70, v169
	v_pk_fma_f32 v[68:69], v[70:71], v[36:37], v[68:69] op_sel_hi:[0,1,1]
	ds_read_b128 v[158:161], v25 offset:56416
	s_waitcnt lgkmcnt(8)
	v_pk_fma_f32 v[74:75], v[40:41], v[170:171], v[78:79] op_sel_hi:[1,0,1]
	s_nop 0
	v_pk_fma_f32 v[70:71], v[170:171], v[38:39], v[74:75] op_sel:[1,0,0]
	s_nop 0
	v_pk_fma_f32 v[70:71], v[172:173], v[42:43], v[70:71] op_sel_hi:[0,1,1]
	v_mov_b32_e32 v72, v173
	v_pk_fma_f32 v[70:71], v[72:73], v[36:37], v[70:71] op_sel_hi:[0,1,1]
	ds_read_b128 v[220:223], v25 offset:64624
	s_waitcnt lgkmcnt(8)
	v_pk_fma_f32 v[40:41], v[40:41], v[174:175], v[80:81] op_sel_hi:[1,0,1]
	s_nop 0
	v_pk_fma_f32 v[38:39], v[174:175], v[38:39], v[40:41] op_sel:[1,0,0]
	v_mov_b32_e32 v40, v177
	v_pk_fma_f32 v[38:39], v[176:177], v[42:43], v[38:39] op_sel_hi:[0,1,1]
	v_pk_fma_f32 v[72:73], v[40:41], v[36:37], v[38:39] op_sel_hi:[0,1,1]
	ds_read_b128 v[224:227], v238 offset:7296
	s_waitcnt lgkmcnt(8)
	v_pk_fma_f32 v[40:41], v[22:23], v[178:179], v[44:45] op_sel_hi:[1,0,1]
	s_nop 0
	v_pk_fma_f32 v[36:37], v[178:179], v[18:19], v[40:41] op_sel:[1,0,0]
	s_nop 0
	v_pk_fma_f32 v[36:37], v[180:181], v[20:21], v[36:37] op_sel_hi:[0,1,1]
	v_mov_b32_e32 v38, v181
	v_pk_fma_f32 v[36:37], v[38:39], v[16:17], v[36:37] op_sel_hi:[0,1,1]
	ds_read_b128 v[228:231], v238 offset:15504
	s_waitcnt lgkmcnt(8)
	v_pk_fma_f32 v[42:43], v[22:23], v[182:183], v[82:83] op_sel_hi:[1,0,1]
	s_nop 0
	v_pk_fma_f32 v[38:39], v[182:183], v[18:19], v[42:43] op_sel:[1,0,0]
	s_nop 0
	v_pk_fma_f32 v[38:39], v[184:185], v[20:21], v[38:39] op_sel_hi:[0,1,1]
	v_mov_b32_e32 v40, v185
	v_pk_fma_f32 v[38:39], v[40:41], v[16:17], v[38:39] op_sel_hi:[0,1,1]
	ds_read_b128 v[232:235], v238 offset:23712
	s_waitcnt lgkmcnt(8)
	v_pk_fma_f32 v[44:45], v[22:23], v[186:187], v[46:47] op_sel_hi:[1,0,1]
	s_nop 0
	v_pk_fma_f32 v[40:41], v[186:187], v[18:19], v[44:45] op_sel:[1,0,0]
	s_nop 0
	v_pk_fma_f32 v[40:41], v[188:189], v[20:21], v[40:41] op_sel_hi:[0,1,1]
	v_mov_b32_e32 v42, v189
	v_pk_fma_f32 v[40:41], v[42:43], v[16:17], v[40:41] op_sel_hi:[0,1,1]
	ds_read_b128 v[242:245], v238 offset:31920
	s_waitcnt lgkmcnt(8)
	v_pk_fma_f32 v[46:47], v[22:23], v[198:199], v[48:49] op_sel_hi:[1,0,1]
	s_nop 0
	v_pk_fma_f32 v[42:43], v[198:199], v[18:19], v[46:47] op_sel:[1,0,0]
	ds_read_b128 v[246:249], v238 offset:40128
	v_pk_fma_f32 v[42:43], v[200:201], v[20:21], v[42:43] op_sel_hi:[0,1,1]
	v_mov_b32_e32 v44, v201
	v_pk_fma_f32 v[44:45], v[44:45], v[16:17], v[42:43] op_sel_hi:[0,1,1]
	s_waitcnt lgkmcnt(8)
	v_pk_fma_f32 v[42:43], v[22:23], v[202:203], v[50:51] op_sel_hi:[1,0,1]
	s_nop 0
	v_pk_fma_f32 v[42:43], v[202:203], v[18:19], v[42:43] op_sel:[1,0,0]
	v_mov_b32_e32 v46, v205
	v_pk_fma_f32 v[42:43], v[204:205], v[20:21], v[42:43] op_sel_hi:[0,1,1]
	v_pk_fma_f32 v[42:43], v[46:47], v[16:17], v[42:43] op_sel_hi:[0,1,1]
	ds_read_b128 v[250:253], v238 offset:48336
	s_waitcnt lgkmcnt(8)
	v_pk_fma_f32 v[50:51], v[22:23], v[216:217], v[52:53] op_sel_hi:[1,0,1]
	s_nop 0
	v_pk_fma_f32 v[46:47], v[216:217], v[18:19], v[50:51] op_sel:[1,0,0]
	s_nop 0
	v_pk_fma_f32 v[46:47], v[218:219], v[20:21], v[46:47] op_sel_hi:[0,1,1]
	v_mov_b32_e32 v48, v219
	v_pk_fma_f32 v[46:47], v[48:49], v[16:17], v[46:47] op_sel_hi:[0,1,1]
	ds_read_b128 v[162:165], v238 offset:56544
	s_waitcnt lgkmcnt(8)
; #define LAS __attribute__((address_space(3)))
; #define WS_STEP(ctrl) v += __int_as_float(__builtin_amdgcn_update_dpp(0, __float_as_int(v), (ctrl), 0xf, 0xf, true))
; __device__ __forceinline__ float wave_sum(float v) {
;     ...
;     WS_STEP(0xB1); WS_STEP(0x4E); WS_STEP(0x124); WS_STEP(0x128);
;     ...
;     const auto r16 = __builtin_amdgcn_permlane16_swap(__float_as_uint(v), __float_as_uint(v), false, false);
;     v = __uint_as_float(r16[0]) + __uint_as_float(r16[1]);
;     const auto rr = __builtin_amdgcn_permlane32_swap(__float_as_uint(v), __float_as_uint(v), false, false);
;     return __uint_as_float(rr[0]) + __uint_as_float(rr[1]);
; }
; __global__ void __launch_bounds__(NTHREADS, 2) hybrid_fwd(Args a) {
;     ...
;                     for (int j = 0; j < 8; ++j) {
; #pragma unroll
;                         for (int e = 0; e < 16; ++e) { const f32x4 w = *(const LAS f32x4*)(rwT + e * 2052 + j * 256 + lane * 4);
;                             acc2[e] += y2[j][0] * (f32x2){w[0], w[0]}; acc2[e] += y2[j][1] * (f32x2){w[1], w[1]};
;                             acc2[e] += y2[j][2] * (f32x2){w[2], w[2]}; acc2[e] += y2[j][3] * (f32x2){w[3], w[3]}; }
;                         __builtin_amdgcn_sched_barrier(0);
;                     }
;                     float acca[16], accb[16];
; #pragma unroll
;                     for (int e = 0; e < 16; ++e) { acca[e] = acc2[e][0]; accb[e] = acc2[e][1]; }
	v_pk_fma_f32 v[52:53], v[22:23], v[158:159], v[54:55] op_sel_hi:[1,0,1]
	s_nop 0
	v_pk_fma_f32 v[48:49], v[158:159], v[18:19], v[52:53] op_sel:[1,0,0]
	s_nop 0
	v_pk_fma_f32 v[48:49], v[160:161], v[20:21], v[48:49] op_sel_hi:[0,1,1]
	v_mov_b32_e32 v50, v161
	v_pk_fma_f32 v[48:49], v[50:51], v[16:17], v[48:49] op_sel_hi:[0,1,1]
	ds_read_b128 v[166:169], v238 offset:64752
	s_waitcnt lgkmcnt(8)
	v_pk_fma_f32 v[54:55], v[22:23], v[220:221], v[56:57] op_sel_hi:[1,0,1]
	s_nop 0
	v_pk_fma_f32 v[50:51], v[220:221], v[18:19], v[54:55] op_sel:[1,0,0]
	s_nop 0
	v_pk_fma_f32 v[50:51], v[222:223], v[20:21], v[50:51] op_sel_hi:[0,1,1]
	v_mov_b32_e32 v52, v223
	v_pk_fma_f32 v[50:51], v[52:53], v[16:17], v[50:51] op_sel_hi:[0,1,1]
	s_waitcnt lgkmcnt(7)
	v_pk_fma_f32 v[56:57], v[22:23], v[224:225], v[58:59] op_sel_hi:[1,0,1]
	s_nop 0
	v_pk_fma_f32 v[52:53], v[224:225], v[18:19], v[56:57] op_sel:[1,0,0]
	s_nop 0
	v_pk_fma_f32 v[52:53], v[226:227], v[20:21], v[52:53] op_sel_hi:[0,1,1]
	v_mov_b32_e32 v54, v227
	v_pk_fma_f32 v[52:53], v[54:55], v[16:17], v[52:53] op_sel_hi:[0,1,1]
	s_waitcnt lgkmcnt(6)
	v_pk_fma_f32 v[58:59], v[22:23], v[228:229], v[60:61] op_sel_hi:[1,0,1]
	s_nop 0
	v_pk_fma_f32 v[54:55], v[228:229], v[18:19], v[58:59] op_sel:[1,0,0]
	s_nop 0
	v_pk_fma_f32 v[54:55], v[230:231], v[20:21], v[54:55] op_sel_hi:[0,1,1]
	v_mov_b32_e32 v56, v231
	v_pk_fma_f32 v[54:55], v[56:57], v[16:17], v[54:55] op_sel_hi:[0,1,1]
	s_waitcnt lgkmcnt(5)
	v_pk_fma_f32 v[60:61], v[22:23], v[232:233], v[62:63] op_sel_hi:[1,0,1]
	s_nop 0
	v_pk_fma_f32 v[56:57], v[232:233], v[18:19], v[60:61] op_sel:[1,0,0]
	s_nop 0
	v_pk_fma_f32 v[56:57], v[234:235], v[20:21], v[56:57] op_sel_hi:[0,1,1]
	v_mov_b32_e32 v58, v235
	v_pk_fma_f32 v[56:57], v[58:59], v[16:17], v[56:57] op_sel_hi:[0,1,1]
	s_waitcnt lgkmcnt(4)
	v_pk_fma_f32 v[62:63], v[22:23], v[242:243], v[64:65] op_sel_hi:[1,0,1]
	s_nop 0
	v_pk_fma_f32 v[58:59], v[242:243], v[18:19], v[62:63] op_sel:[1,0,0]
	s_nop 0
	v_pk_fma_f32 v[58:59], v[244:245], v[20:21], v[58:59] op_sel_hi:[0,1,1]
	v_mov_b32_e32 v60, v245
	v_pk_fma_f32 v[58:59], v[60:61], v[16:17], v[58:59] op_sel_hi:[0,1,1]
	s_waitcnt lgkmcnt(3)
	v_pk_fma_f32 v[64:65], v[22:23], v[246:247], v[66:67] op_sel_hi:[1,0,1]
	s_nop 0
	v_pk_fma_f32 v[60:61], v[246:247], v[18:19], v[64:65] op_sel:[1,0,0]
	s_nop 0
	v_pk_fma_f32 v[60:61], v[248:249], v[20:21], v[60:61] op_sel_hi:[0,1,1]
	v_mov_b32_e32 v62, v249
	v_pk_fma_f32 v[60:61], v[62:63], v[16:17], v[60:61] op_sel_hi:[0,1,1]
	s_waitcnt lgkmcnt(2)
	v_pk_fma_f32 v[66:67], v[22:23], v[250:251], v[68:69] op_sel_hi:[1,0,1]
	s_nop 0
	v_pk_fma_f32 v[62:63], v[250:251], v[18:19], v[66:67] op_sel:[1,0,0]
	s_nop 0
	v_pk_fma_f32 v[62:63], v[252:253], v[20:21], v[62:63] op_sel_hi:[0,1,1]
	v_mov_b32_e32 v64, v253
	v_pk_fma_f32 v[62:63], v[64:65], v[16:17], v[62:63] op_sel_hi:[0,1,1]
	s_waitcnt lgkmcnt(1)
	v_pk_fma_f32 v[68:69], v[22:23], v[162:163], v[70:71] op_sel_hi:[1,0,1]
	s_nop 0
	v_pk_fma_f32 v[64:65], v[162:163], v[18:19], v[68:69] op_sel:[1,0,0]
	s_nop 0
	v_pk_fma_f32 v[64:65], v[164:165], v[20:21], v[64:65] op_sel_hi:[0,1,1]
	v_mov_b32_e32 v66, v165
	v_pk_fma_f32 v[64:65], v[66:67], v[16:17], v[64:65] op_sel_hi:[0,1,1]
	s_waitcnt lgkmcnt(0)
	v_pk_fma_f32 v[22:23], v[22:23], v[166:167], v[72:73] op_sel_hi:[1,0,1]
	s_nop 0
	v_pk_fma_f32 v[18:19], v[166:167], v[18:19], v[22:23] op_sel:[1,0,0]
	s_nop 0
	v_pk_fma_f32 v[18:19], v[168:169], v[20:21], v[18:19] op_sel_hi:[0,1,1]
	v_mov_b32_e32 v20, v169
	v_pk_fma_f32 v[16:17], v[20:21], v[16:17], v[18:19] op_sel_hi:[0,1,1]
	v_add_f32_dpp v18, v36, v36 quad_perm:[1,0,3,2] row_mask:0xf bank_mask:0xf bound_ctrl:1
	s_nop 0
	v_add_f32_dpp v16, v16, v16 quad_perm:[1,0,3,2] row_mask:0xf bank_mask:0xf bound_ctrl:1
	v_add_f32_dpp v36, v62, v62 quad_perm:[1,0,3,2] row_mask:0xf bank_mask:0xf bound_ctrl:1
	v_add_f32_dpp v18, v18, v18 quad_perm:[2,3,0,1] row_mask:0xf bank_mask:0xf bound_ctrl:1
	v_add_f32_dpp v16, v16, v16 quad_perm:[2,3,0,1] row_mask:0xf bank_mask:0xf bound_ctrl:1
	v_add_f32_dpp v36, v36, v36 quad_perm:[2,3,0,1] row_mask:0xf bank_mask:0xf bound_ctrl:1
	v_add_f32_dpp v18, v18, v18 row_ror:4 row_mask:0xf bank_mask:0xf bound_ctrl:1
	v_add_f32_dpp v16, v16, v16 row_ror:4 row_mask:0xf bank_mask:0xf bound_ctrl:1
	v_add_f32_dpp v36, v36, v36 row_ror:4 row_mask:0xf bank_mask:0xf bound_ctrl:1
	v_add_f32_dpp v18, v18, v18 row_ror:8 row_mask:0xf bank_mask:0xf bound_ctrl:1
	v_mov_b32_e32 v19, v18
	s_nop 1
	v_permlane16_swap_b32_e32 v18, v19
	v_add_f32_e32 v18, v18, v19
	v_mov_b32_e32 v19, v18
	s_nop 1
	v_permlane32_swap_b32_e32 v18, v19
	v_add_f32_e32 v18, v18, v19
	s_nop 0
	v_add_f32_dpp v19, v38, v38 quad_perm:[1,0,3,2] row_mask:0xf bank_mask:0xf bound_ctrl:1
	v_mul_f32_e32 v18, 0xbfb8aa3b, v18
	v_exp_f32_e32 v18, v18
	v_add_f32_dpp v19, v19, v19 quad_perm:[2,3,0,1] row_mask:0xf bank_mask:0xf bound_ctrl:1
	v_add_f32_dpp v16, v16, v16 row_ror:8 row_mask:0xf bank_mask:0xf bound_ctrl:1
	v_add_f32_dpp v36, v36, v36 row_ror:8 row_mask:0xf bank_mask:0xf bound_ctrl:1
	v_add_f32_dpp v19, v19, v19 row_ror:4 row_mask:0xf bank_mask:0xf bound_ctrl:1
	v_add_f32_e32 v18, 1.0, v18
	v_rcp_f32_e32 v18, v18
	v_add_f32_dpp v19, v19, v19 row_ror:8 row_mask:0xf bank_mask:0xf bound_ctrl:1
	v_mov_b32_e32 v20, v19
	s_nop 1
	v_permlane16_swap_b32_e32 v19, v20
	v_add_f32_e32 v19, v19, v20
	v_mov_b32_e32 v20, v19
	s_nop 1
	v_permlane32_swap_b32_e32 v19, v20
	v_add_f32_e32 v19, v19, v20
	s_nop 0
	v_add_f32_dpp v20, v40, v40 quad_perm:[1,0,3,2] row_mask:0xf bank_mask:0xf bound_ctrl:1
	v_mul_f32_e32 v19, 0xbfb8aa3b, v19
	v_exp_f32_e32 v19, v19
	v_add_f32_dpp v20, v20, v20 quad_perm:[2,3,0,1] row_mask:0xf bank_mask:0xf bound_ctrl:1
; #define WS_STEP(ctrl) v += __int_as_float(__builtin_amdgcn_update_dpp(0, __float_as_int(v), (ctrl), 0xf, 0xf, true))
; __device__ __forceinline__ float wave_sum(float v) {
;     ...
;     WS_STEP(0xB1); WS_STEP(0x4E); WS_STEP(0x124); WS_STEP(0x128);
;     ...
;     const auto r16 = __builtin_amdgcn_permlane16_swap(__float_as_uint(v), __float_as_uint(v), false, false);
;     v = __uint_as_float(r16[0]) + __uint_as_float(r16[1]);
;     const auto rr = __builtin_amdgcn_permlane32_swap(__float_as_uint(v), __float_as_uint(v), false, false);
;     return __uint_as_float(rr[0]) + __uint_as_float(rr[1]);
; }
	v_add_f32_dpp v40, v64, v64 quad_perm:[1,0,3,2] row_mask:0xf bank_mask:0xf bound_ctrl:1
	v_mov_b32_e32 v38, v36
	v_add_f32_dpp v20, v20, v20 row_ror:4 row_mask:0xf bank_mask:0xf bound_ctrl:1
	v_add_f32_e32 v19, 1.0, v19
	v_rcp_f32_e32 v19, v19
	v_add_f32_dpp v20, v20, v20 row_ror:8 row_mask:0xf bank_mask:0xf bound_ctrl:1
	v_mov_b32_e32 v21, v20
	s_nop 1
	v_permlane16_swap_b32_e32 v20, v21
	v_add_f32_e32 v20, v20, v21
	v_mov_b32_e32 v21, v20
	s_nop 1
	v_permlane32_swap_b32_e32 v20, v21
	v_add_f32_e32 v20, v20, v21
	s_nop 0
	v_add_f32_dpp v21, v44, v44 quad_perm:[1,0,3,2] row_mask:0xf bank_mask:0xf bound_ctrl:1
	v_mul_f32_e32 v20, 0xbfb8aa3b, v20
	v_exp_f32_e32 v20, v20
	v_add_f32_dpp v21, v21, v21 quad_perm:[2,3,0,1] row_mask:0xf bank_mask:0xf bound_ctrl:1
	v_mov_b32_e32 v44, v16
	s_nop 1
	v_permlane16_swap_b32_e32 v16, v44
	v_add_f32_dpp v21, v21, v21 row_ror:4 row_mask:0xf bank_mask:0xf bound_ctrl:1
	v_add_f32_e32 v20, 1.0, v20
	v_rcp_f32_e32 v70, v20
	v_add_f32_dpp v21, v21, v21 row_ror:8 row_mask:0xf bank_mask:0xf bound_ctrl:1
	v_mov_b32_e32 v22, v21
	s_nop 1
	v_permlane16_swap_b32_e32 v21, v22
	v_add_f32_e32 v21, v21, v22
	v_mov_b32_e32 v22, v21
	s_nop 1
	v_permlane32_swap_b32_e32 v21, v22
	v_add_f32_e32 v21, v21, v22
	s_nop 0
	v_add_f32_dpp v22, v42, v42 quad_perm:[1,0,3,2] row_mask:0xf bank_mask:0xf bound_ctrl:1
	v_mul_f32_e32 v21, 0xbfb8aa3b, v21
	v_exp_f32_e32 v21, v21
	v_add_f32_dpp v22, v22, v22 quad_perm:[2,3,0,1] row_mask:0xf bank_mask:0xf bound_ctrl:1
	v_add_f32_e32 v79, v14, v70
	v_add_f32_e32 v44, v16, v44
	v_add_f32_dpp v22, v22, v22 row_ror:4 row_mask:0xf bank_mask:0xf bound_ctrl:1
	v_add_f32_e32 v20, 1.0, v21
	v_rcp_f32_e32 v72, v20
	v_add_f32_dpp v22, v22, v22 row_ror:8 row_mask:0xf bank_mask:0xf bound_ctrl:1
	v_mov_b32_e32 v23, v22
	s_nop 1
	v_permlane16_swap_b32_e32 v22, v23
	v_add_f32_e32 v69, v22, v23
	s_nop 0
	v_add_f32_dpp v22, v46, v46 quad_perm:[1,0,3,2] row_mask:0xf bank_mask:0xf bound_ctrl:1
	v_pk_add_f32 v[20:21], v[12:13], v[18:19]
	v_add_f32_e32 v80, v15, v72
	v_add_f32_dpp v22, v22, v22 quad_perm:[2,3,0,1] row_mask:0xf bank_mask:0xf bound_ctrl:1
	v_cmp_gt_f32_e32 vcc, v21, v20
	v_add_f32_dpp v40, v40, v40 quad_perm:[2,3,0,1] row_mask:0xf bank_mask:0xf bound_ctrl:1
	v_add_f32_dpp v22, v22, v22 row_ror:4 row_mask:0xf bank_mask:0xf bound_ctrl:1
	v_cndmask_b32_e32 v16, v20, v21, vcc
	v_cmp_gt_f32_e64 s[6:7], v79, v16
	v_add_f32_dpp v22, v22, v22 row_ror:8 row_mask:0xf bank_mask:0xf bound_ctrl:1
	v_mov_b32_e32 v23, v22
	s_nop 1
	v_permlane16_swap_b32_e32 v22, v23
	v_add_f32_e32 v73, v22, v23
	s_nop 0
	v_add_f32_dpp v22, v48, v48 quad_perm:[1,0,3,2] row_mask:0xf bank_mask:0xf bound_ctrl:1
	v_cndmask_b32_e64 v48, 0, 1, vcc
	v_cndmask_b32_e64 v16, v16, v79, s[6:7]
	v_add_f32_dpp v22, v22, v22 quad_perm:[2,3,0,1] row_mask:0xf bank_mask:0xf bound_ctrl:1
	v_cndmask_b32_e64 v48, v48, 2, s[6:7]
	v_cmp_ngt_f32_e64 s[8:9], v80, v16
	v_add_f32_dpp v22, v22, v22 row_ror:4 row_mask:0xf bank_mask:0xf bound_ctrl:1
	v_add_f32_dpp v40, v40, v40 row_ror:4 row_mask:0xf bank_mask:0xf bound_ctrl:1
	v_permlane16_swap_b32_e32 v36, v38
	v_add_f32_dpp v22, v22, v22 row_ror:8 row_mask:0xf bank_mask:0xf bound_ctrl:1
	v_mov_b32_e32 v23, v22
	s_nop 1
	v_permlane16_swap_b32_e32 v22, v23
	v_add_f32_e32 v75, v22, v23
	s_nop 0
	v_add_f32_dpp v22, v50, v50 quad_perm:[1,0,3,2] row_mask:0xf bank_mask:0xf bound_ctrl:1
	v_add_f32_dpp v40, v40, v40 row_ror:8 row_mask:0xf bank_mask:0xf bound_ctrl:1
	v_mov_b32_e32 v42, v40
	v_add_f32_dpp v22, v22, v22 quad_perm:[2,3,0,1] row_mask:0xf bank_mask:0xf bound_ctrl:1
	s_nop 0
	v_permlane16_swap_b32_e32 v40, v42
	v_add_f32_dpp v22, v22, v22 row_ror:4 row_mask:0xf bank_mask:0xf bound_ctrl:1
	v_add_f32_e32 v36, v36, v38
	v_add_f32_e32 v40, v40, v42
	v_add_f32_dpp v22, v22, v22 row_ror:8 row_mask:0xf bank_mask:0xf bound_ctrl:1
	v_mov_b32_e32 v23, v22
	s_nop 1
	v_permlane16_swap_b32_e32 v22, v23
	v_add_f32_e32 v77, v22, v23
	s_nop 0
	v_add_f32_dpp v22, v52, v52 quad_perm:[1,0,3,2] row_mask:0xf bank_mask:0xf bound_ctrl:1
	v_cndmask_b32_e64 v62, v80, v16, s[8:9]
	v_mov_b32_e32 v71, v69
	v_add_f32_dpp v22, v22, v22 quad_perm:[2,3,0,1] row_mask:0xf bank_mask:0xf bound_ctrl:1
	v_mov_b32_e32 v74, v73
	v_mov_b32_e32 v76, v75
	v_add_f32_dpp v22, v22, v22 row_ror:4 row_mask:0xf bank_mask:0xf bound_ctrl:1
	v_mov_b32_e32 v78, v77
	v_mov_b32_e32 v38, v36
	v_add_f32_dpp v22, v22, v22 row_ror:8 row_mask:0xf bank_mask:0xf bound_ctrl:1
	v_mov_b32_e32 v23, v22
	s_nop 1
	v_permlane16_swap_b32_e32 v22, v23
	v_add_f32_e32 v50, v22, v23
	s_nop 0
	v_add_f32_dpp v22, v54, v54 quad_perm:[1,0,3,2] row_mask:0xf bank_mask:0xf bound_ctrl:1
	v_mov_b32_e32 v52, v50
	v_mov_b32_e32 v42, v40
	v_add_f32_dpp v22, v22, v22 quad_perm:[2,3,0,1] row_mask:0xf bank_mask:0xf bound_ctrl:1
	v_mov_b32_e32 v46, v44
	v_permlane32_swap_b32_e32 v69, v71
	v_add_f32_dpp v22, v22, v22 row_ror:4 row_mask:0xf bank_mask:0xf bound_ctrl:1
	v_permlane32_swap_b32_e32 v73, v74
	s_nop 0
	v_add_f32_dpp v22, v22, v22 row_ror:8 row_mask:0xf bank_mask:0xf bound_ctrl:1
	v_mov_b32_e32 v23, v22
	s_nop 1
	v_permlane16_swap_b32_e32 v22, v23
	v_add_f32_e32 v54, v22, v23
	s_nop 0
	v_add_f32_dpp v22, v56, v56 quad_perm:[1,0,3,2] row_mask:0xf bank_mask:0xf bound_ctrl:1
	v_mov_b32_e32 v66, v54
	v_permlane32_swap_b32_e32 v75, v76
	v_add_f32_dpp v22, v22, v22 quad_perm:[2,3,0,1] row_mask:0xf bank_mask:0xf bound_ctrl:1
	v_permlane32_swap_b32_e32 v77, v78
	s_nop 0
	v_add_f32_dpp v22, v22, v22 row_ror:4 row_mask:0xf bank_mask:0xf bound_ctrl:1
	v_permlane32_swap_b32_e32 v50, v52
	s_nop 0
	v_add_f32_dpp v22, v22, v22 row_ror:8 row_mask:0xf bank_mask:0xf bound_ctrl:1
	v_mov_b32_e32 v23, v22
	s_nop 1
	v_permlane16_swap_b32_e32 v22, v23
	v_add_f32_e32 v56, v22, v23
	s_nop 0
	v_add_f32_dpp v22, v58, v58 quad_perm:[1,0,3,2] row_mask:0xf bank_mask:0xf bound_ctrl:1
	v_mov_b32_e32 v67, v56
	v_permlane32_swap_b32_e32 v54, v66
	v_add_f32_dpp v22, v22, v22 quad_perm:[2,3,0,1] row_mask:0xf bank_mask:0xf bound_ctrl:1
	v_permlane32_swap_b32_e32 v56, v67
	s_nop 0
	v_add_f32_dpp v22, v22, v22 row_ror:4 row_mask:0xf bank_mask:0xf bound_ctrl:1
	v_permlane32_swap_b32_e32 v36, v38
	s_nop 0
	v_add_f32_dpp v22, v22, v22 row_ror:8 row_mask:0xf bank_mask:0xf bound_ctrl:1
	v_mov_b32_e32 v23, v22
	s_nop 1
	v_permlane16_swap_b32_e32 v22, v23
	v_add_f32_e32 v58, v22, v23
	s_nop 0
	v_add_f32_dpp v22, v60, v60 quad_perm:[1,0,3,2] row_mask:0xf bank_mask:0xf bound_ctrl:1
	v_cndmask_b32_e64 v60, 3, v48, s[8:9]
	v_mov_b32_e32 v48, 0xff800000
	v_cmp_eq_u32_e64 s[10:11], 0, v60
	v_cmp_nlg_f32_e64 s[12:13], v20, v48
	s_or_b64 s[10:11], s[10:11], s[12:13]
	v_cndmask_b32_e64 v20, v20, v48, s[10:11]
	v_cmp_ne_u32_e64 s[12:13], 1, v60
	v_cmp_gt_f32_e64 s[14:15], v21, v20
	s_and_b64 s[12:13], s[12:13], s[14:15]
	v_cndmask_b32_e64 v20, v20, v21, s[12:13]
	v_add_f32_dpp v22, v22, v22 quad_perm:[2,3,0,1] row_mask:0xf bank_mask:0xf bound_ctrl:1
	v_cmp_ne_u32_e64 s[14:15], 2, v60
	v_cmp_gt_f32_e64 s[16:17], v79, v20
	v_add_f32_dpp v22, v22, v22 row_ror:4 row_mask:0xf bank_mask:0xf bound_ctrl:1
	s_and_b64 s[14:15], s[14:15], s[16:17]
	v_cndmask_b32_e64 v20, v20, v79, s[14:15]
	v_add_f32_dpp v22, v22, v22 row_ror:8 row_mask:0xf bank_mask:0xf bound_ctrl:1
	v_mov_b32_e32 v23, v22
	v_cmp_gt_f32_e64 s[16:17], v80, v20
	s_nop 0
	v_permlane16_swap_b32_e32 v22, v23
	s_and_b64 s[16:17], s[8:9], s[16:17]
	v_add_f32_e32 v22, v22, v23
	v_cndmask_b32_e64 v20, v20, v80, s[16:17]
	v_mov_b32_e32 v68, v58
	v_mov_b32_e32 v23, v22
	v_add_f32_e32 v62, v62, v20
	v_permlane32_swap_b32_e32 v58, v68
	v_permlane32_swap_b32_e32 v22, v23
	v_permlane32_swap_b32_e32 v40, v42
	v_permlane32_swap_b32_e32 v44, v46
	v_mov_b32_e32 v16, 1
	v_cmp_lg_f32_e64 s[18:19], v62, v48
	v_mov_b32_e32 v21, 0
	v_mov_b32_e32 v20, 0
	s_and_saveexec_b64 s[38:39], s[18:19]
	s_cbranch_execz .LBB0_911
	v_cndmask_b32_e64 v20, v18, 0, s[10:11]
	v_cndmask_b32_e64 v16, 0, 1, s[12:13]
	v_cndmask_b32_e64 v20, v20, v19, s[12:13]
	v_cndmask_b32_e32 v18, v18, v19, vcc
	v_cndmask_b32_e64 v16, v16, 2, s[14:15]
	v_cndmask_b32_e64 v20, v20, v70, s[14:15]
	v_cndmask_b32_e64 v18, v18, v70, s[6:7]
	v_cndmask_b32_e64 v16, v16, 3, s[16:17]
	v_cndmask_b32_e64 v35, v20, v72, s[16:17]
	v_cndmask_b32_e64 v21, v72, v18, s[8:9]
	v_mov_b32_e32 v20, v60
	v_mov_b32_e32 v48, v62
